# previous (phase-6 down-weight conversion moved into phase 8) plus hand-written 3-deep conversion items in phases 2, 4 and 5
# baseline (speedup 1.0000x reference)
.LBB0_168:
	s_cmpk_gt_i32 s4, 0x3ff
	s_mov_b64 s[30:31], -1
	s_barrier
	s_mov_b32 s61, s4
	s_lshr_b32 s60, s61, 5
	s_and_b32 s61, s61, 31
	v_readlane_b32 s56, v254, 6
	v_readlane_b32 s57, v254, 7
	s_lshl_b32 s62, s60, 25
	s_and_b32 s63, s61, 1
	s_lshl_b32 s63, s63, 13
	s_add_u32 s62, s62, s63
	s_lshr_b32 s63, s61, 1
	s_lshl_b32 s63, s63, 9
	s_add_u32 s62, s62, s63
	s_add_u32 s56, s56, s62
	s_addc_u32 s57, s57, 0
	s_lshl_b32 s62, s60, 23
	s_lshl_b32 s63, s61, 18
	s_add_u32 s62, s62, s63
	s_add_u32 s62, s62, 0x40000000
	v_readlane_b32 s58, v254, 57
	v_readlane_b32 s59, v254, 58
	s_add_u32 s58, s58, s62
	s_addc_u32 s59, s59, 0
	s_mov_b32 s62, 0xc3e00000
	v_mov_b32_e32 v154, 0x43e00000
	v_lshrrev_b32_e32 v233, 5, v0
	v_and_b32_e32 v226, 31, v0
	v_lshlrev_b32_e32 v227, 4, v226
	v_lshlrev_b32_e32 v228, 18, v233
	v_add_u32_e32 v166, v228, v227
	v_add_u32_e32 v250, 0x4000, v166
	v_add_u32_e32 v251, 0x8000, v166
	v_add_u32_e32 v246, 0xc000, v166
	v_add_u32_e32 v247, 0x10000, v166
	v_add_u32_e32 v248, 0x14000, v166
	v_add_u32_e32 v249, 0x18000, v166
	v_add_u32_e32 v242, 0x1c000, v166
	v_add_u32_e32 v243, 0x20000, v166
	v_add_u32_e32 v244, 0x24000, v166
	v_add_u32_e32 v245, 0x28000, v166
	v_add_u32_e32 v238, 0x2c000, v166
	v_add_u32_e32 v239, 0x30000, v166
	v_add_u32_e32 v240, 0x34000, v166
	v_add_u32_e32 v241, 0x38000, v166
	v_add_u32_e32 v234, 0x3c000, v166
	v_lshrrev_b32_e32 v202, 4, v0
	v_and_b32_e32 v203, 15, v0
	v_lshlrev_b32_e32 v235, 11, v202
	v_lshl_add_u32 v235, v203, 4, v235
	v_add_u32_e32 v236, 0x10000, v235
	v_add_u32_e32 v237, 0x20000, v235
	v_add_u32_e32 v230, 0x30000, v235
	v_mul_u32_u24_e32 v231, 0x440, v226
	v_lshl_add_u32 v231, v233, 4, v231
	v_mul_u32_u24_e32 v232, 0x110, v202
	v_lshl_add_u32 v232, v203, 4, v232
	global_load_dwordx4 v[2:5], v166, s[56:57] nt
	global_load_dwordx4 v[6:9], v250, s[56:57] nt
	global_load_dwordx4 v[10:13], v251, s[56:57] nt
	global_load_dwordx4 v[14:17], v246, s[56:57] nt
	global_load_dwordx4 v[18:21], v247, s[56:57] nt
	global_load_dwordx4 v[22:25], v248, s[56:57] nt
	global_load_dwordx4 v[26:29], v249, s[56:57] nt
	global_load_dwordx4 v[30:33], v242, s[56:57] nt
	global_load_dwordx4 v[34:37], v243, s[56:57] nt
	global_load_dwordx4 v[38:41], v244, s[56:57] nt
	global_load_dwordx4 v[42:45], v245, s[56:57] nt
	global_load_dwordx4 v[46:49], v238, s[56:57] nt
	global_load_dwordx4 v[50:53], v239, s[56:57] nt
	global_load_dwordx4 v[54:57], v240, s[56:57] nt
	global_load_dwordx4 v[58:61], v241, s[56:57] nt
	global_load_dwordx4 v[62:65], v234, s[56:57] nt
	s_add_u32 s56, s56, 0x400000
	s_addc_u32 s57, s57, 0
	global_load_dwordx4 v[66:69], v166, s[56:57] nt
	global_load_dwordx4 v[70:73], v250, s[56:57] nt
	global_load_dwordx4 v[74:77], v251, s[56:57] nt
	global_load_dwordx4 v[78:81], v246, s[56:57] nt
	global_load_dwordx4 v[82:85], v247, s[56:57] nt
	global_load_dwordx4 v[86:89], v248, s[56:57] nt
	global_load_dwordx4 v[90:93], v249, s[56:57] nt
	global_load_dwordx4 v[94:97], v242, s[56:57] nt
	global_load_dwordx4 v[98:101], v243, s[56:57] nt
	global_load_dwordx4 v[102:105], v244, s[56:57] nt
	global_load_dwordx4 v[106:109], v245, s[56:57] nt
	global_load_dwordx4 v[110:113], v238, s[56:57] nt
	global_load_dwordx4 v[114:117], v239, s[56:57] nt
	global_load_dwordx4 v[118:121], v240, s[56:57] nt
	global_load_dwordx4 v[122:125], v241, s[56:57] nt
	global_load_dwordx4 v[126:129], v234, s[56:57] nt
	s_add_u32 s56, s56, 0x400000
	s_addc_u32 s57, s57, 0
	global_load_dwordx4 v[130:133], v166, s[56:57] nt
	global_load_dwordx4 v[134:137], v250, s[56:57] nt
	global_load_dwordx4 v[138:141], v251, s[56:57] nt
	global_load_dwordx4 v[142:145], v246, s[56:57] nt
	global_load_dwordx4 v[146:149], v247, s[56:57] nt
	global_load_dwordx4 v[150:153], v248, s[56:57] nt
	global_load_dwordx4 v[158:161], v249, s[56:57] nt
	global_load_dwordx4 v[162:165], v242, s[56:57] nt
	global_load_dwordx4 v[168:171], v243, s[56:57] nt
	global_load_dwordx4 v[174:177], v244, s[56:57] nt
	global_load_dwordx4 v[178:181], v245, s[56:57] nt
	global_load_dwordx4 v[182:185], v238, s[56:57] nt
	global_load_dwordx4 v[186:189], v239, s[56:57] nt
	global_load_dwordx4 v[190:193], v240, s[56:57] nt
	global_load_dwordx4 v[194:197], v241, s[56:57] nt
	global_load_dwordx4 v[198:201], v234, s[56:57] nt
	s_add_u32 s56, s56, 0x400000
	s_addc_u32 s57, s57, 0
	s_waitcnt vmcnt(44)
	v_mul_f32_e32 v233, 0x43800000, v2
	v_mul_f32_e32 v226, 0x43800000, v6
	v_med3_f32 v233, v233, s62, v154
	v_med3_f32 v226, v226, s62, v154
	v_mul_f32_e32 v227, 0x43800000, v10
	v_mul_f32_e32 v228, 0x43800000, v14
	v_cvt_pk_fp8_f32 v202, v233, v226
	v_med3_f32 v227, v227, s62, v154
	v_med3_f32 v228, v228, s62, v154
	v_cvt_pk_fp8_f32 v202, v227, v228 op_sel:[0,0,1]
	s_waitcnt vmcnt(40)
	v_mul_f32_e32 v233, 0x43800000, v18
	v_mul_f32_e32 v226, 0x43800000, v22
	v_med3_f32 v233, v233, s62, v154
	v_med3_f32 v226, v226, s62, v154
	v_mul_f32_e32 v227, 0x43800000, v26
	v_mul_f32_e32 v228, 0x43800000, v30
	v_cvt_pk_fp8_f32 v203, v233, v226
	v_med3_f32 v227, v227, s62, v154
	v_med3_f32 v228, v228, s62, v154
	v_cvt_pk_fp8_f32 v203, v227, v228 op_sel:[0,0,1]
	s_waitcnt vmcnt(36)
	v_mul_f32_e32 v233, 0x43800000, v34
	v_mul_f32_e32 v226, 0x43800000, v38
	v_med3_f32 v233, v233, s62, v154
	v_med3_f32 v226, v226, s62, v154
	v_mul_f32_e32 v227, 0x43800000, v42
	v_mul_f32_e32 v228, 0x43800000, v46
	v_cvt_pk_fp8_f32 v204, v233, v226
	v_med3_f32 v227, v227, s62, v154
	v_med3_f32 v228, v228, s62, v154
	v_cvt_pk_fp8_f32 v204, v227, v228 op_sel:[0,0,1]
	s_waitcnt vmcnt(32)
	v_mul_f32_e32 v233, 0x43800000, v50
	v_mul_f32_e32 v226, 0x43800000, v54
	v_med3_f32 v233, v233, s62, v154
	v_med3_f32 v226, v226, s62, v154
	v_mul_f32_e32 v227, 0x43800000, v58
	v_mul_f32_e32 v228, 0x43800000, v62
	v_cvt_pk_fp8_f32 v205, v233, v226
	v_med3_f32 v227, v227, s62, v154
	v_med3_f32 v228, v228, s62, v154
	v_cvt_pk_fp8_f32 v205, v227, v228 op_sel:[0,0,1]
	s_nop 1
	ds_write_b128 v231, v[202:205] offset:0
	v_mul_f32_e32 v233, 0x43800000, v3
	v_mul_f32_e32 v226, 0x43800000, v7
	v_med3_f32 v233, v233, s62, v154
	v_med3_f32 v226, v226, s62, v154
	v_mul_f32_e32 v227, 0x43800000, v11
	v_mul_f32_e32 v228, 0x43800000, v15
	v_cvt_pk_fp8_f32 v206, v233, v226
	v_med3_f32 v227, v227, s62, v154
	v_med3_f32 v228, v228, s62, v154
	v_cvt_pk_fp8_f32 v206, v227, v228 op_sel:[0,0,1]
	v_mul_f32_e32 v233, 0x43800000, v19
	v_mul_f32_e32 v226, 0x43800000, v23
	v_med3_f32 v233, v233, s62, v154
	v_med3_f32 v226, v226, s62, v154
	v_mul_f32_e32 v227, 0x43800000, v27
	v_mul_f32_e32 v228, 0x43800000, v31
	v_cvt_pk_fp8_f32 v207, v233, v226
	v_med3_f32 v227, v227, s62, v154
	v_med3_f32 v228, v228, s62, v154
	v_cvt_pk_fp8_f32 v207, v227, v228 op_sel:[0,0,1]
	v_mul_f32_e32 v233, 0x43800000, v35
	v_mul_f32_e32 v226, 0x43800000, v39
	v_med3_f32 v233, v233, s62, v154
	v_med3_f32 v226, v226, s62, v154
	v_mul_f32_e32 v227, 0x43800000, v43
	v_mul_f32_e32 v228, 0x43800000, v47
	v_cvt_pk_fp8_f32 v208, v233, v226
	v_med3_f32 v227, v227, s62, v154
	v_med3_f32 v228, v228, s62, v154
	v_cvt_pk_fp8_f32 v208, v227, v228 op_sel:[0,0,1]
	v_mul_f32_e32 v233, 0x43800000, v51
	v_mul_f32_e32 v226, 0x43800000, v55
	v_med3_f32 v233, v233, s62, v154
	v_med3_f32 v226, v226, s62, v154
	v_mul_f32_e32 v227, 0x43800000, v59
	v_mul_f32_e32 v228, 0x43800000, v63
	v_cvt_pk_fp8_f32 v209, v233, v226
	v_med3_f32 v227, v227, s62, v154
	v_med3_f32 v228, v228, s62, v154
	v_cvt_pk_fp8_f32 v209, v227, v228 op_sel:[0,0,1]
	s_nop 1
	ds_write_b128 v231, v[206:209] offset:272
	v_mul_f32_e32 v233, 0x43800000, v4
	v_mul_f32_e32 v226, 0x43800000, v8
	v_med3_f32 v233, v233, s62, v154
	v_med3_f32 v226, v226, s62, v154
	v_mul_f32_e32 v227, 0x43800000, v12
	v_mul_f32_e32 v228, 0x43800000, v16
	v_cvt_pk_fp8_f32 v210, v233, v226
	v_med3_f32 v227, v227, s62, v154
	v_med3_f32 v228, v228, s62, v154
	v_cvt_pk_fp8_f32 v210, v227, v228 op_sel:[0,0,1]
	v_mul_f32_e32 v233, 0x43800000, v20
	v_mul_f32_e32 v226, 0x43800000, v24
	v_med3_f32 v233, v233, s62, v154
	v_med3_f32 v226, v226, s62, v154
	v_mul_f32_e32 v227, 0x43800000, v28
	v_mul_f32_e32 v228, 0x43800000, v32
	v_cvt_pk_fp8_f32 v211, v233, v226
	v_med3_f32 v227, v227, s62, v154
	v_med3_f32 v228, v228, s62, v154
	v_cvt_pk_fp8_f32 v211, v227, v228 op_sel:[0,0,1]
	v_mul_f32_e32 v233, 0x43800000, v36
	v_mul_f32_e32 v226, 0x43800000, v40
	v_med3_f32 v233, v233, s62, v154
	v_med3_f32 v226, v226, s62, v154
	v_mul_f32_e32 v227, 0x43800000, v44
	v_mul_f32_e32 v228, 0x43800000, v48
	v_cvt_pk_fp8_f32 v212, v233, v226
	v_med3_f32 v227, v227, s62, v154
	v_med3_f32 v228, v228, s62, v154
	v_cvt_pk_fp8_f32 v212, v227, v228 op_sel:[0,0,1]
	v_mul_f32_e32 v233, 0x43800000, v52
	v_mul_f32_e32 v226, 0x43800000, v56
	v_med3_f32 v233, v233, s62, v154
	v_med3_f32 v226, v226, s62, v154
	v_mul_f32_e32 v227, 0x43800000, v60
	v_mul_f32_e32 v228, 0x43800000, v64
	v_cvt_pk_fp8_f32 v213, v233, v226
	v_med3_f32 v227, v227, s62, v154
	v_med3_f32 v228, v228, s62, v154
	v_cvt_pk_fp8_f32 v213, v227, v228 op_sel:[0,0,1]
	s_nop 1
	ds_write_b128 v231, v[210:213] offset:544
	v_mul_f32_e32 v233, 0x43800000, v5
	v_mul_f32_e32 v226, 0x43800000, v9
	v_med3_f32 v233, v233, s62, v154
	v_med3_f32 v226, v226, s62, v154
	v_mul_f32_e32 v227, 0x43800000, v13
	v_mul_f32_e32 v228, 0x43800000, v17
	v_cvt_pk_fp8_f32 v214, v233, v226
	v_med3_f32 v227, v227, s62, v154
	v_med3_f32 v228, v228, s62, v154
	v_cvt_pk_fp8_f32 v214, v227, v228 op_sel:[0,0,1]
	v_mul_f32_e32 v233, 0x43800000, v21
	v_mul_f32_e32 v226, 0x43800000, v25
	v_med3_f32 v233, v233, s62, v154
	v_med3_f32 v226, v226, s62, v154
	v_mul_f32_e32 v227, 0x43800000, v29
	v_mul_f32_e32 v228, 0x43800000, v33
	v_cvt_pk_fp8_f32 v215, v233, v226
	v_med3_f32 v227, v227, s62, v154
	v_med3_f32 v228, v228, s62, v154
	v_cvt_pk_fp8_f32 v215, v227, v228 op_sel:[0,0,1]
	v_mul_f32_e32 v233, 0x43800000, v37
	v_mul_f32_e32 v226, 0x43800000, v41
	v_med3_f32 v233, v233, s62, v154
	v_med3_f32 v226, v226, s62, v154
	v_mul_f32_e32 v227, 0x43800000, v45
	v_mul_f32_e32 v228, 0x43800000, v49
	v_cvt_pk_fp8_f32 v216, v233, v226
	v_med3_f32 v227, v227, s62, v154
	v_med3_f32 v228, v228, s62, v154
	v_cvt_pk_fp8_f32 v216, v227, v228 op_sel:[0,0,1]
	v_mul_f32_e32 v233, 0x43800000, v53
	v_mul_f32_e32 v226, 0x43800000, v57
	v_med3_f32 v233, v233, s62, v154
	v_med3_f32 v226, v226, s62, v154
	v_mul_f32_e32 v227, 0x43800000, v61
	v_mul_f32_e32 v228, 0x43800000, v65
	v_cvt_pk_fp8_f32 v217, v233, v226
	v_med3_f32 v227, v227, s62, v154
	v_med3_f32 v228, v228, s62, v154
	v_cvt_pk_fp8_f32 v217, v227, v228 op_sel:[0,0,1]
	s_nop 1
	ds_write_b128 v231, v[214:217] offset:816
	s_waitcnt lgkmcnt(0)
	s_barrier
	global_load_dwordx4 v[2:5], v166, s[56:57] nt
	global_load_dwordx4 v[6:9], v250, s[56:57] nt
	global_load_dwordx4 v[10:13], v251, s[56:57] nt
	global_load_dwordx4 v[14:17], v246, s[56:57] nt
	global_load_dwordx4 v[18:21], v247, s[56:57] nt
	global_load_dwordx4 v[22:25], v248, s[56:57] nt
	global_load_dwordx4 v[26:29], v249, s[56:57] nt
	global_load_dwordx4 v[30:33], v242, s[56:57] nt
	global_load_dwordx4 v[34:37], v243, s[56:57] nt
	global_load_dwordx4 v[38:41], v244, s[56:57] nt
	global_load_dwordx4 v[42:45], v245, s[56:57] nt
	global_load_dwordx4 v[46:49], v238, s[56:57] nt
	global_load_dwordx4 v[50:53], v239, s[56:57] nt
	global_load_dwordx4 v[54:57], v240, s[56:57] nt
	global_load_dwordx4 v[58:61], v241, s[56:57] nt
	global_load_dwordx4 v[62:65], v234, s[56:57] nt
	s_add_u32 s56, s56, 0x400000
	s_addc_u32 s57, s57, 0
	ds_read_b128 v[202:205], v232 offset:0
	ds_read_b128 v[206:209], v232 offset:8704
	ds_read_b128 v[210:213], v232 offset:17408
	ds_read_b128 v[214:217], v232 offset:26112
	s_waitcnt lgkmcnt(3)
	global_store_dwordx4 v235, v[202:205], s[58:59] nt
	s_waitcnt lgkmcnt(2)
	global_store_dwordx4 v236, v[206:209], s[58:59] nt
	s_waitcnt lgkmcnt(1)
	global_store_dwordx4 v237, v[210:213], s[58:59] nt
	s_waitcnt lgkmcnt(0)
	global_store_dwordx4 v230, v[214:217], s[58:59] nt
	s_add_u32 s58, s58, 0x100
	s_addc_u32 s59, s59, 0
	s_waitcnt vmcnt(48)
	v_mul_f32_e32 v233, 0x43800000, v66
	v_mul_f32_e32 v226, 0x43800000, v70
	v_med3_f32 v233, v233, s62, v154
	v_med3_f32 v226, v226, s62, v154
	v_mul_f32_e32 v227, 0x43800000, v74
	v_mul_f32_e32 v228, 0x43800000, v78
	v_cvt_pk_fp8_f32 v202, v233, v226
	v_med3_f32 v227, v227, s62, v154
	v_med3_f32 v228, v228, s62, v154
	v_cvt_pk_fp8_f32 v202, v227, v228 op_sel:[0,0,1]
	s_waitcnt vmcnt(44)
	v_mul_f32_e32 v233, 0x43800000, v82
	v_mul_f32_e32 v226, 0x43800000, v86
	v_med3_f32 v233, v233, s62, v154
	v_med3_f32 v226, v226, s62, v154
	v_mul_f32_e32 v227, 0x43800000, v90
	v_mul_f32_e32 v228, 0x43800000, v94
	v_cvt_pk_fp8_f32 v203, v233, v226
	v_med3_f32 v227, v227, s62, v154
	v_med3_f32 v228, v228, s62, v154
	v_cvt_pk_fp8_f32 v203, v227, v228 op_sel:[0,0,1]
	s_waitcnt vmcnt(40)
	v_mul_f32_e32 v233, 0x43800000, v98
	v_mul_f32_e32 v226, 0x43800000, v102
	v_med3_f32 v233, v233, s62, v154
	v_med3_f32 v226, v226, s62, v154
	v_mul_f32_e32 v227, 0x43800000, v106
	v_mul_f32_e32 v228, 0x43800000, v110
	v_cvt_pk_fp8_f32 v204, v233, v226
	v_med3_f32 v227, v227, s62, v154
	v_med3_f32 v228, v228, s62, v154
	v_cvt_pk_fp8_f32 v204, v227, v228 op_sel:[0,0,1]
	s_waitcnt vmcnt(36)
	v_mul_f32_e32 v233, 0x43800000, v114
	v_mul_f32_e32 v226, 0x43800000, v118
	v_med3_f32 v233, v233, s62, v154
	v_med3_f32 v226, v226, s62, v154
	v_mul_f32_e32 v227, 0x43800000, v122
	v_mul_f32_e32 v228, 0x43800000, v126
	v_cvt_pk_fp8_f32 v205, v233, v226
	v_med3_f32 v227, v227, s62, v154
	v_med3_f32 v228, v228, s62, v154
	v_cvt_pk_fp8_f32 v205, v227, v228 op_sel:[0,0,1]
	s_nop 1
	ds_write_b128 v231, v[202:205] offset:34816
	v_mul_f32_e32 v233, 0x43800000, v67
	v_mul_f32_e32 v226, 0x43800000, v71
	v_med3_f32 v233, v233, s62, v154
	v_med3_f32 v226, v226, s62, v154
	v_mul_f32_e32 v227, 0x43800000, v75
	v_mul_f32_e32 v228, 0x43800000, v79
	v_cvt_pk_fp8_f32 v206, v233, v226
	v_med3_f32 v227, v227, s62, v154
	v_med3_f32 v228, v228, s62, v154
	v_cvt_pk_fp8_f32 v206, v227, v228 op_sel:[0,0,1]
	v_mul_f32_e32 v233, 0x43800000, v83
	v_mul_f32_e32 v226, 0x43800000, v87
	v_med3_f32 v233, v233, s62, v154
	v_med3_f32 v226, v226, s62, v154
	v_mul_f32_e32 v227, 0x43800000, v91
	v_mul_f32_e32 v228, 0x43800000, v95
	v_cvt_pk_fp8_f32 v207, v233, v226
	v_med3_f32 v227, v227, s62, v154
	v_med3_f32 v228, v228, s62, v154
	v_cvt_pk_fp8_f32 v207, v227, v228 op_sel:[0,0,1]
	v_mul_f32_e32 v233, 0x43800000, v99
	v_mul_f32_e32 v226, 0x43800000, v103
	v_med3_f32 v233, v233, s62, v154
	v_med3_f32 v226, v226, s62, v154
	v_mul_f32_e32 v227, 0x43800000, v107
	v_mul_f32_e32 v228, 0x43800000, v111
	v_cvt_pk_fp8_f32 v208, v233, v226
	v_med3_f32 v227, v227, s62, v154
	v_med3_f32 v228, v228, s62, v154
	v_cvt_pk_fp8_f32 v208, v227, v228 op_sel:[0,0,1]
	v_mul_f32_e32 v233, 0x43800000, v115
	v_mul_f32_e32 v226, 0x43800000, v119
	v_med3_f32 v233, v233, s62, v154
	v_med3_f32 v226, v226, s62, v154
	v_mul_f32_e32 v227, 0x43800000, v123
	v_mul_f32_e32 v228, 0x43800000, v127
	v_cvt_pk_fp8_f32 v209, v233, v226
	v_med3_f32 v227, v227, s62, v154
	v_med3_f32 v228, v228, s62, v154
	v_cvt_pk_fp8_f32 v209, v227, v228 op_sel:[0,0,1]
	s_nop 1
	ds_write_b128 v231, v[206:209] offset:35088
	v_mul_f32_e32 v233, 0x43800000, v68
	v_mul_f32_e32 v226, 0x43800000, v72
	v_med3_f32 v233, v233, s62, v154
	v_med3_f32 v226, v226, s62, v154
	v_mul_f32_e32 v227, 0x43800000, v76
	v_mul_f32_e32 v228, 0x43800000, v80
	v_cvt_pk_fp8_f32 v210, v233, v226
	v_med3_f32 v227, v227, s62, v154
	v_med3_f32 v228, v228, s62, v154
	v_cvt_pk_fp8_f32 v210, v227, v228 op_sel:[0,0,1]
	v_mul_f32_e32 v233, 0x43800000, v84
	v_mul_f32_e32 v226, 0x43800000, v88
	v_med3_f32 v233, v233, s62, v154
	v_med3_f32 v226, v226, s62, v154
	v_mul_f32_e32 v227, 0x43800000, v92
	v_mul_f32_e32 v228, 0x43800000, v96
	v_cvt_pk_fp8_f32 v211, v233, v226
	v_med3_f32 v227, v227, s62, v154
	v_med3_f32 v228, v228, s62, v154
	v_cvt_pk_fp8_f32 v211, v227, v228 op_sel:[0,0,1]
	v_mul_f32_e32 v233, 0x43800000, v100
	v_mul_f32_e32 v226, 0x43800000, v104
	v_med3_f32 v233, v233, s62, v154
	v_med3_f32 v226, v226, s62, v154
	v_mul_f32_e32 v227, 0x43800000, v108
	v_mul_f32_e32 v228, 0x43800000, v112
	v_cvt_pk_fp8_f32 v212, v233, v226
	v_med3_f32 v227, v227, s62, v154
	v_med3_f32 v228, v228, s62, v154
	v_cvt_pk_fp8_f32 v212, v227, v228 op_sel:[0,0,1]
	v_mul_f32_e32 v233, 0x43800000, v116
	v_mul_f32_e32 v226, 0x43800000, v120
	v_med3_f32 v233, v233, s62, v154
	v_med3_f32 v226, v226, s62, v154
	v_mul_f32_e32 v227, 0x43800000, v124
	v_mul_f32_e32 v228, 0x43800000, v128
	v_cvt_pk_fp8_f32 v213, v233, v226
	v_med3_f32 v227, v227, s62, v154
	v_med3_f32 v228, v228, s62, v154
	v_cvt_pk_fp8_f32 v213, v227, v228 op_sel:[0,0,1]
	s_nop 1
	ds_write_b128 v231, v[210:213] offset:35360
	v_mul_f32_e32 v233, 0x43800000, v69
	v_mul_f32_e32 v226, 0x43800000, v73
	v_med3_f32 v233, v233, s62, v154
	v_med3_f32 v226, v226, s62, v154
	v_mul_f32_e32 v227, 0x43800000, v77
	v_mul_f32_e32 v228, 0x43800000, v81
	v_cvt_pk_fp8_f32 v214, v233, v226
	v_med3_f32 v227, v227, s62, v154
	v_med3_f32 v228, v228, s62, v154
	v_cvt_pk_fp8_f32 v214, v227, v228 op_sel:[0,0,1]
	v_mul_f32_e32 v233, 0x43800000, v85
	v_mul_f32_e32 v226, 0x43800000, v89
	v_med3_f32 v233, v233, s62, v154
	v_med3_f32 v226, v226, s62, v154
	v_mul_f32_e32 v227, 0x43800000, v93
	v_mul_f32_e32 v228, 0x43800000, v97
	v_cvt_pk_fp8_f32 v215, v233, v226
	v_med3_f32 v227, v227, s62, v154
	v_med3_f32 v228, v228, s62, v154
	v_cvt_pk_fp8_f32 v215, v227, v228 op_sel:[0,0,1]
	v_mul_f32_e32 v233, 0x43800000, v101
	v_mul_f32_e32 v226, 0x43800000, v105
	v_med3_f32 v233, v233, s62, v154
	v_med3_f32 v226, v226, s62, v154
	v_mul_f32_e32 v227, 0x43800000, v109
	v_mul_f32_e32 v228, 0x43800000, v113
	v_cvt_pk_fp8_f32 v216, v233, v226
	v_med3_f32 v227, v227, s62, v154
	v_med3_f32 v228, v228, s62, v154
	v_cvt_pk_fp8_f32 v216, v227, v228 op_sel:[0,0,1]
	v_mul_f32_e32 v233, 0x43800000, v117
	v_mul_f32_e32 v226, 0x43800000, v121
	v_med3_f32 v233, v233, s62, v154
	v_med3_f32 v226, v226, s62, v154
	v_mul_f32_e32 v227, 0x43800000, v125
	v_mul_f32_e32 v228, 0x43800000, v129
	v_cvt_pk_fp8_f32 v217, v233, v226
	v_med3_f32 v227, v227, s62, v154
	v_med3_f32 v228, v228, s62, v154
	v_cvt_pk_fp8_f32 v217, v227, v228 op_sel:[0,0,1]
	s_nop 1
	ds_write_b128 v231, v[214:217] offset:35632
	s_waitcnt lgkmcnt(0)
	s_barrier
	global_load_dwordx4 v[66:69], v166, s[56:57] nt
	global_load_dwordx4 v[70:73], v250, s[56:57] nt
	global_load_dwordx4 v[74:77], v251, s[56:57] nt
	global_load_dwordx4 v[78:81], v246, s[56:57] nt
	global_load_dwordx4 v[82:85], v247, s[56:57] nt
	global_load_dwordx4 v[86:89], v248, s[56:57] nt
	global_load_dwordx4 v[90:93], v249, s[56:57] nt
	global_load_dwordx4 v[94:97], v242, s[56:57] nt
	global_load_dwordx4 v[98:101], v243, s[56:57] nt
	global_load_dwordx4 v[102:105], v244, s[56:57] nt
	global_load_dwordx4 v[106:109], v245, s[56:57] nt
	global_load_dwordx4 v[110:113], v238, s[56:57] nt
	global_load_dwordx4 v[114:117], v239, s[56:57] nt
	global_load_dwordx4 v[118:121], v240, s[56:57] nt
	global_load_dwordx4 v[122:125], v241, s[56:57] nt
	global_load_dwordx4 v[126:129], v234, s[56:57] nt
	s_add_u32 s56, s56, 0x400000
	s_addc_u32 s57, s57, 0
	ds_read_b128 v[202:205], v232 offset:34816
	ds_read_b128 v[206:209], v232 offset:43520
	ds_read_b128 v[210:213], v232 offset:52224
	ds_read_b128 v[214:217], v232 offset:60928
	s_waitcnt lgkmcnt(3)
	global_store_dwordx4 v235, v[202:205], s[58:59] nt
	s_waitcnt lgkmcnt(2)
	global_store_dwordx4 v236, v[206:209], s[58:59] nt
	s_waitcnt lgkmcnt(1)
	global_store_dwordx4 v237, v[210:213], s[58:59] nt
	s_waitcnt lgkmcnt(0)
	global_store_dwordx4 v230, v[214:217], s[58:59] nt
	s_add_u32 s58, s58, 0x100
	s_addc_u32 s59, s59, 0
	s_waitcnt vmcnt(52)
	v_mul_f32_e32 v233, 0x43800000, v130
	v_mul_f32_e32 v226, 0x43800000, v134
	v_med3_f32 v233, v233, s62, v154
	v_med3_f32 v226, v226, s62, v154
	v_mul_f32_e32 v227, 0x43800000, v138
	v_mul_f32_e32 v228, 0x43800000, v142
	v_cvt_pk_fp8_f32 v202, v233, v226
	v_med3_f32 v227, v227, s62, v154
	v_med3_f32 v228, v228, s62, v154
	v_cvt_pk_fp8_f32 v202, v227, v228 op_sel:[0,0,1]
	s_waitcnt vmcnt(48)
	v_mul_f32_e32 v233, 0x43800000, v146
	v_mul_f32_e32 v226, 0x43800000, v150
	v_med3_f32 v233, v233, s62, v154
	v_med3_f32 v226, v226, s62, v154
	v_mul_f32_e32 v227, 0x43800000, v158
	v_mul_f32_e32 v228, 0x43800000, v162
	v_cvt_pk_fp8_f32 v203, v233, v226
	v_med3_f32 v227, v227, s62, v154
	v_med3_f32 v228, v228, s62, v154
	v_cvt_pk_fp8_f32 v203, v227, v228 op_sel:[0,0,1]
	s_waitcnt vmcnt(44)
	v_mul_f32_e32 v233, 0x43800000, v168
	v_mul_f32_e32 v226, 0x43800000, v174
	v_med3_f32 v233, v233, s62, v154
	v_med3_f32 v226, v226, s62, v154
	v_mul_f32_e32 v227, 0x43800000, v178
	v_mul_f32_e32 v228, 0x43800000, v182
	v_cvt_pk_fp8_f32 v204, v233, v226
	v_med3_f32 v227, v227, s62, v154
	v_med3_f32 v228, v228, s62, v154
	v_cvt_pk_fp8_f32 v204, v227, v228 op_sel:[0,0,1]
	s_waitcnt vmcnt(40)
	v_mul_f32_e32 v233, 0x43800000, v186
	v_mul_f32_e32 v226, 0x43800000, v190
	v_med3_f32 v233, v233, s62, v154
	v_med3_f32 v226, v226, s62, v154
	v_mul_f32_e32 v227, 0x43800000, v194
	v_mul_f32_e32 v228, 0x43800000, v198
	v_cvt_pk_fp8_f32 v205, v233, v226
	v_med3_f32 v227, v227, s62, v154
	v_med3_f32 v228, v228, s62, v154
	v_cvt_pk_fp8_f32 v205, v227, v228 op_sel:[0,0,1]
	s_nop 1
	ds_write_b128 v231, v[202:205] offset:0
	v_mul_f32_e32 v233, 0x43800000, v131
	v_mul_f32_e32 v226, 0x43800000, v135
	v_med3_f32 v233, v233, s62, v154
	v_med3_f32 v226, v226, s62, v154
	v_mul_f32_e32 v227, 0x43800000, v139
	v_mul_f32_e32 v228, 0x43800000, v143
	v_cvt_pk_fp8_f32 v206, v233, v226
	v_med3_f32 v227, v227, s62, v154
	v_med3_f32 v228, v228, s62, v154
	v_cvt_pk_fp8_f32 v206, v227, v228 op_sel:[0,0,1]
	v_mul_f32_e32 v233, 0x43800000, v147
	v_mul_f32_e32 v226, 0x43800000, v151
	v_med3_f32 v233, v233, s62, v154
	v_med3_f32 v226, v226, s62, v154
	v_mul_f32_e32 v227, 0x43800000, v159
	v_mul_f32_e32 v228, 0x43800000, v163
	v_cvt_pk_fp8_f32 v207, v233, v226
	v_med3_f32 v227, v227, s62, v154
	v_med3_f32 v228, v228, s62, v154
	v_cvt_pk_fp8_f32 v207, v227, v228 op_sel:[0,0,1]
	v_mul_f32_e32 v233, 0x43800000, v169
	v_mul_f32_e32 v226, 0x43800000, v175
	v_med3_f32 v233, v233, s62, v154
	v_med3_f32 v226, v226, s62, v154
	v_mul_f32_e32 v227, 0x43800000, v179
	v_mul_f32_e32 v228, 0x43800000, v183
	v_cvt_pk_fp8_f32 v208, v233, v226
	v_med3_f32 v227, v227, s62, v154
	v_med3_f32 v228, v228, s62, v154
	v_cvt_pk_fp8_f32 v208, v227, v228 op_sel:[0,0,1]
	v_mul_f32_e32 v233, 0x43800000, v187
	v_mul_f32_e32 v226, 0x43800000, v191
	v_med3_f32 v233, v233, s62, v154
	v_med3_f32 v226, v226, s62, v154
	v_mul_f32_e32 v227, 0x43800000, v195
	v_mul_f32_e32 v228, 0x43800000, v199
	v_cvt_pk_fp8_f32 v209, v233, v226
	v_med3_f32 v227, v227, s62, v154
	v_med3_f32 v228, v228, s62, v154
	v_cvt_pk_fp8_f32 v209, v227, v228 op_sel:[0,0,1]
	s_nop 1
	ds_write_b128 v231, v[206:209] offset:272
	v_mul_f32_e32 v233, 0x43800000, v132
	v_mul_f32_e32 v226, 0x43800000, v136
	v_med3_f32 v233, v233, s62, v154
	v_med3_f32 v226, v226, s62, v154
	v_mul_f32_e32 v227, 0x43800000, v140
	v_mul_f32_e32 v228, 0x43800000, v144
	v_cvt_pk_fp8_f32 v210, v233, v226
	v_med3_f32 v227, v227, s62, v154
	v_med3_f32 v228, v228, s62, v154
	v_cvt_pk_fp8_f32 v210, v227, v228 op_sel:[0,0,1]
	v_mul_f32_e32 v233, 0x43800000, v148
	v_mul_f32_e32 v226, 0x43800000, v152
	v_med3_f32 v233, v233, s62, v154
	v_med3_f32 v226, v226, s62, v154
	v_mul_f32_e32 v227, 0x43800000, v160
	v_mul_f32_e32 v228, 0x43800000, v164
	v_cvt_pk_fp8_f32 v211, v233, v226
	v_med3_f32 v227, v227, s62, v154
	v_med3_f32 v228, v228, s62, v154
	v_cvt_pk_fp8_f32 v211, v227, v228 op_sel:[0,0,1]
	v_mul_f32_e32 v233, 0x43800000, v170
	v_mul_f32_e32 v226, 0x43800000, v176
	v_med3_f32 v233, v233, s62, v154
	v_med3_f32 v226, v226, s62, v154
	v_mul_f32_e32 v227, 0x43800000, v180
	v_mul_f32_e32 v228, 0x43800000, v184
	v_cvt_pk_fp8_f32 v212, v233, v226
	v_med3_f32 v227, v227, s62, v154
	v_med3_f32 v228, v228, s62, v154
	v_cvt_pk_fp8_f32 v212, v227, v228 op_sel:[0,0,1]
	v_mul_f32_e32 v233, 0x43800000, v188
	v_mul_f32_e32 v226, 0x43800000, v192
	v_med3_f32 v233, v233, s62, v154
	v_med3_f32 v226, v226, s62, v154
	v_mul_f32_e32 v227, 0x43800000, v196
	v_mul_f32_e32 v228, 0x43800000, v200
	v_cvt_pk_fp8_f32 v213, v233, v226
	v_med3_f32 v227, v227, s62, v154
	v_med3_f32 v228, v228, s62, v154
	v_cvt_pk_fp8_f32 v213, v227, v228 op_sel:[0,0,1]
	s_nop 1
	ds_write_b128 v231, v[210:213] offset:544
	v_mul_f32_e32 v233, 0x43800000, v133
	v_mul_f32_e32 v226, 0x43800000, v137
	v_med3_f32 v233, v233, s62, v154
	v_med3_f32 v226, v226, s62, v154
	v_mul_f32_e32 v227, 0x43800000, v141
	v_mul_f32_e32 v228, 0x43800000, v145
	v_cvt_pk_fp8_f32 v214, v233, v226
	v_med3_f32 v227, v227, s62, v154
	v_med3_f32 v228, v228, s62, v154
	v_cvt_pk_fp8_f32 v214, v227, v228 op_sel:[0,0,1]
	v_mul_f32_e32 v233, 0x43800000, v149
	v_mul_f32_e32 v226, 0x43800000, v153
	v_med3_f32 v233, v233, s62, v154
	v_med3_f32 v226, v226, s62, v154
	v_mul_f32_e32 v227, 0x43800000, v161
	v_mul_f32_e32 v228, 0x43800000, v165
	v_cvt_pk_fp8_f32 v215, v233, v226
	v_med3_f32 v227, v227, s62, v154
	v_med3_f32 v228, v228, s62, v154
	v_cvt_pk_fp8_f32 v215, v227, v228 op_sel:[0,0,1]
	v_mul_f32_e32 v233, 0x43800000, v171
	v_mul_f32_e32 v226, 0x43800000, v177
	v_med3_f32 v233, v233, s62, v154
	v_med3_f32 v226, v226, s62, v154
	v_mul_f32_e32 v227, 0x43800000, v181
	v_mul_f32_e32 v228, 0x43800000, v185
	v_cvt_pk_fp8_f32 v216, v233, v226
	v_med3_f32 v227, v227, s62, v154
	v_med3_f32 v228, v228, s62, v154
	v_cvt_pk_fp8_f32 v216, v227, v228 op_sel:[0,0,1]
	v_mul_f32_e32 v233, 0x43800000, v189
	v_mul_f32_e32 v226, 0x43800000, v193
	v_med3_f32 v233, v233, s62, v154
	v_med3_f32 v226, v226, s62, v154
	v_mul_f32_e32 v227, 0x43800000, v197
	v_mul_f32_e32 v228, 0x43800000, v201
	v_cvt_pk_fp8_f32 v217, v233, v226
	v_med3_f32 v227, v227, s62, v154
	v_med3_f32 v228, v228, s62, v154
	v_cvt_pk_fp8_f32 v217, v227, v228 op_sel:[0,0,1]
	s_nop 1
	ds_write_b128 v231, v[214:217] offset:816
	s_waitcnt lgkmcnt(0)
	s_barrier
	global_load_dwordx4 v[130:133], v166, s[56:57] nt
	global_load_dwordx4 v[134:137], v250, s[56:57] nt
	global_load_dwordx4 v[138:141], v251, s[56:57] nt
	global_load_dwordx4 v[142:145], v246, s[56:57] nt
	global_load_dwordx4 v[146:149], v247, s[56:57] nt
	global_load_dwordx4 v[150:153], v248, s[56:57] nt
	global_load_dwordx4 v[158:161], v249, s[56:57] nt
	global_load_dwordx4 v[162:165], v242, s[56:57] nt
	global_load_dwordx4 v[168:171], v243, s[56:57] nt
	global_load_dwordx4 v[174:177], v244, s[56:57] nt
	global_load_dwordx4 v[178:181], v245, s[56:57] nt
	global_load_dwordx4 v[182:185], v238, s[56:57] nt
	global_load_dwordx4 v[186:189], v239, s[56:57] nt
	global_load_dwordx4 v[190:193], v240, s[56:57] nt
	global_load_dwordx4 v[194:197], v241, s[56:57] nt
	global_load_dwordx4 v[198:201], v234, s[56:57] nt
	s_add_u32 s56, s56, 0x400000
	s_addc_u32 s57, s57, 0
	ds_read_b128 v[202:205], v232 offset:0
	ds_read_b128 v[206:209], v232 offset:8704
	ds_read_b128 v[210:213], v232 offset:17408
	ds_read_b128 v[214:217], v232 offset:26112
	s_waitcnt lgkmcnt(3)
	global_store_dwordx4 v235, v[202:205], s[58:59] nt
	s_waitcnt lgkmcnt(2)
	global_store_dwordx4 v236, v[206:209], s[58:59] nt
	s_waitcnt lgkmcnt(1)
	global_store_dwordx4 v237, v[210:213], s[58:59] nt
	s_waitcnt lgkmcnt(0)
	global_store_dwordx4 v230, v[214:217], s[58:59] nt
	s_add_u32 s58, s58, 0x100
	s_addc_u32 s59, s59, 0
	s_waitcnt vmcnt(56)
	v_mul_f32_e32 v233, 0x43800000, v2
	v_mul_f32_e32 v226, 0x43800000, v6
	v_med3_f32 v233, v233, s62, v154
	v_med3_f32 v226, v226, s62, v154
	v_mul_f32_e32 v227, 0x43800000, v10
	v_mul_f32_e32 v228, 0x43800000, v14
	v_cvt_pk_fp8_f32 v202, v233, v226
	v_med3_f32 v227, v227, s62, v154
	v_med3_f32 v228, v228, s62, v154
	v_cvt_pk_fp8_f32 v202, v227, v228 op_sel:[0,0,1]
	s_waitcnt vmcnt(52)
	v_mul_f32_e32 v233, 0x43800000, v18
	v_mul_f32_e32 v226, 0x43800000, v22
	v_med3_f32 v233, v233, s62, v154
	v_med3_f32 v226, v226, s62, v154
	v_mul_f32_e32 v227, 0x43800000, v26
	v_mul_f32_e32 v228, 0x43800000, v30
	v_cvt_pk_fp8_f32 v203, v233, v226
	v_med3_f32 v227, v227, s62, v154
	v_med3_f32 v228, v228, s62, v154
	v_cvt_pk_fp8_f32 v203, v227, v228 op_sel:[0,0,1]
	s_waitcnt vmcnt(48)
	v_mul_f32_e32 v233, 0x43800000, v34
	v_mul_f32_e32 v226, 0x43800000, v38
	v_med3_f32 v233, v233, s62, v154
	v_med3_f32 v226, v226, s62, v154
	v_mul_f32_e32 v227, 0x43800000, v42
	v_mul_f32_e32 v228, 0x43800000, v46
	v_cvt_pk_fp8_f32 v204, v233, v226
	v_med3_f32 v227, v227, s62, v154
	v_med3_f32 v228, v228, s62, v154
	v_cvt_pk_fp8_f32 v204, v227, v228 op_sel:[0,0,1]
	s_waitcnt vmcnt(44)
	v_mul_f32_e32 v233, 0x43800000, v50
	v_mul_f32_e32 v226, 0x43800000, v54
	v_med3_f32 v233, v233, s62, v154
	v_med3_f32 v226, v226, s62, v154
	v_mul_f32_e32 v227, 0x43800000, v58
	v_mul_f32_e32 v228, 0x43800000, v62
	v_cvt_pk_fp8_f32 v205, v233, v226
	v_med3_f32 v227, v227, s62, v154
	v_med3_f32 v228, v228, s62, v154
	v_cvt_pk_fp8_f32 v205, v227, v228 op_sel:[0,0,1]
	s_nop 1
	ds_write_b128 v231, v[202:205] offset:34816
	v_mul_f32_e32 v233, 0x43800000, v3
	v_mul_f32_e32 v226, 0x43800000, v7
	v_med3_f32 v233, v233, s62, v154
	v_med3_f32 v226, v226, s62, v154
	v_mul_f32_e32 v227, 0x43800000, v11
	v_mul_f32_e32 v228, 0x43800000, v15
	v_cvt_pk_fp8_f32 v206, v233, v226
	v_med3_f32 v227, v227, s62, v154
	v_med3_f32 v228, v228, s62, v154
	v_cvt_pk_fp8_f32 v206, v227, v228 op_sel:[0,0,1]
	v_mul_f32_e32 v233, 0x43800000, v19
	v_mul_f32_e32 v226, 0x43800000, v23
	v_med3_f32 v233, v233, s62, v154
	v_med3_f32 v226, v226, s62, v154
	v_mul_f32_e32 v227, 0x43800000, v27
	v_mul_f32_e32 v228, 0x43800000, v31
	v_cvt_pk_fp8_f32 v207, v233, v226
	v_med3_f32 v227, v227, s62, v154
	v_med3_f32 v228, v228, s62, v154
	v_cvt_pk_fp8_f32 v207, v227, v228 op_sel:[0,0,1]
	v_mul_f32_e32 v233, 0x43800000, v35
	v_mul_f32_e32 v226, 0x43800000, v39
	v_med3_f32 v233, v233, s62, v154
	v_med3_f32 v226, v226, s62, v154
	v_mul_f32_e32 v227, 0x43800000, v43
	v_mul_f32_e32 v228, 0x43800000, v47
	v_cvt_pk_fp8_f32 v208, v233, v226
	v_med3_f32 v227, v227, s62, v154
	v_med3_f32 v228, v228, s62, v154
	v_cvt_pk_fp8_f32 v208, v227, v228 op_sel:[0,0,1]
	v_mul_f32_e32 v233, 0x43800000, v51
	v_mul_f32_e32 v226, 0x43800000, v55
	v_med3_f32 v233, v233, s62, v154
	v_med3_f32 v226, v226, s62, v154
	v_mul_f32_e32 v227, 0x43800000, v59
	v_mul_f32_e32 v228, 0x43800000, v63
	v_cvt_pk_fp8_f32 v209, v233, v226
	v_med3_f32 v227, v227, s62, v154
	v_med3_f32 v228, v228, s62, v154
	v_cvt_pk_fp8_f32 v209, v227, v228 op_sel:[0,0,1]
	s_nop 1
	ds_write_b128 v231, v[206:209] offset:35088
	v_mul_f32_e32 v233, 0x43800000, v4
	v_mul_f32_e32 v226, 0x43800000, v8
	v_med3_f32 v233, v233, s62, v154
	v_med3_f32 v226, v226, s62, v154
	v_mul_f32_e32 v227, 0x43800000, v12
	v_mul_f32_e32 v228, 0x43800000, v16
	v_cvt_pk_fp8_f32 v210, v233, v226
	v_med3_f32 v227, v227, s62, v154
	v_med3_f32 v228, v228, s62, v154
	v_cvt_pk_fp8_f32 v210, v227, v228 op_sel:[0,0,1]
	v_mul_f32_e32 v233, 0x43800000, v20
	v_mul_f32_e32 v226, 0x43800000, v24
	v_med3_f32 v233, v233, s62, v154
	v_med3_f32 v226, v226, s62, v154
	v_mul_f32_e32 v227, 0x43800000, v28
	v_mul_f32_e32 v228, 0x43800000, v32
	v_cvt_pk_fp8_f32 v211, v233, v226
	v_med3_f32 v227, v227, s62, v154
	v_med3_f32 v228, v228, s62, v154
	v_cvt_pk_fp8_f32 v211, v227, v228 op_sel:[0,0,1]
	v_mul_f32_e32 v233, 0x43800000, v36
	v_mul_f32_e32 v226, 0x43800000, v40
	v_med3_f32 v233, v233, s62, v154
	v_med3_f32 v226, v226, s62, v154
	v_mul_f32_e32 v227, 0x43800000, v44
	v_mul_f32_e32 v228, 0x43800000, v48
	v_cvt_pk_fp8_f32 v212, v233, v226
	v_med3_f32 v227, v227, s62, v154
	v_med3_f32 v228, v228, s62, v154
	v_cvt_pk_fp8_f32 v212, v227, v228 op_sel:[0,0,1]
	v_mul_f32_e32 v233, 0x43800000, v52
	v_mul_f32_e32 v226, 0x43800000, v56
	v_med3_f32 v233, v233, s62, v154
	v_med3_f32 v226, v226, s62, v154
	v_mul_f32_e32 v227, 0x43800000, v60
	v_mul_f32_e32 v228, 0x43800000, v64
	v_cvt_pk_fp8_f32 v213, v233, v226
	v_med3_f32 v227, v227, s62, v154
	v_med3_f32 v228, v228, s62, v154
	v_cvt_pk_fp8_f32 v213, v227, v228 op_sel:[0,0,1]
	s_nop 1
	ds_write_b128 v231, v[210:213] offset:35360
	v_mul_f32_e32 v233, 0x43800000, v5
	v_mul_f32_e32 v226, 0x43800000, v9
	v_med3_f32 v233, v233, s62, v154
	v_med3_f32 v226, v226, s62, v154
	v_mul_f32_e32 v227, 0x43800000, v13
	v_mul_f32_e32 v228, 0x43800000, v17
	v_cvt_pk_fp8_f32 v214, v233, v226
	v_med3_f32 v227, v227, s62, v154
	v_med3_f32 v228, v228, s62, v154
	v_cvt_pk_fp8_f32 v214, v227, v228 op_sel:[0,0,1]
	v_mul_f32_e32 v233, 0x43800000, v21
	v_mul_f32_e32 v226, 0x43800000, v25
	v_med3_f32 v233, v233, s62, v154
	v_med3_f32 v226, v226, s62, v154
	v_mul_f32_e32 v227, 0x43800000, v29
	v_mul_f32_e32 v228, 0x43800000, v33
	v_cvt_pk_fp8_f32 v215, v233, v226
	v_med3_f32 v227, v227, s62, v154
	v_med3_f32 v228, v228, s62, v154
	v_cvt_pk_fp8_f32 v215, v227, v228 op_sel:[0,0,1]
	v_mul_f32_e32 v233, 0x43800000, v37
	v_mul_f32_e32 v226, 0x43800000, v41
	v_med3_f32 v233, v233, s62, v154
	v_med3_f32 v226, v226, s62, v154
	v_mul_f32_e32 v227, 0x43800000, v45
	v_mul_f32_e32 v228, 0x43800000, v49
	v_cvt_pk_fp8_f32 v216, v233, v226
	v_med3_f32 v227, v227, s62, v154
	v_med3_f32 v228, v228, s62, v154
	v_cvt_pk_fp8_f32 v216, v227, v228 op_sel:[0,0,1]
	v_mul_f32_e32 v233, 0x43800000, v53
	v_mul_f32_e32 v226, 0x43800000, v57
	v_med3_f32 v233, v233, s62, v154
	v_med3_f32 v226, v226, s62, v154
	v_mul_f32_e32 v227, 0x43800000, v61
	v_mul_f32_e32 v228, 0x43800000, v65
	v_cvt_pk_fp8_f32 v217, v233, v226
	v_med3_f32 v227, v227, s62, v154
	v_med3_f32 v228, v228, s62, v154
	v_cvt_pk_fp8_f32 v217, v227, v228 op_sel:[0,0,1]
	s_nop 1
	ds_write_b128 v231, v[214:217] offset:35632
	s_waitcnt lgkmcnt(0)
	s_barrier
	global_load_dwordx4 v[2:5], v166, s[56:57] nt
	global_load_dwordx4 v[6:9], v250, s[56:57] nt
	global_load_dwordx4 v[10:13], v251, s[56:57] nt
	global_load_dwordx4 v[14:17], v246, s[56:57] nt
	global_load_dwordx4 v[18:21], v247, s[56:57] nt
	global_load_dwordx4 v[22:25], v248, s[56:57] nt
	global_load_dwordx4 v[26:29], v249, s[56:57] nt
	global_load_dwordx4 v[30:33], v242, s[56:57] nt
	global_load_dwordx4 v[34:37], v243, s[56:57] nt
	global_load_dwordx4 v[38:41], v244, s[56:57] nt
	global_load_dwordx4 v[42:45], v245, s[56:57] nt
	global_load_dwordx4 v[46:49], v238, s[56:57] nt
	global_load_dwordx4 v[50:53], v239, s[56:57] nt
	global_load_dwordx4 v[54:57], v240, s[56:57] nt
	global_load_dwordx4 v[58:61], v241, s[56:57] nt
	global_load_dwordx4 v[62:65], v234, s[56:57] nt
	s_add_u32 s56, s56, 0x400000
	s_addc_u32 s57, s57, 0
	ds_read_b128 v[202:205], v232 offset:34816
	ds_read_b128 v[206:209], v232 offset:43520
	ds_read_b128 v[210:213], v232 offset:52224
	ds_read_b128 v[214:217], v232 offset:60928
	s_waitcnt lgkmcnt(3)
	global_store_dwordx4 v235, v[202:205], s[58:59] nt
	s_waitcnt lgkmcnt(2)
	global_store_dwordx4 v236, v[206:209], s[58:59] nt
	s_waitcnt lgkmcnt(1)
	global_store_dwordx4 v237, v[210:213], s[58:59] nt
	s_waitcnt lgkmcnt(0)
	global_store_dwordx4 v230, v[214:217], s[58:59] nt
	s_add_u32 s58, s58, 0x100
	s_addc_u32 s59, s59, 0
	s_waitcnt vmcnt(56)
	v_mul_f32_e32 v233, 0x43800000, v66
	v_mul_f32_e32 v226, 0x43800000, v70
	v_med3_f32 v233, v233, s62, v154
	v_med3_f32 v226, v226, s62, v154
	v_mul_f32_e32 v227, 0x43800000, v74
	v_mul_f32_e32 v228, 0x43800000, v78
	v_cvt_pk_fp8_f32 v202, v233, v226
	v_med3_f32 v227, v227, s62, v154
	v_med3_f32 v228, v228, s62, v154
	v_cvt_pk_fp8_f32 v202, v227, v228 op_sel:[0,0,1]
	s_waitcnt vmcnt(52)
	v_mul_f32_e32 v233, 0x43800000, v82
	v_mul_f32_e32 v226, 0x43800000, v86
	v_med3_f32 v233, v233, s62, v154
	v_med3_f32 v226, v226, s62, v154
	v_mul_f32_e32 v227, 0x43800000, v90
	v_mul_f32_e32 v228, 0x43800000, v94
	v_cvt_pk_fp8_f32 v203, v233, v226
	v_med3_f32 v227, v227, s62, v154
	v_med3_f32 v228, v228, s62, v154
	v_cvt_pk_fp8_f32 v203, v227, v228 op_sel:[0,0,1]
	s_waitcnt vmcnt(48)
	v_mul_f32_e32 v233, 0x43800000, v98
	v_mul_f32_e32 v226, 0x43800000, v102
	v_med3_f32 v233, v233, s62, v154
	v_med3_f32 v226, v226, s62, v154
	v_mul_f32_e32 v227, 0x43800000, v106
	v_mul_f32_e32 v228, 0x43800000, v110
	v_cvt_pk_fp8_f32 v204, v233, v226
	v_med3_f32 v227, v227, s62, v154
	v_med3_f32 v228, v228, s62, v154
	v_cvt_pk_fp8_f32 v204, v227, v228 op_sel:[0,0,1]
	s_waitcnt vmcnt(44)
	v_mul_f32_e32 v233, 0x43800000, v114
	v_mul_f32_e32 v226, 0x43800000, v118
	v_med3_f32 v233, v233, s62, v154
	v_med3_f32 v226, v226, s62, v154
	v_mul_f32_e32 v227, 0x43800000, v122
	v_mul_f32_e32 v228, 0x43800000, v126
	v_cvt_pk_fp8_f32 v205, v233, v226
	v_med3_f32 v227, v227, s62, v154
	v_med3_f32 v228, v228, s62, v154
	v_cvt_pk_fp8_f32 v205, v227, v228 op_sel:[0,0,1]
	s_nop 1
	ds_write_b128 v231, v[202:205] offset:0
	v_mul_f32_e32 v233, 0x43800000, v67
	v_mul_f32_e32 v226, 0x43800000, v71
	v_med3_f32 v233, v233, s62, v154
	v_med3_f32 v226, v226, s62, v154
	v_mul_f32_e32 v227, 0x43800000, v75
	v_mul_f32_e32 v228, 0x43800000, v79
	v_cvt_pk_fp8_f32 v206, v233, v226
	v_med3_f32 v227, v227, s62, v154
	v_med3_f32 v228, v228, s62, v154
	v_cvt_pk_fp8_f32 v206, v227, v228 op_sel:[0,0,1]
	v_mul_f32_e32 v233, 0x43800000, v83
	v_mul_f32_e32 v226, 0x43800000, v87
	v_med3_f32 v233, v233, s62, v154
	v_med3_f32 v226, v226, s62, v154
	v_mul_f32_e32 v227, 0x43800000, v91
	v_mul_f32_e32 v228, 0x43800000, v95
	v_cvt_pk_fp8_f32 v207, v233, v226
	v_med3_f32 v227, v227, s62, v154
	v_med3_f32 v228, v228, s62, v154
	v_cvt_pk_fp8_f32 v207, v227, v228 op_sel:[0,0,1]
	v_mul_f32_e32 v233, 0x43800000, v99
	v_mul_f32_e32 v226, 0x43800000, v103
	v_med3_f32 v233, v233, s62, v154
	v_med3_f32 v226, v226, s62, v154
	v_mul_f32_e32 v227, 0x43800000, v107
	v_mul_f32_e32 v228, 0x43800000, v111
	v_cvt_pk_fp8_f32 v208, v233, v226
	v_med3_f32 v227, v227, s62, v154
	v_med3_f32 v228, v228, s62, v154
	v_cvt_pk_fp8_f32 v208, v227, v228 op_sel:[0,0,1]
	v_mul_f32_e32 v233, 0x43800000, v115
	v_mul_f32_e32 v226, 0x43800000, v119
	v_med3_f32 v233, v233, s62, v154
	v_med3_f32 v226, v226, s62, v154
	v_mul_f32_e32 v227, 0x43800000, v123
	v_mul_f32_e32 v228, 0x43800000, v127
	v_cvt_pk_fp8_f32 v209, v233, v226
	v_med3_f32 v227, v227, s62, v154
	v_med3_f32 v228, v228, s62, v154
	v_cvt_pk_fp8_f32 v209, v227, v228 op_sel:[0,0,1]
	s_nop 1
	ds_write_b128 v231, v[206:209] offset:272
	v_mul_f32_e32 v233, 0x43800000, v68
	v_mul_f32_e32 v226, 0x43800000, v72
	v_med3_f32 v233, v233, s62, v154
	v_med3_f32 v226, v226, s62, v154
	v_mul_f32_e32 v227, 0x43800000, v76
	v_mul_f32_e32 v228, 0x43800000, v80
	v_cvt_pk_fp8_f32 v210, v233, v226
	v_med3_f32 v227, v227, s62, v154
	v_med3_f32 v228, v228, s62, v154
	v_cvt_pk_fp8_f32 v210, v227, v228 op_sel:[0,0,1]
	v_mul_f32_e32 v233, 0x43800000, v84
	v_mul_f32_e32 v226, 0x43800000, v88
	v_med3_f32 v233, v233, s62, v154
	v_med3_f32 v226, v226, s62, v154
	v_mul_f32_e32 v227, 0x43800000, v92
	v_mul_f32_e32 v228, 0x43800000, v96
	v_cvt_pk_fp8_f32 v211, v233, v226
	v_med3_f32 v227, v227, s62, v154
	v_med3_f32 v228, v228, s62, v154
	v_cvt_pk_fp8_f32 v211, v227, v228 op_sel:[0,0,1]
	v_mul_f32_e32 v233, 0x43800000, v100
	v_mul_f32_e32 v226, 0x43800000, v104
	v_med3_f32 v233, v233, s62, v154
	v_med3_f32 v226, v226, s62, v154
	v_mul_f32_e32 v227, 0x43800000, v108
	v_mul_f32_e32 v228, 0x43800000, v112
	v_cvt_pk_fp8_f32 v212, v233, v226
	v_med3_f32 v227, v227, s62, v154
	v_med3_f32 v228, v228, s62, v154
	v_cvt_pk_fp8_f32 v212, v227, v228 op_sel:[0,0,1]
	v_mul_f32_e32 v233, 0x43800000, v116
	v_mul_f32_e32 v226, 0x43800000, v120
	v_med3_f32 v233, v233, s62, v154
	v_med3_f32 v226, v226, s62, v154
	v_mul_f32_e32 v227, 0x43800000, v124
	v_mul_f32_e32 v228, 0x43800000, v128
	v_cvt_pk_fp8_f32 v213, v233, v226
	v_med3_f32 v227, v227, s62, v154
	v_med3_f32 v228, v228, s62, v154
	v_cvt_pk_fp8_f32 v213, v227, v228 op_sel:[0,0,1]
	s_nop 1
	ds_write_b128 v231, v[210:213] offset:544
	v_mul_f32_e32 v233, 0x43800000, v69
	v_mul_f32_e32 v226, 0x43800000, v73
	v_med3_f32 v233, v233, s62, v154
	v_med3_f32 v226, v226, s62, v154
	v_mul_f32_e32 v227, 0x43800000, v77
	v_mul_f32_e32 v228, 0x43800000, v81
	v_cvt_pk_fp8_f32 v214, v233, v226
	v_med3_f32 v227, v227, s62, v154
	v_med3_f32 v228, v228, s62, v154
	v_cvt_pk_fp8_f32 v214, v227, v228 op_sel:[0,0,1]
	v_mul_f32_e32 v233, 0x43800000, v85
	v_mul_f32_e32 v226, 0x43800000, v89
	v_med3_f32 v233, v233, s62, v154
	v_med3_f32 v226, v226, s62, v154
	v_mul_f32_e32 v227, 0x43800000, v93
	v_mul_f32_e32 v228, 0x43800000, v97
	v_cvt_pk_fp8_f32 v215, v233, v226
	v_med3_f32 v227, v227, s62, v154
	v_med3_f32 v228, v228, s62, v154
	v_cvt_pk_fp8_f32 v215, v227, v228 op_sel:[0,0,1]
	v_mul_f32_e32 v233, 0x43800000, v101
	v_mul_f32_e32 v226, 0x43800000, v105
	v_med3_f32 v233, v233, s62, v154
	v_med3_f32 v226, v226, s62, v154
	v_mul_f32_e32 v227, 0x43800000, v109
	v_mul_f32_e32 v228, 0x43800000, v113
	v_cvt_pk_fp8_f32 v216, v233, v226
	v_med3_f32 v227, v227, s62, v154
	v_med3_f32 v228, v228, s62, v154
	v_cvt_pk_fp8_f32 v216, v227, v228 op_sel:[0,0,1]
	v_mul_f32_e32 v233, 0x43800000, v117
	v_mul_f32_e32 v226, 0x43800000, v121
	v_med3_f32 v233, v233, s62, v154
	v_med3_f32 v226, v226, s62, v154
	v_mul_f32_e32 v227, 0x43800000, v125
	v_mul_f32_e32 v228, 0x43800000, v129
	v_cvt_pk_fp8_f32 v217, v233, v226
	v_med3_f32 v227, v227, s62, v154
	v_med3_f32 v228, v228, s62, v154
	v_cvt_pk_fp8_f32 v217, v227, v228 op_sel:[0,0,1]
	s_nop 1
	ds_write_b128 v231, v[214:217] offset:816
	s_waitcnt lgkmcnt(0)
	s_barrier
	global_load_dwordx4 v[66:69], v166, s[56:57] nt
	global_load_dwordx4 v[70:73], v250, s[56:57] nt
	global_load_dwordx4 v[74:77], v251, s[56:57] nt
	global_load_dwordx4 v[78:81], v246, s[56:57] nt
	global_load_dwordx4 v[82:85], v247, s[56:57] nt
	global_load_dwordx4 v[86:89], v248, s[56:57] nt
	global_load_dwordx4 v[90:93], v249, s[56:57] nt
	global_load_dwordx4 v[94:97], v242, s[56:57] nt
	global_load_dwordx4 v[98:101], v243, s[56:57] nt
	global_load_dwordx4 v[102:105], v244, s[56:57] nt
	global_load_dwordx4 v[106:109], v245, s[56:57] nt
	global_load_dwordx4 v[110:113], v238, s[56:57] nt
	global_load_dwordx4 v[114:117], v239, s[56:57] nt
	global_load_dwordx4 v[118:121], v240, s[56:57] nt
	global_load_dwordx4 v[122:125], v241, s[56:57] nt
	global_load_dwordx4 v[126:129], v234, s[56:57] nt
	s_add_u32 s56, s56, 0x400000
	s_addc_u32 s57, s57, 0
	ds_read_b128 v[202:205], v232 offset:0
	ds_read_b128 v[206:209], v232 offset:8704
	ds_read_b128 v[210:213], v232 offset:17408
	ds_read_b128 v[214:217], v232 offset:26112
	s_waitcnt lgkmcnt(3)
	global_store_dwordx4 v235, v[202:205], s[58:59] nt
	s_waitcnt lgkmcnt(2)
	global_store_dwordx4 v236, v[206:209], s[58:59] nt
	s_waitcnt lgkmcnt(1)
	global_store_dwordx4 v237, v[210:213], s[58:59] nt
	s_waitcnt lgkmcnt(0)
	global_store_dwordx4 v230, v[214:217], s[58:59] nt
	s_add_u32 s58, s58, 0x100
	s_addc_u32 s59, s59, 0
	s_waitcnt vmcnt(56)
	v_mul_f32_e32 v233, 0x43800000, v130
	v_mul_f32_e32 v226, 0x43800000, v134
	v_med3_f32 v233, v233, s62, v154
	v_med3_f32 v226, v226, s62, v154
	v_mul_f32_e32 v227, 0x43800000, v138
	v_mul_f32_e32 v228, 0x43800000, v142
	v_cvt_pk_fp8_f32 v202, v233, v226
	v_med3_f32 v227, v227, s62, v154
	v_med3_f32 v228, v228, s62, v154
	v_cvt_pk_fp8_f32 v202, v227, v228 op_sel:[0,0,1]
	s_waitcnt vmcnt(52)
	v_mul_f32_e32 v233, 0x43800000, v146
	v_mul_f32_e32 v226, 0x43800000, v150
	v_med3_f32 v233, v233, s62, v154
	v_med3_f32 v226, v226, s62, v154
	v_mul_f32_e32 v227, 0x43800000, v158
	v_mul_f32_e32 v228, 0x43800000, v162
	v_cvt_pk_fp8_f32 v203, v233, v226
	v_med3_f32 v227, v227, s62, v154
	v_med3_f32 v228, v228, s62, v154
	v_cvt_pk_fp8_f32 v203, v227, v228 op_sel:[0,0,1]
	s_waitcnt vmcnt(48)
	v_mul_f32_e32 v233, 0x43800000, v168
	v_mul_f32_e32 v226, 0x43800000, v174
	v_med3_f32 v233, v233, s62, v154
	v_med3_f32 v226, v226, s62, v154
	v_mul_f32_e32 v227, 0x43800000, v178
	v_mul_f32_e32 v228, 0x43800000, v182
	v_cvt_pk_fp8_f32 v204, v233, v226
	v_med3_f32 v227, v227, s62, v154
	v_med3_f32 v228, v228, s62, v154
	v_cvt_pk_fp8_f32 v204, v227, v228 op_sel:[0,0,1]
	s_waitcnt vmcnt(44)
	v_mul_f32_e32 v233, 0x43800000, v186
	v_mul_f32_e32 v226, 0x43800000, v190
	v_med3_f32 v233, v233, s62, v154
	v_med3_f32 v226, v226, s62, v154
	v_mul_f32_e32 v227, 0x43800000, v194
	v_mul_f32_e32 v228, 0x43800000, v198
	v_cvt_pk_fp8_f32 v205, v233, v226
	v_med3_f32 v227, v227, s62, v154
	v_med3_f32 v228, v228, s62, v154
	v_cvt_pk_fp8_f32 v205, v227, v228 op_sel:[0,0,1]
	s_nop 1
	ds_write_b128 v231, v[202:205] offset:34816
	v_mul_f32_e32 v233, 0x43800000, v131
	v_mul_f32_e32 v226, 0x43800000, v135
	v_med3_f32 v233, v233, s62, v154
	v_med3_f32 v226, v226, s62, v154
	v_mul_f32_e32 v227, 0x43800000, v139
	v_mul_f32_e32 v228, 0x43800000, v143
	v_cvt_pk_fp8_f32 v206, v233, v226
	v_med3_f32 v227, v227, s62, v154
	v_med3_f32 v228, v228, s62, v154
	v_cvt_pk_fp8_f32 v206, v227, v228 op_sel:[0,0,1]
	v_mul_f32_e32 v233, 0x43800000, v147
	v_mul_f32_e32 v226, 0x43800000, v151
	v_med3_f32 v233, v233, s62, v154
	v_med3_f32 v226, v226, s62, v154
	v_mul_f32_e32 v227, 0x43800000, v159
	v_mul_f32_e32 v228, 0x43800000, v163
	v_cvt_pk_fp8_f32 v207, v233, v226
	v_med3_f32 v227, v227, s62, v154
	v_med3_f32 v228, v228, s62, v154
	v_cvt_pk_fp8_f32 v207, v227, v228 op_sel:[0,0,1]
	v_mul_f32_e32 v233, 0x43800000, v169
	v_mul_f32_e32 v226, 0x43800000, v175
	v_med3_f32 v233, v233, s62, v154
	v_med3_f32 v226, v226, s62, v154
	v_mul_f32_e32 v227, 0x43800000, v179
	v_mul_f32_e32 v228, 0x43800000, v183
	v_cvt_pk_fp8_f32 v208, v233, v226
	v_med3_f32 v227, v227, s62, v154
	v_med3_f32 v228, v228, s62, v154
	v_cvt_pk_fp8_f32 v208, v227, v228 op_sel:[0,0,1]
	v_mul_f32_e32 v233, 0x43800000, v187
	v_mul_f32_e32 v226, 0x43800000, v191
	v_med3_f32 v233, v233, s62, v154
	v_med3_f32 v226, v226, s62, v154
	v_mul_f32_e32 v227, 0x43800000, v195
	v_mul_f32_e32 v228, 0x43800000, v199
	v_cvt_pk_fp8_f32 v209, v233, v226
	v_med3_f32 v227, v227, s62, v154
	v_med3_f32 v228, v228, s62, v154
	v_cvt_pk_fp8_f32 v209, v227, v228 op_sel:[0,0,1]
	s_nop 1
	ds_write_b128 v231, v[206:209] offset:35088
	v_mul_f32_e32 v233, 0x43800000, v132
	v_mul_f32_e32 v226, 0x43800000, v136
	v_med3_f32 v233, v233, s62, v154
	v_med3_f32 v226, v226, s62, v154
	v_mul_f32_e32 v227, 0x43800000, v140
	v_mul_f32_e32 v228, 0x43800000, v144
	v_cvt_pk_fp8_f32 v210, v233, v226
	v_med3_f32 v227, v227, s62, v154
	v_med3_f32 v228, v228, s62, v154
	v_cvt_pk_fp8_f32 v210, v227, v228 op_sel:[0,0,1]
	v_mul_f32_e32 v233, 0x43800000, v148
	v_mul_f32_e32 v226, 0x43800000, v152
	v_med3_f32 v233, v233, s62, v154
	v_med3_f32 v226, v226, s62, v154
	v_mul_f32_e32 v227, 0x43800000, v160
	v_mul_f32_e32 v228, 0x43800000, v164
	v_cvt_pk_fp8_f32 v211, v233, v226
	v_med3_f32 v227, v227, s62, v154
	v_med3_f32 v228, v228, s62, v154
	v_cvt_pk_fp8_f32 v211, v227, v228 op_sel:[0,0,1]
	v_mul_f32_e32 v233, 0x43800000, v170
	v_mul_f32_e32 v226, 0x43800000, v176
	v_med3_f32 v233, v233, s62, v154
	v_med3_f32 v226, v226, s62, v154
	v_mul_f32_e32 v227, 0x43800000, v180
	v_mul_f32_e32 v228, 0x43800000, v184
	v_cvt_pk_fp8_f32 v212, v233, v226
	v_med3_f32 v227, v227, s62, v154
	v_med3_f32 v228, v228, s62, v154
	v_cvt_pk_fp8_f32 v212, v227, v228 op_sel:[0,0,1]
	v_mul_f32_e32 v233, 0x43800000, v188
	v_mul_f32_e32 v226, 0x43800000, v192
	v_med3_f32 v233, v233, s62, v154
	v_med3_f32 v226, v226, s62, v154
	v_mul_f32_e32 v227, 0x43800000, v196
	v_mul_f32_e32 v228, 0x43800000, v200
	v_cvt_pk_fp8_f32 v213, v233, v226
	v_med3_f32 v227, v227, s62, v154
	v_med3_f32 v228, v228, s62, v154
	v_cvt_pk_fp8_f32 v213, v227, v228 op_sel:[0,0,1]
	s_nop 1
	ds_write_b128 v231, v[210:213] offset:35360
	v_mul_f32_e32 v233, 0x43800000, v133
	v_mul_f32_e32 v226, 0x43800000, v137
	v_med3_f32 v233, v233, s62, v154
	v_med3_f32 v226, v226, s62, v154
	v_mul_f32_e32 v227, 0x43800000, v141
	v_mul_f32_e32 v228, 0x43800000, v145
	v_cvt_pk_fp8_f32 v214, v233, v226
	v_med3_f32 v227, v227, s62, v154
	v_med3_f32 v228, v228, s62, v154
	v_cvt_pk_fp8_f32 v214, v227, v228 op_sel:[0,0,1]
	v_mul_f32_e32 v233, 0x43800000, v149
	v_mul_f32_e32 v226, 0x43800000, v153
	v_med3_f32 v233, v233, s62, v154
	v_med3_f32 v226, v226, s62, v154
	v_mul_f32_e32 v227, 0x43800000, v161
	v_mul_f32_e32 v228, 0x43800000, v165
	v_cvt_pk_fp8_f32 v215, v233, v226
	v_med3_f32 v227, v227, s62, v154
	v_med3_f32 v228, v228, s62, v154
	v_cvt_pk_fp8_f32 v215, v227, v228 op_sel:[0,0,1]
	v_mul_f32_e32 v233, 0x43800000, v171
	v_mul_f32_e32 v226, 0x43800000, v177
	v_med3_f32 v233, v233, s62, v154
	v_med3_f32 v226, v226, s62, v154
	v_mul_f32_e32 v227, 0x43800000, v181
	v_mul_f32_e32 v228, 0x43800000, v185
	v_cvt_pk_fp8_f32 v216, v233, v226
	v_med3_f32 v227, v227, s62, v154
	v_med3_f32 v228, v228, s62, v154
	v_cvt_pk_fp8_f32 v216, v227, v228 op_sel:[0,0,1]
	v_mul_f32_e32 v233, 0x43800000, v189
	v_mul_f32_e32 v226, 0x43800000, v193
	v_med3_f32 v233, v233, s62, v154
	v_med3_f32 v226, v226, s62, v154
	v_mul_f32_e32 v227, 0x43800000, v197
	v_mul_f32_e32 v228, 0x43800000, v201
	v_cvt_pk_fp8_f32 v217, v233, v226
	v_med3_f32 v227, v227, s62, v154
	v_med3_f32 v228, v228, s62, v154
	v_cvt_pk_fp8_f32 v217, v227, v228 op_sel:[0,0,1]
	s_nop 1
	ds_write_b128 v231, v[214:217] offset:35632
	s_waitcnt lgkmcnt(0)
	s_barrier
	ds_read_b128 v[202:205], v232 offset:34816
	ds_read_b128 v[206:209], v232 offset:43520
	ds_read_b128 v[210:213], v232 offset:52224
	ds_read_b128 v[214:217], v232 offset:60928
	s_waitcnt lgkmcnt(3)
	global_store_dwordx4 v235, v[202:205], s[58:59] nt
	s_waitcnt lgkmcnt(2)
	global_store_dwordx4 v236, v[206:209], s[58:59] nt
	s_waitcnt lgkmcnt(1)
	global_store_dwordx4 v237, v[210:213], s[58:59] nt
	s_waitcnt lgkmcnt(0)
	global_store_dwordx4 v230, v[214:217], s[58:59] nt
	s_add_u32 s58, s58, 0x100
	s_addc_u32 s59, s59, 0
	s_waitcnt vmcnt(40)
	v_mul_f32_e32 v233, 0x43800000, v2
	v_mul_f32_e32 v226, 0x43800000, v6
	v_med3_f32 v233, v233, s62, v154
	v_med3_f32 v226, v226, s62, v154
	v_mul_f32_e32 v227, 0x43800000, v10
	v_mul_f32_e32 v228, 0x43800000, v14
	v_cvt_pk_fp8_f32 v202, v233, v226
	v_med3_f32 v227, v227, s62, v154
	v_med3_f32 v228, v228, s62, v154
	v_cvt_pk_fp8_f32 v202, v227, v228 op_sel:[0,0,1]
	s_waitcnt vmcnt(36)
	v_mul_f32_e32 v233, 0x43800000, v18
	v_mul_f32_e32 v226, 0x43800000, v22
	v_med3_f32 v233, v233, s62, v154
	v_med3_f32 v226, v226, s62, v154
	v_mul_f32_e32 v227, 0x43800000, v26
	v_mul_f32_e32 v228, 0x43800000, v30
	v_cvt_pk_fp8_f32 v203, v233, v226
	v_med3_f32 v227, v227, s62, v154
	v_med3_f32 v228, v228, s62, v154
	v_cvt_pk_fp8_f32 v203, v227, v228 op_sel:[0,0,1]
	s_waitcnt vmcnt(32)
	v_mul_f32_e32 v233, 0x43800000, v34
	v_mul_f32_e32 v226, 0x43800000, v38
	v_med3_f32 v233, v233, s62, v154
	v_med3_f32 v226, v226, s62, v154
	v_mul_f32_e32 v227, 0x43800000, v42
	v_mul_f32_e32 v228, 0x43800000, v46
	v_cvt_pk_fp8_f32 v204, v233, v226
	v_med3_f32 v227, v227, s62, v154
	v_med3_f32 v228, v228, s62, v154
	v_cvt_pk_fp8_f32 v204, v227, v228 op_sel:[0,0,1]
	s_waitcnt vmcnt(28)
	v_mul_f32_e32 v233, 0x43800000, v50
	v_mul_f32_e32 v226, 0x43800000, v54
	v_med3_f32 v233, v233, s62, v154
	v_med3_f32 v226, v226, s62, v154
	v_mul_f32_e32 v227, 0x43800000, v58
	v_mul_f32_e32 v228, 0x43800000, v62
	v_cvt_pk_fp8_f32 v205, v233, v226
	v_med3_f32 v227, v227, s62, v154
	v_med3_f32 v228, v228, s62, v154
	v_cvt_pk_fp8_f32 v205, v227, v228 op_sel:[0,0,1]
	s_nop 1
	ds_write_b128 v231, v[202:205] offset:0
	v_mul_f32_e32 v233, 0x43800000, v3
	v_mul_f32_e32 v226, 0x43800000, v7
	v_med3_f32 v233, v233, s62, v154
	v_med3_f32 v226, v226, s62, v154
	v_mul_f32_e32 v227, 0x43800000, v11
	v_mul_f32_e32 v228, 0x43800000, v15
	v_cvt_pk_fp8_f32 v206, v233, v226
	v_med3_f32 v227, v227, s62, v154
	v_med3_f32 v228, v228, s62, v154
	v_cvt_pk_fp8_f32 v206, v227, v228 op_sel:[0,0,1]
	v_mul_f32_e32 v233, 0x43800000, v19
	v_mul_f32_e32 v226, 0x43800000, v23
	v_med3_f32 v233, v233, s62, v154
	v_med3_f32 v226, v226, s62, v154
	v_mul_f32_e32 v227, 0x43800000, v27
	v_mul_f32_e32 v228, 0x43800000, v31
	v_cvt_pk_fp8_f32 v207, v233, v226
	v_med3_f32 v227, v227, s62, v154
	v_med3_f32 v228, v228, s62, v154
	v_cvt_pk_fp8_f32 v207, v227, v228 op_sel:[0,0,1]
	v_mul_f32_e32 v233, 0x43800000, v35
	v_mul_f32_e32 v226, 0x43800000, v39
	v_med3_f32 v233, v233, s62, v154
	v_med3_f32 v226, v226, s62, v154
	v_mul_f32_e32 v227, 0x43800000, v43
	v_mul_f32_e32 v228, 0x43800000, v47
	v_cvt_pk_fp8_f32 v208, v233, v226
	v_med3_f32 v227, v227, s62, v154
	v_med3_f32 v228, v228, s62, v154
	v_cvt_pk_fp8_f32 v208, v227, v228 op_sel:[0,0,1]
	v_mul_f32_e32 v233, 0x43800000, v51
	v_mul_f32_e32 v226, 0x43800000, v55
	v_med3_f32 v233, v233, s62, v154
	v_med3_f32 v226, v226, s62, v154
	v_mul_f32_e32 v227, 0x43800000, v59
	v_mul_f32_e32 v228, 0x43800000, v63
	v_cvt_pk_fp8_f32 v209, v233, v226
	v_med3_f32 v227, v227, s62, v154
	v_med3_f32 v228, v228, s62, v154
	v_cvt_pk_fp8_f32 v209, v227, v228 op_sel:[0,0,1]
	s_nop 1
	ds_write_b128 v231, v[206:209] offset:272
	v_mul_f32_e32 v233, 0x43800000, v4
	v_mul_f32_e32 v226, 0x43800000, v8
	v_med3_f32 v233, v233, s62, v154
	v_med3_f32 v226, v226, s62, v154
	v_mul_f32_e32 v227, 0x43800000, v12
	v_mul_f32_e32 v228, 0x43800000, v16
	v_cvt_pk_fp8_f32 v210, v233, v226
	v_med3_f32 v227, v227, s62, v154
	v_med3_f32 v228, v228, s62, v154
	v_cvt_pk_fp8_f32 v210, v227, v228 op_sel:[0,0,1]
	v_mul_f32_e32 v233, 0x43800000, v20
	v_mul_f32_e32 v226, 0x43800000, v24
	v_med3_f32 v233, v233, s62, v154
	v_med3_f32 v226, v226, s62, v154
	v_mul_f32_e32 v227, 0x43800000, v28
	v_mul_f32_e32 v228, 0x43800000, v32
	v_cvt_pk_fp8_f32 v211, v233, v226
	v_med3_f32 v227, v227, s62, v154
	v_med3_f32 v228, v228, s62, v154
	v_cvt_pk_fp8_f32 v211, v227, v228 op_sel:[0,0,1]
	v_mul_f32_e32 v233, 0x43800000, v36
	v_mul_f32_e32 v226, 0x43800000, v40
	v_med3_f32 v233, v233, s62, v154
	v_med3_f32 v226, v226, s62, v154
	v_mul_f32_e32 v227, 0x43800000, v44
	v_mul_f32_e32 v228, 0x43800000, v48
	v_cvt_pk_fp8_f32 v212, v233, v226
	v_med3_f32 v227, v227, s62, v154
	v_med3_f32 v228, v228, s62, v154
	v_cvt_pk_fp8_f32 v212, v227, v228 op_sel:[0,0,1]
	v_mul_f32_e32 v233, 0x43800000, v52
	v_mul_f32_e32 v226, 0x43800000, v56
	v_med3_f32 v233, v233, s62, v154
	v_med3_f32 v226, v226, s62, v154
	v_mul_f32_e32 v227, 0x43800000, v60
	v_mul_f32_e32 v228, 0x43800000, v64
	v_cvt_pk_fp8_f32 v213, v233, v226
	v_med3_f32 v227, v227, s62, v154
	v_med3_f32 v228, v228, s62, v154
	v_cvt_pk_fp8_f32 v213, v227, v228 op_sel:[0,0,1]
	s_nop 1
	ds_write_b128 v231, v[210:213] offset:544
	v_mul_f32_e32 v233, 0x43800000, v5
	v_mul_f32_e32 v226, 0x43800000, v9
	v_med3_f32 v233, v233, s62, v154
	v_med3_f32 v226, v226, s62, v154
	v_mul_f32_e32 v227, 0x43800000, v13
	v_mul_f32_e32 v228, 0x43800000, v17
	v_cvt_pk_fp8_f32 v214, v233, v226
	v_med3_f32 v227, v227, s62, v154
	v_med3_f32 v228, v228, s62, v154
	v_cvt_pk_fp8_f32 v214, v227, v228 op_sel:[0,0,1]
	v_mul_f32_e32 v233, 0x43800000, v21
	v_mul_f32_e32 v226, 0x43800000, v25
	v_med3_f32 v233, v233, s62, v154
	v_med3_f32 v226, v226, s62, v154
	v_mul_f32_e32 v227, 0x43800000, v29
	v_mul_f32_e32 v228, 0x43800000, v33
	v_cvt_pk_fp8_f32 v215, v233, v226
	v_med3_f32 v227, v227, s62, v154
	v_med3_f32 v228, v228, s62, v154
	v_cvt_pk_fp8_f32 v215, v227, v228 op_sel:[0,0,1]
	v_mul_f32_e32 v233, 0x43800000, v37
	v_mul_f32_e32 v226, 0x43800000, v41
	v_med3_f32 v233, v233, s62, v154
	v_med3_f32 v226, v226, s62, v154
	v_mul_f32_e32 v227, 0x43800000, v45
	v_mul_f32_e32 v228, 0x43800000, v49
	v_cvt_pk_fp8_f32 v216, v233, v226
	v_med3_f32 v227, v227, s62, v154
	v_med3_f32 v228, v228, s62, v154
	v_cvt_pk_fp8_f32 v216, v227, v228 op_sel:[0,0,1]
	v_mul_f32_e32 v233, 0x43800000, v53
	v_mul_f32_e32 v226, 0x43800000, v57
	v_med3_f32 v233, v233, s62, v154
	v_med3_f32 v226, v226, s62, v154
	v_mul_f32_e32 v227, 0x43800000, v61
	v_mul_f32_e32 v228, 0x43800000, v65
	v_cvt_pk_fp8_f32 v217, v233, v226
	v_med3_f32 v227, v227, s62, v154
	v_med3_f32 v228, v228, s62, v154
	v_cvt_pk_fp8_f32 v217, v227, v228 op_sel:[0,0,1]
	s_nop 1
	ds_write_b128 v231, v[214:217] offset:816
	s_waitcnt lgkmcnt(0)
	s_barrier
	ds_read_b128 v[202:205], v232 offset:0
	ds_read_b128 v[206:209], v232 offset:8704
	ds_read_b128 v[210:213], v232 offset:17408
	ds_read_b128 v[214:217], v232 offset:26112
	s_waitcnt lgkmcnt(3)
	global_store_dwordx4 v235, v[202:205], s[58:59] nt
	s_waitcnt lgkmcnt(2)
	global_store_dwordx4 v236, v[206:209], s[58:59] nt
	s_waitcnt lgkmcnt(1)
	global_store_dwordx4 v237, v[210:213], s[58:59] nt
	s_waitcnt lgkmcnt(0)
	global_store_dwordx4 v230, v[214:217], s[58:59] nt
	s_add_u32 s58, s58, 0x100
	s_addc_u32 s59, s59, 0
	s_waitcnt vmcnt(24)
	v_mul_f32_e32 v233, 0x43800000, v66
	v_mul_f32_e32 v226, 0x43800000, v70
	v_med3_f32 v233, v233, s62, v154
	v_med3_f32 v226, v226, s62, v154
	v_mul_f32_e32 v227, 0x43800000, v74
	v_mul_f32_e32 v228, 0x43800000, v78
	v_cvt_pk_fp8_f32 v202, v233, v226
	v_med3_f32 v227, v227, s62, v154
	v_med3_f32 v228, v228, s62, v154
	v_cvt_pk_fp8_f32 v202, v227, v228 op_sel:[0,0,1]
	s_waitcnt vmcnt(20)
	v_mul_f32_e32 v233, 0x43800000, v82
	v_mul_f32_e32 v226, 0x43800000, v86
	v_med3_f32 v233, v233, s62, v154
	v_med3_f32 v226, v226, s62, v154
	v_mul_f32_e32 v227, 0x43800000, v90
	v_mul_f32_e32 v228, 0x43800000, v94
	v_cvt_pk_fp8_f32 v203, v233, v226
	v_med3_f32 v227, v227, s62, v154
	v_med3_f32 v228, v228, s62, v154
	v_cvt_pk_fp8_f32 v203, v227, v228 op_sel:[0,0,1]
	s_waitcnt vmcnt(16)
	v_mul_f32_e32 v233, 0x43800000, v98
	v_mul_f32_e32 v226, 0x43800000, v102
	v_med3_f32 v233, v233, s62, v154
	v_med3_f32 v226, v226, s62, v154
	v_mul_f32_e32 v227, 0x43800000, v106
	v_mul_f32_e32 v228, 0x43800000, v110
	v_cvt_pk_fp8_f32 v204, v233, v226
	v_med3_f32 v227, v227, s62, v154
	v_med3_f32 v228, v228, s62, v154
	v_cvt_pk_fp8_f32 v204, v227, v228 op_sel:[0,0,1]
	s_waitcnt vmcnt(12)
	v_mul_f32_e32 v233, 0x43800000, v114
	v_mul_f32_e32 v226, 0x43800000, v118
	v_med3_f32 v233, v233, s62, v154
	v_med3_f32 v226, v226, s62, v154
	v_mul_f32_e32 v227, 0x43800000, v122
	v_mul_f32_e32 v228, 0x43800000, v126
	v_cvt_pk_fp8_f32 v205, v233, v226
	v_med3_f32 v227, v227, s62, v154
	v_med3_f32 v228, v228, s62, v154
	v_cvt_pk_fp8_f32 v205, v227, v228 op_sel:[0,0,1]
	s_nop 1
	ds_write_b128 v231, v[202:205] offset:34816
	v_mul_f32_e32 v233, 0x43800000, v67
	v_mul_f32_e32 v226, 0x43800000, v71
	v_med3_f32 v233, v233, s62, v154
	v_med3_f32 v226, v226, s62, v154
	v_mul_f32_e32 v227, 0x43800000, v75
	v_mul_f32_e32 v228, 0x43800000, v79
	v_cvt_pk_fp8_f32 v206, v233, v226
	v_med3_f32 v227, v227, s62, v154
	v_med3_f32 v228, v228, s62, v154
	v_cvt_pk_fp8_f32 v206, v227, v228 op_sel:[0,0,1]
	v_mul_f32_e32 v233, 0x43800000, v83
	v_mul_f32_e32 v226, 0x43800000, v87
	v_med3_f32 v233, v233, s62, v154
	v_med3_f32 v226, v226, s62, v154
	v_mul_f32_e32 v227, 0x43800000, v91
	v_mul_f32_e32 v228, 0x43800000, v95
	v_cvt_pk_fp8_f32 v207, v233, v226
	v_med3_f32 v227, v227, s62, v154
	v_med3_f32 v228, v228, s62, v154
	v_cvt_pk_fp8_f32 v207, v227, v228 op_sel:[0,0,1]
	v_mul_f32_e32 v233, 0x43800000, v99
	v_mul_f32_e32 v226, 0x43800000, v103
	v_med3_f32 v233, v233, s62, v154
	v_med3_f32 v226, v226, s62, v154
	v_mul_f32_e32 v227, 0x43800000, v107
	v_mul_f32_e32 v228, 0x43800000, v111
	v_cvt_pk_fp8_f32 v208, v233, v226
	v_med3_f32 v227, v227, s62, v154
	v_med3_f32 v228, v228, s62, v154
	v_cvt_pk_fp8_f32 v208, v227, v228 op_sel:[0,0,1]
	v_mul_f32_e32 v233, 0x43800000, v115
	v_mul_f32_e32 v226, 0x43800000, v119
	v_med3_f32 v233, v233, s62, v154
	v_med3_f32 v226, v226, s62, v154
	v_mul_f32_e32 v227, 0x43800000, v123
	v_mul_f32_e32 v228, 0x43800000, v127
	v_cvt_pk_fp8_f32 v209, v233, v226
	v_med3_f32 v227, v227, s62, v154
	v_med3_f32 v228, v228, s62, v154
	v_cvt_pk_fp8_f32 v209, v227, v228 op_sel:[0,0,1]
	s_nop 1
	ds_write_b128 v231, v[206:209] offset:35088
	v_mul_f32_e32 v233, 0x43800000, v68
	v_mul_f32_e32 v226, 0x43800000, v72
	v_med3_f32 v233, v233, s62, v154
	v_med3_f32 v226, v226, s62, v154
	v_mul_f32_e32 v227, 0x43800000, v76
	v_mul_f32_e32 v228, 0x43800000, v80
	v_cvt_pk_fp8_f32 v210, v233, v226
	v_med3_f32 v227, v227, s62, v154
	v_med3_f32 v228, v228, s62, v154
	v_cvt_pk_fp8_f32 v210, v227, v228 op_sel:[0,0,1]
	v_mul_f32_e32 v233, 0x43800000, v84
	v_mul_f32_e32 v226, 0x43800000, v88
	v_med3_f32 v233, v233, s62, v154
	v_med3_f32 v226, v226, s62, v154
	v_mul_f32_e32 v227, 0x43800000, v92
	v_mul_f32_e32 v228, 0x43800000, v96
	v_cvt_pk_fp8_f32 v211, v233, v226
	v_med3_f32 v227, v227, s62, v154
	v_med3_f32 v228, v228, s62, v154
	v_cvt_pk_fp8_f32 v211, v227, v228 op_sel:[0,0,1]
	v_mul_f32_e32 v233, 0x43800000, v100
	v_mul_f32_e32 v226, 0x43800000, v104
	v_med3_f32 v233, v233, s62, v154
	v_med3_f32 v226, v226, s62, v154
	v_mul_f32_e32 v227, 0x43800000, v108
	v_mul_f32_e32 v228, 0x43800000, v112
	v_cvt_pk_fp8_f32 v212, v233, v226
	v_med3_f32 v227, v227, s62, v154
	v_med3_f32 v228, v228, s62, v154
	v_cvt_pk_fp8_f32 v212, v227, v228 op_sel:[0,0,1]
	v_mul_f32_e32 v233, 0x43800000, v116
	v_mul_f32_e32 v226, 0x43800000, v120
	v_med3_f32 v233, v233, s62, v154
	v_med3_f32 v226, v226, s62, v154
	v_mul_f32_e32 v227, 0x43800000, v124
	v_mul_f32_e32 v228, 0x43800000, v128
	v_cvt_pk_fp8_f32 v213, v233, v226
	v_med3_f32 v227, v227, s62, v154
	v_med3_f32 v228, v228, s62, v154
	v_cvt_pk_fp8_f32 v213, v227, v228 op_sel:[0,0,1]
	s_nop 1
	ds_write_b128 v231, v[210:213] offset:35360
	v_mul_f32_e32 v233, 0x43800000, v69
	v_mul_f32_e32 v226, 0x43800000, v73
	v_med3_f32 v233, v233, s62, v154
	v_med3_f32 v226, v226, s62, v154
	v_mul_f32_e32 v227, 0x43800000, v77
	v_mul_f32_e32 v228, 0x43800000, v81
	v_cvt_pk_fp8_f32 v214, v233, v226
	v_med3_f32 v227, v227, s62, v154
	v_med3_f32 v228, v228, s62, v154
	v_cvt_pk_fp8_f32 v214, v227, v228 op_sel:[0,0,1]
	v_mul_f32_e32 v233, 0x43800000, v85
	v_mul_f32_e32 v226, 0x43800000, v89
	v_med3_f32 v233, v233, s62, v154
	v_med3_f32 v226, v226, s62, v154
	v_mul_f32_e32 v227, 0x43800000, v93
	v_mul_f32_e32 v228, 0x43800000, v97
	v_cvt_pk_fp8_f32 v215, v233, v226
	v_med3_f32 v227, v227, s62, v154
	v_med3_f32 v228, v228, s62, v154
	v_cvt_pk_fp8_f32 v215, v227, v228 op_sel:[0,0,1]
	v_mul_f32_e32 v233, 0x43800000, v101
	v_mul_f32_e32 v226, 0x43800000, v105
	v_med3_f32 v233, v233, s62, v154
	v_med3_f32 v226, v226, s62, v154
	v_mul_f32_e32 v227, 0x43800000, v109
	v_mul_f32_e32 v228, 0x43800000, v113
	v_cvt_pk_fp8_f32 v216, v233, v226
	v_med3_f32 v227, v227, s62, v154
	v_med3_f32 v228, v228, s62, v154
	v_cvt_pk_fp8_f32 v216, v227, v228 op_sel:[0,0,1]
	v_mul_f32_e32 v233, 0x43800000, v117
	v_mul_f32_e32 v226, 0x43800000, v121
	v_med3_f32 v233, v233, s62, v154
	v_med3_f32 v226, v226, s62, v154
	v_mul_f32_e32 v227, 0x43800000, v125
	v_mul_f32_e32 v228, 0x43800000, v129
	v_cvt_pk_fp8_f32 v217, v233, v226
	v_med3_f32 v227, v227, s62, v154
	v_med3_f32 v228, v228, s62, v154
	v_cvt_pk_fp8_f32 v217, v227, v228 op_sel:[0,0,1]
	s_nop 1
	ds_write_b128 v231, v[214:217] offset:35632
	s_waitcnt lgkmcnt(0)
	s_barrier
	ds_read_b128 v[202:205], v232 offset:34816
	ds_read_b128 v[206:209], v232 offset:43520
	ds_read_b128 v[210:213], v232 offset:52224
	ds_read_b128 v[214:217], v232 offset:60928
	s_waitcnt lgkmcnt(3)
	global_store_dwordx4 v235, v[202:205], s[58:59] nt
	s_waitcnt lgkmcnt(2)
	global_store_dwordx4 v236, v[206:209], s[58:59] nt
	s_waitcnt lgkmcnt(1)
	global_store_dwordx4 v237, v[210:213], s[58:59] nt
	s_waitcnt lgkmcnt(0)
	global_store_dwordx4 v230, v[214:217], s[58:59] nt
	s_add_u32 s58, s58, 0x100
	s_addc_u32 s59, s59, 0
	s_barrier

.LBB0_273:
	v_readlane_b32 s78, v254, 57
	v_readlane_b32 s16, v254, 63
	v_readlane_b32 s66, v254, 61
	s_bitcmp1_b32 s3, 5
	v_readlane_b32 s79, v254, 58
	v_readlane_b32 s64, v254, 53
	v_readlane_b32 s77, v254, 54
	v_readlane_b32 s17, v255, 0
	v_readlane_b32 s67, v254, 62
	v_and_b32_e32 v252, 63, v0
	s_cbranch_scc0 .LBB0_279
	s_barrier
	s_mov_b32 s5, s4
	s_lshr_b32 s4, s5, 5
	s_and_b32 s5, s5, 31
	v_readlane_b32 s0, v254, 6
	v_readlane_b32 s1, v254, 7
	s_lshl_b32 s6, s4, 25
	s_and_b32 s7, s5, 1
	s_lshl_b32 s7, s7, 13
	s_add_u32 s6, s6, s7
	s_lshr_b32 s7, s5, 1
	s_lshl_b32 s7, s7, 9
	s_add_u32 s6, s6, s7
	s_add_u32 s0, s0, s6
	s_addc_u32 s1, s1, 0
	s_lshl_b32 s6, s4, 23
	s_lshl_b32 s7, s5, 18
	s_add_u32 s6, s6, s7
	s_add_u32 s6, s6, 0x40000000
	v_readlane_b32 s2, v254, 57
	v_readlane_b32 s3, v254, 58
	s_add_u32 s2, s2, s6
	s_addc_u32 s3, s3, 0
	s_mov_b32 s6, 0xc3e00000
	v_mov_b32_e32 v1, 0x43e00000
	v_lshrrev_b32_e32 v226, 5, v0
	v_and_b32_e32 v227, 31, v0
	v_lshlrev_b32_e32 v228, 4, v227
	v_lshlrev_b32_e32 v229, 18, v226
	v_add_u32_e32 v250, v229, v228
	v_add_u32_e32 v251, 0x4000, v250
	v_add_u32_e32 v246, 0x8000, v250
	v_add_u32_e32 v247, 0xc000, v250
	v_add_u32_e32 v248, 0x10000, v250
	v_add_u32_e32 v249, 0x14000, v250
	v_add_u32_e32 v242, 0x18000, v250
	v_add_u32_e32 v243, 0x1c000, v250
	v_add_u32_e32 v244, 0x20000, v250
	v_add_u32_e32 v245, 0x24000, v250
	v_add_u32_e32 v238, 0x28000, v250
	v_add_u32_e32 v239, 0x2c000, v250
	v_add_u32_e32 v240, 0x30000, v250
	v_add_u32_e32 v241, 0x34000, v250
	v_add_u32_e32 v234, 0x38000, v250
	v_add_u32_e32 v235, 0x3c000, v250
	v_lshrrev_b32_e32 v194, 4, v0
	v_and_b32_e32 v195, 15, v0
	v_lshlrev_b32_e32 v236, 11, v194
	v_lshl_add_u32 v236, v195, 4, v236
	v_add_u32_e32 v237, 0x10000, v236
	v_add_u32_e32 v230, 0x20000, v236
	v_add_u32_e32 v231, 0x30000, v236
	v_mul_u32_u24_e32 v232, 0x440, v227
	v_lshl_add_u32 v232, v226, 4, v232
	v_mul_u32_u24_e32 v233, 0x110, v194
	v_lshl_add_u32 v233, v195, 4, v233
	global_load_dwordx4 v[2:5], v250, s[0:1] nt
	global_load_dwordx4 v[6:9], v251, s[0:1] nt
	global_load_dwordx4 v[10:13], v246, s[0:1] nt
	global_load_dwordx4 v[14:17], v247, s[0:1] nt
	global_load_dwordx4 v[18:21], v248, s[0:1] nt
	global_load_dwordx4 v[22:25], v249, s[0:1] nt
	global_load_dwordx4 v[26:29], v242, s[0:1] nt
	global_load_dwordx4 v[30:33], v243, s[0:1] nt
	global_load_dwordx4 v[34:37], v244, s[0:1] nt
	global_load_dwordx4 v[38:41], v245, s[0:1] nt
	global_load_dwordx4 v[42:45], v238, s[0:1] nt
	global_load_dwordx4 v[46:49], v239, s[0:1] nt
	global_load_dwordx4 v[50:53], v240, s[0:1] nt
	global_load_dwordx4 v[54:57], v241, s[0:1] nt
	global_load_dwordx4 v[58:61], v234, s[0:1] nt
	global_load_dwordx4 v[62:65], v235, s[0:1] nt
	s_add_u32 s0, s0, 0x400000
	s_addc_u32 s1, s1, 0
	global_load_dwordx4 v[66:69], v250, s[0:1] nt
	global_load_dwordx4 v[70:73], v251, s[0:1] nt
	global_load_dwordx4 v[74:77], v246, s[0:1] nt
	global_load_dwordx4 v[78:81], v247, s[0:1] nt
	global_load_dwordx4 v[82:85], v248, s[0:1] nt
	global_load_dwordx4 v[86:89], v249, s[0:1] nt
	global_load_dwordx4 v[90:93], v242, s[0:1] nt
	global_load_dwordx4 v[94:97], v243, s[0:1] nt
	global_load_dwordx4 v[98:101], v244, s[0:1] nt
	global_load_dwordx4 v[102:105], v245, s[0:1] nt
	global_load_dwordx4 v[106:109], v238, s[0:1] nt
	global_load_dwordx4 v[110:113], v239, s[0:1] nt
	global_load_dwordx4 v[114:117], v240, s[0:1] nt
	global_load_dwordx4 v[118:121], v241, s[0:1] nt
	global_load_dwordx4 v[122:125], v234, s[0:1] nt
	global_load_dwordx4 v[126:129], v235, s[0:1] nt
	s_add_u32 s0, s0, 0x400000
	s_addc_u32 s1, s1, 0
	global_load_dwordx4 v[130:133], v250, s[0:1] nt
	global_load_dwordx4 v[134:137], v251, s[0:1] nt
	global_load_dwordx4 v[138:141], v246, s[0:1] nt
	global_load_dwordx4 v[142:145], v247, s[0:1] nt
	global_load_dwordx4 v[146:149], v248, s[0:1] nt
	global_load_dwordx4 v[150:153], v249, s[0:1] nt
	global_load_dwordx4 v[154:157], v242, s[0:1] nt
	global_load_dwordx4 v[158:161], v243, s[0:1] nt
	global_load_dwordx4 v[162:165], v244, s[0:1] nt
	global_load_dwordx4 v[166:169], v245, s[0:1] nt
	global_load_dwordx4 v[170:173], v238, s[0:1] nt
	global_load_dwordx4 v[174:177], v239, s[0:1] nt
	global_load_dwordx4 v[178:181], v240, s[0:1] nt
	global_load_dwordx4 v[182:185], v241, s[0:1] nt
	global_load_dwordx4 v[186:189], v234, s[0:1] nt
	global_load_dwordx4 v[190:193], v235, s[0:1] nt
	s_add_u32 s0, s0, 0x400000
	s_addc_u32 s1, s1, 0
	s_waitcnt vmcnt(44)
	v_mul_f32_e32 v226, 0x43800000, v2
	v_mul_f32_e32 v227, 0x43800000, v6
	v_med3_f32 v226, v226, s6, v1
	v_med3_f32 v227, v227, s6, v1
	v_mul_f32_e32 v228, 0x43800000, v10
	v_mul_f32_e32 v229, 0x43800000, v14
	v_cvt_pk_fp8_f32 v194, v226, v227
	v_med3_f32 v228, v228, s6, v1
	v_med3_f32 v229, v229, s6, v1
	v_cvt_pk_fp8_f32 v194, v228, v229 op_sel:[0,0,1]
	s_waitcnt vmcnt(40)
	v_mul_f32_e32 v226, 0x43800000, v18
	v_mul_f32_e32 v227, 0x43800000, v22
	v_med3_f32 v226, v226, s6, v1
	v_med3_f32 v227, v227, s6, v1
	v_mul_f32_e32 v228, 0x43800000, v26
	v_mul_f32_e32 v229, 0x43800000, v30
	v_cvt_pk_fp8_f32 v195, v226, v227
	v_med3_f32 v228, v228, s6, v1
	v_med3_f32 v229, v229, s6, v1
	v_cvt_pk_fp8_f32 v195, v228, v229 op_sel:[0,0,1]
	s_waitcnt vmcnt(36)
	v_mul_f32_e32 v226, 0x43800000, v34
	v_mul_f32_e32 v227, 0x43800000, v38
	v_med3_f32 v226, v226, s6, v1
	v_med3_f32 v227, v227, s6, v1
	v_mul_f32_e32 v228, 0x43800000, v42
	v_mul_f32_e32 v229, 0x43800000, v46
	v_cvt_pk_fp8_f32 v196, v226, v227
	v_med3_f32 v228, v228, s6, v1
	v_med3_f32 v229, v229, s6, v1
	v_cvt_pk_fp8_f32 v196, v228, v229 op_sel:[0,0,1]
	s_waitcnt vmcnt(32)
	v_mul_f32_e32 v226, 0x43800000, v50
	v_mul_f32_e32 v227, 0x43800000, v54
	v_med3_f32 v226, v226, s6, v1
	v_med3_f32 v227, v227, s6, v1
	v_mul_f32_e32 v228, 0x43800000, v58
	v_mul_f32_e32 v229, 0x43800000, v62
	v_cvt_pk_fp8_f32 v197, v226, v227
	v_med3_f32 v228, v228, s6, v1
	v_med3_f32 v229, v229, s6, v1
	v_cvt_pk_fp8_f32 v197, v228, v229 op_sel:[0,0,1]
	s_nop 1
	ds_write_b128 v232, v[194:197] offset:0
	v_mul_f32_e32 v226, 0x43800000, v3
	v_mul_f32_e32 v227, 0x43800000, v7
	v_med3_f32 v226, v226, s6, v1
	v_med3_f32 v227, v227, s6, v1
	v_mul_f32_e32 v228, 0x43800000, v11
	v_mul_f32_e32 v229, 0x43800000, v15
	v_cvt_pk_fp8_f32 v198, v226, v227
	v_med3_f32 v228, v228, s6, v1
	v_med3_f32 v229, v229, s6, v1
	v_cvt_pk_fp8_f32 v198, v228, v229 op_sel:[0,0,1]
	v_mul_f32_e32 v226, 0x43800000, v19
	v_mul_f32_e32 v227, 0x43800000, v23
	v_med3_f32 v226, v226, s6, v1
	v_med3_f32 v227, v227, s6, v1
	v_mul_f32_e32 v228, 0x43800000, v27
	v_mul_f32_e32 v229, 0x43800000, v31
	v_cvt_pk_fp8_f32 v199, v226, v227
	v_med3_f32 v228, v228, s6, v1
	v_med3_f32 v229, v229, s6, v1
	v_cvt_pk_fp8_f32 v199, v228, v229 op_sel:[0,0,1]
	v_mul_f32_e32 v226, 0x43800000, v35
	v_mul_f32_e32 v227, 0x43800000, v39
	v_med3_f32 v226, v226, s6, v1
	v_med3_f32 v227, v227, s6, v1
	v_mul_f32_e32 v228, 0x43800000, v43
	v_mul_f32_e32 v229, 0x43800000, v47
	v_cvt_pk_fp8_f32 v200, v226, v227
	v_med3_f32 v228, v228, s6, v1
	v_med3_f32 v229, v229, s6, v1
	v_cvt_pk_fp8_f32 v200, v228, v229 op_sel:[0,0,1]
	v_mul_f32_e32 v226, 0x43800000, v51
	v_mul_f32_e32 v227, 0x43800000, v55
	v_med3_f32 v226, v226, s6, v1
	v_med3_f32 v227, v227, s6, v1
	v_mul_f32_e32 v228, 0x43800000, v59
	v_mul_f32_e32 v229, 0x43800000, v63
	v_cvt_pk_fp8_f32 v201, v226, v227
	v_med3_f32 v228, v228, s6, v1
	v_med3_f32 v229, v229, s6, v1
	v_cvt_pk_fp8_f32 v201, v228, v229 op_sel:[0,0,1]
	s_nop 1
	ds_write_b128 v232, v[198:201] offset:272
	v_mul_f32_e32 v226, 0x43800000, v4
	v_mul_f32_e32 v227, 0x43800000, v8
	v_med3_f32 v226, v226, s6, v1
	v_med3_f32 v227, v227, s6, v1
	v_mul_f32_e32 v228, 0x43800000, v12
	v_mul_f32_e32 v229, 0x43800000, v16
	v_cvt_pk_fp8_f32 v202, v226, v227
	v_med3_f32 v228, v228, s6, v1
	v_med3_f32 v229, v229, s6, v1
	v_cvt_pk_fp8_f32 v202, v228, v229 op_sel:[0,0,1]
	v_mul_f32_e32 v226, 0x43800000, v20
	v_mul_f32_e32 v227, 0x43800000, v24
	v_med3_f32 v226, v226, s6, v1
	v_med3_f32 v227, v227, s6, v1
	v_mul_f32_e32 v228, 0x43800000, v28
	v_mul_f32_e32 v229, 0x43800000, v32
	v_cvt_pk_fp8_f32 v203, v226, v227
	v_med3_f32 v228, v228, s6, v1
	v_med3_f32 v229, v229, s6, v1
	v_cvt_pk_fp8_f32 v203, v228, v229 op_sel:[0,0,1]
	v_mul_f32_e32 v226, 0x43800000, v36
	v_mul_f32_e32 v227, 0x43800000, v40
	v_med3_f32 v226, v226, s6, v1
	v_med3_f32 v227, v227, s6, v1
	v_mul_f32_e32 v228, 0x43800000, v44
	v_mul_f32_e32 v229, 0x43800000, v48
	v_cvt_pk_fp8_f32 v204, v226, v227
	v_med3_f32 v228, v228, s6, v1
	v_med3_f32 v229, v229, s6, v1
	v_cvt_pk_fp8_f32 v204, v228, v229 op_sel:[0,0,1]
	v_mul_f32_e32 v226, 0x43800000, v52
	v_mul_f32_e32 v227, 0x43800000, v56
	v_med3_f32 v226, v226, s6, v1
	v_med3_f32 v227, v227, s6, v1
	v_mul_f32_e32 v228, 0x43800000, v60
	v_mul_f32_e32 v229, 0x43800000, v64
	v_cvt_pk_fp8_f32 v205, v226, v227
	v_med3_f32 v228, v228, s6, v1
	v_med3_f32 v229, v229, s6, v1
	v_cvt_pk_fp8_f32 v205, v228, v229 op_sel:[0,0,1]
	s_nop 1
	ds_write_b128 v232, v[202:205] offset:544
	v_mul_f32_e32 v226, 0x43800000, v5
	v_mul_f32_e32 v227, 0x43800000, v9
	v_med3_f32 v226, v226, s6, v1
	v_med3_f32 v227, v227, s6, v1
	v_mul_f32_e32 v228, 0x43800000, v13
	v_mul_f32_e32 v229, 0x43800000, v17
	v_cvt_pk_fp8_f32 v206, v226, v227
	v_med3_f32 v228, v228, s6, v1
	v_med3_f32 v229, v229, s6, v1
	v_cvt_pk_fp8_f32 v206, v228, v229 op_sel:[0,0,1]
	v_mul_f32_e32 v226, 0x43800000, v21
	v_mul_f32_e32 v227, 0x43800000, v25
	v_med3_f32 v226, v226, s6, v1
	v_med3_f32 v227, v227, s6, v1
	v_mul_f32_e32 v228, 0x43800000, v29
	v_mul_f32_e32 v229, 0x43800000, v33
	v_cvt_pk_fp8_f32 v207, v226, v227
	v_med3_f32 v228, v228, s6, v1
	v_med3_f32 v229, v229, s6, v1
	v_cvt_pk_fp8_f32 v207, v228, v229 op_sel:[0,0,1]
	v_mul_f32_e32 v226, 0x43800000, v37
	v_mul_f32_e32 v227, 0x43800000, v41
	v_med3_f32 v226, v226, s6, v1
	v_med3_f32 v227, v227, s6, v1
	v_mul_f32_e32 v228, 0x43800000, v45
	v_mul_f32_e32 v229, 0x43800000, v49
	v_cvt_pk_fp8_f32 v208, v226, v227
	v_med3_f32 v228, v228, s6, v1
	v_med3_f32 v229, v229, s6, v1
	v_cvt_pk_fp8_f32 v208, v228, v229 op_sel:[0,0,1]
	v_mul_f32_e32 v226, 0x43800000, v53
	v_mul_f32_e32 v227, 0x43800000, v57
	v_med3_f32 v226, v226, s6, v1
	v_med3_f32 v227, v227, s6, v1
	v_mul_f32_e32 v228, 0x43800000, v61
	v_mul_f32_e32 v229, 0x43800000, v65
	v_cvt_pk_fp8_f32 v209, v226, v227
	v_med3_f32 v228, v228, s6, v1
	v_med3_f32 v229, v229, s6, v1
	v_cvt_pk_fp8_f32 v209, v228, v229 op_sel:[0,0,1]
	s_nop 1
	ds_write_b128 v232, v[206:209] offset:816
	s_waitcnt lgkmcnt(0)
	s_barrier
	global_load_dwordx4 v[2:5], v250, s[0:1] nt
	global_load_dwordx4 v[6:9], v251, s[0:1] nt
	global_load_dwordx4 v[10:13], v246, s[0:1] nt
	global_load_dwordx4 v[14:17], v247, s[0:1] nt
	global_load_dwordx4 v[18:21], v248, s[0:1] nt
	global_load_dwordx4 v[22:25], v249, s[0:1] nt
	global_load_dwordx4 v[26:29], v242, s[0:1] nt
	global_load_dwordx4 v[30:33], v243, s[0:1] nt
	global_load_dwordx4 v[34:37], v244, s[0:1] nt
	global_load_dwordx4 v[38:41], v245, s[0:1] nt
	global_load_dwordx4 v[42:45], v238, s[0:1] nt
	global_load_dwordx4 v[46:49], v239, s[0:1] nt
	global_load_dwordx4 v[50:53], v240, s[0:1] nt
	global_load_dwordx4 v[54:57], v241, s[0:1] nt
	global_load_dwordx4 v[58:61], v234, s[0:1] nt
	global_load_dwordx4 v[62:65], v235, s[0:1] nt
	s_add_u32 s0, s0, 0x400000
	s_addc_u32 s1, s1, 0
	ds_read_b128 v[194:197], v233 offset:0
	ds_read_b128 v[198:201], v233 offset:8704
	ds_read_b128 v[202:205], v233 offset:17408
	ds_read_b128 v[206:209], v233 offset:26112
	s_waitcnt lgkmcnt(3)
	global_store_dwordx4 v236, v[194:197], s[2:3] nt
	s_waitcnt lgkmcnt(2)
	global_store_dwordx4 v237, v[198:201], s[2:3] nt
	s_waitcnt lgkmcnt(1)
	global_store_dwordx4 v230, v[202:205], s[2:3] nt
	s_waitcnt lgkmcnt(0)
	global_store_dwordx4 v231, v[206:209], s[2:3] nt
	s_add_u32 s2, s2, 0x100
	s_addc_u32 s3, s3, 0
	s_waitcnt vmcnt(48)
	v_mul_f32_e32 v226, 0x43800000, v66
	v_mul_f32_e32 v227, 0x43800000, v70
	v_med3_f32 v226, v226, s6, v1
	v_med3_f32 v227, v227, s6, v1
	v_mul_f32_e32 v228, 0x43800000, v74
	v_mul_f32_e32 v229, 0x43800000, v78
	v_cvt_pk_fp8_f32 v194, v226, v227
	v_med3_f32 v228, v228, s6, v1
	v_med3_f32 v229, v229, s6, v1
	v_cvt_pk_fp8_f32 v194, v228, v229 op_sel:[0,0,1]
	s_waitcnt vmcnt(44)
	v_mul_f32_e32 v226, 0x43800000, v82
	v_mul_f32_e32 v227, 0x43800000, v86
	v_med3_f32 v226, v226, s6, v1
	v_med3_f32 v227, v227, s6, v1
	v_mul_f32_e32 v228, 0x43800000, v90
	v_mul_f32_e32 v229, 0x43800000, v94
	v_cvt_pk_fp8_f32 v195, v226, v227
	v_med3_f32 v228, v228, s6, v1
	v_med3_f32 v229, v229, s6, v1
	v_cvt_pk_fp8_f32 v195, v228, v229 op_sel:[0,0,1]
	s_waitcnt vmcnt(40)
	v_mul_f32_e32 v226, 0x43800000, v98
	v_mul_f32_e32 v227, 0x43800000, v102
	v_med3_f32 v226, v226, s6, v1
	v_med3_f32 v227, v227, s6, v1
	v_mul_f32_e32 v228, 0x43800000, v106
	v_mul_f32_e32 v229, 0x43800000, v110
	v_cvt_pk_fp8_f32 v196, v226, v227
	v_med3_f32 v228, v228, s6, v1
	v_med3_f32 v229, v229, s6, v1
	v_cvt_pk_fp8_f32 v196, v228, v229 op_sel:[0,0,1]
	s_waitcnt vmcnt(36)
	v_mul_f32_e32 v226, 0x43800000, v114
	v_mul_f32_e32 v227, 0x43800000, v118
	v_med3_f32 v226, v226, s6, v1
	v_med3_f32 v227, v227, s6, v1
	v_mul_f32_e32 v228, 0x43800000, v122
	v_mul_f32_e32 v229, 0x43800000, v126
	v_cvt_pk_fp8_f32 v197, v226, v227
	v_med3_f32 v228, v228, s6, v1
	v_med3_f32 v229, v229, s6, v1
	v_cvt_pk_fp8_f32 v197, v228, v229 op_sel:[0,0,1]
	s_nop 1
	ds_write_b128 v232, v[194:197] offset:34816
	v_mul_f32_e32 v226, 0x43800000, v67
	v_mul_f32_e32 v227, 0x43800000, v71
	v_med3_f32 v226, v226, s6, v1
	v_med3_f32 v227, v227, s6, v1
	v_mul_f32_e32 v228, 0x43800000, v75
	v_mul_f32_e32 v229, 0x43800000, v79
	v_cvt_pk_fp8_f32 v198, v226, v227
	v_med3_f32 v228, v228, s6, v1
	v_med3_f32 v229, v229, s6, v1
	v_cvt_pk_fp8_f32 v198, v228, v229 op_sel:[0,0,1]
	v_mul_f32_e32 v226, 0x43800000, v83
	v_mul_f32_e32 v227, 0x43800000, v87
	v_med3_f32 v226, v226, s6, v1
	v_med3_f32 v227, v227, s6, v1
	v_mul_f32_e32 v228, 0x43800000, v91
	v_mul_f32_e32 v229, 0x43800000, v95
	v_cvt_pk_fp8_f32 v199, v226, v227
	v_med3_f32 v228, v228, s6, v1
	v_med3_f32 v229, v229, s6, v1
	v_cvt_pk_fp8_f32 v199, v228, v229 op_sel:[0,0,1]
	v_mul_f32_e32 v226, 0x43800000, v99
	v_mul_f32_e32 v227, 0x43800000, v103
	v_med3_f32 v226, v226, s6, v1
	v_med3_f32 v227, v227, s6, v1
	v_mul_f32_e32 v228, 0x43800000, v107
	v_mul_f32_e32 v229, 0x43800000, v111
	v_cvt_pk_fp8_f32 v200, v226, v227
	v_med3_f32 v228, v228, s6, v1
	v_med3_f32 v229, v229, s6, v1
	v_cvt_pk_fp8_f32 v200, v228, v229 op_sel:[0,0,1]
	v_mul_f32_e32 v226, 0x43800000, v115
	v_mul_f32_e32 v227, 0x43800000, v119
	v_med3_f32 v226, v226, s6, v1
	v_med3_f32 v227, v227, s6, v1
	v_mul_f32_e32 v228, 0x43800000, v123
	v_mul_f32_e32 v229, 0x43800000, v127
	v_cvt_pk_fp8_f32 v201, v226, v227
	v_med3_f32 v228, v228, s6, v1
	v_med3_f32 v229, v229, s6, v1
	v_cvt_pk_fp8_f32 v201, v228, v229 op_sel:[0,0,1]
	s_nop 1
	ds_write_b128 v232, v[198:201] offset:35088
	v_mul_f32_e32 v226, 0x43800000, v68
	v_mul_f32_e32 v227, 0x43800000, v72
	v_med3_f32 v226, v226, s6, v1
	v_med3_f32 v227, v227, s6, v1
	v_mul_f32_e32 v228, 0x43800000, v76
	v_mul_f32_e32 v229, 0x43800000, v80
	v_cvt_pk_fp8_f32 v202, v226, v227
	v_med3_f32 v228, v228, s6, v1
	v_med3_f32 v229, v229, s6, v1
	v_cvt_pk_fp8_f32 v202, v228, v229 op_sel:[0,0,1]
	v_mul_f32_e32 v226, 0x43800000, v84
	v_mul_f32_e32 v227, 0x43800000, v88
	v_med3_f32 v226, v226, s6, v1
	v_med3_f32 v227, v227, s6, v1
	v_mul_f32_e32 v228, 0x43800000, v92
	v_mul_f32_e32 v229, 0x43800000, v96
	v_cvt_pk_fp8_f32 v203, v226, v227
	v_med3_f32 v228, v228, s6, v1
	v_med3_f32 v229, v229, s6, v1
	v_cvt_pk_fp8_f32 v203, v228, v229 op_sel:[0,0,1]
	v_mul_f32_e32 v226, 0x43800000, v100
	v_mul_f32_e32 v227, 0x43800000, v104
	v_med3_f32 v226, v226, s6, v1
	v_med3_f32 v227, v227, s6, v1
	v_mul_f32_e32 v228, 0x43800000, v108
	v_mul_f32_e32 v229, 0x43800000, v112
	v_cvt_pk_fp8_f32 v204, v226, v227
	v_med3_f32 v228, v228, s6, v1
	v_med3_f32 v229, v229, s6, v1
	v_cvt_pk_fp8_f32 v204, v228, v229 op_sel:[0,0,1]
	v_mul_f32_e32 v226, 0x43800000, v116
	v_mul_f32_e32 v227, 0x43800000, v120
	v_med3_f32 v226, v226, s6, v1
	v_med3_f32 v227, v227, s6, v1
	v_mul_f32_e32 v228, 0x43800000, v124
	v_mul_f32_e32 v229, 0x43800000, v128
	v_cvt_pk_fp8_f32 v205, v226, v227
	v_med3_f32 v228, v228, s6, v1
	v_med3_f32 v229, v229, s6, v1
	v_cvt_pk_fp8_f32 v205, v228, v229 op_sel:[0,0,1]
	s_nop 1
	ds_write_b128 v232, v[202:205] offset:35360
	v_mul_f32_e32 v226, 0x43800000, v69
	v_mul_f32_e32 v227, 0x43800000, v73
	v_med3_f32 v226, v226, s6, v1
	v_med3_f32 v227, v227, s6, v1
	v_mul_f32_e32 v228, 0x43800000, v77
	v_mul_f32_e32 v229, 0x43800000, v81
	v_cvt_pk_fp8_f32 v206, v226, v227
	v_med3_f32 v228, v228, s6, v1
	v_med3_f32 v229, v229, s6, v1
	v_cvt_pk_fp8_f32 v206, v228, v229 op_sel:[0,0,1]
	v_mul_f32_e32 v226, 0x43800000, v85
	v_mul_f32_e32 v227, 0x43800000, v89
	v_med3_f32 v226, v226, s6, v1
	v_med3_f32 v227, v227, s6, v1
	v_mul_f32_e32 v228, 0x43800000, v93
	v_mul_f32_e32 v229, 0x43800000, v97
	v_cvt_pk_fp8_f32 v207, v226, v227
	v_med3_f32 v228, v228, s6, v1
	v_med3_f32 v229, v229, s6, v1
	v_cvt_pk_fp8_f32 v207, v228, v229 op_sel:[0,0,1]
	v_mul_f32_e32 v226, 0x43800000, v101
	v_mul_f32_e32 v227, 0x43800000, v105
	v_med3_f32 v226, v226, s6, v1
	v_med3_f32 v227, v227, s6, v1
	v_mul_f32_e32 v228, 0x43800000, v109
	v_mul_f32_e32 v229, 0x43800000, v113
	v_cvt_pk_fp8_f32 v208, v226, v227
	v_med3_f32 v228, v228, s6, v1
	v_med3_f32 v229, v229, s6, v1
	v_cvt_pk_fp8_f32 v208, v228, v229 op_sel:[0,0,1]
	v_mul_f32_e32 v226, 0x43800000, v117
	v_mul_f32_e32 v227, 0x43800000, v121
	v_med3_f32 v226, v226, s6, v1
	v_med3_f32 v227, v227, s6, v1
	v_mul_f32_e32 v228, 0x43800000, v125
	v_mul_f32_e32 v229, 0x43800000, v129
	v_cvt_pk_fp8_f32 v209, v226, v227
	v_med3_f32 v228, v228, s6, v1
	v_med3_f32 v229, v229, s6, v1
	v_cvt_pk_fp8_f32 v209, v228, v229 op_sel:[0,0,1]
	s_nop 1
	ds_write_b128 v232, v[206:209] offset:35632
	s_waitcnt lgkmcnt(0)
	s_barrier
	global_load_dwordx4 v[66:69], v250, s[0:1] nt
	global_load_dwordx4 v[70:73], v251, s[0:1] nt
	global_load_dwordx4 v[74:77], v246, s[0:1] nt
	global_load_dwordx4 v[78:81], v247, s[0:1] nt
	global_load_dwordx4 v[82:85], v248, s[0:1] nt
	global_load_dwordx4 v[86:89], v249, s[0:1] nt
	global_load_dwordx4 v[90:93], v242, s[0:1] nt
	global_load_dwordx4 v[94:97], v243, s[0:1] nt
	global_load_dwordx4 v[98:101], v244, s[0:1] nt
	global_load_dwordx4 v[102:105], v245, s[0:1] nt
	global_load_dwordx4 v[106:109], v238, s[0:1] nt
	global_load_dwordx4 v[110:113], v239, s[0:1] nt
	global_load_dwordx4 v[114:117], v240, s[0:1] nt
	global_load_dwordx4 v[118:121], v241, s[0:1] nt
	global_load_dwordx4 v[122:125], v234, s[0:1] nt
	global_load_dwordx4 v[126:129], v235, s[0:1] nt
	s_add_u32 s0, s0, 0x400000
	s_addc_u32 s1, s1, 0
	ds_read_b128 v[194:197], v233 offset:34816
	ds_read_b128 v[198:201], v233 offset:43520
	ds_read_b128 v[202:205], v233 offset:52224
	ds_read_b128 v[206:209], v233 offset:60928
	s_waitcnt lgkmcnt(3)
	global_store_dwordx4 v236, v[194:197], s[2:3] nt
	s_waitcnt lgkmcnt(2)
	global_store_dwordx4 v237, v[198:201], s[2:3] nt
	s_waitcnt lgkmcnt(1)
	global_store_dwordx4 v230, v[202:205], s[2:3] nt
	s_waitcnt lgkmcnt(0)
	global_store_dwordx4 v231, v[206:209], s[2:3] nt
	s_add_u32 s2, s2, 0x100
	s_addc_u32 s3, s3, 0
	s_waitcnt vmcnt(52)
	v_mul_f32_e32 v226, 0x43800000, v130
	v_mul_f32_e32 v227, 0x43800000, v134
	v_med3_f32 v226, v226, s6, v1
	v_med3_f32 v227, v227, s6, v1
	v_mul_f32_e32 v228, 0x43800000, v138
	v_mul_f32_e32 v229, 0x43800000, v142
	v_cvt_pk_fp8_f32 v194, v226, v227
	v_med3_f32 v228, v228, s6, v1
	v_med3_f32 v229, v229, s6, v1
	v_cvt_pk_fp8_f32 v194, v228, v229 op_sel:[0,0,1]
	s_waitcnt vmcnt(48)
	v_mul_f32_e32 v226, 0x43800000, v146
	v_mul_f32_e32 v227, 0x43800000, v150
	v_med3_f32 v226, v226, s6, v1
	v_med3_f32 v227, v227, s6, v1
	v_mul_f32_e32 v228, 0x43800000, v154
	v_mul_f32_e32 v229, 0x43800000, v158
	v_cvt_pk_fp8_f32 v195, v226, v227
	v_med3_f32 v228, v228, s6, v1
	v_med3_f32 v229, v229, s6, v1
	v_cvt_pk_fp8_f32 v195, v228, v229 op_sel:[0,0,1]
	s_waitcnt vmcnt(44)
	v_mul_f32_e32 v226, 0x43800000, v162
	v_mul_f32_e32 v227, 0x43800000, v166
	v_med3_f32 v226, v226, s6, v1
	v_med3_f32 v227, v227, s6, v1
	v_mul_f32_e32 v228, 0x43800000, v170
	v_mul_f32_e32 v229, 0x43800000, v174
	v_cvt_pk_fp8_f32 v196, v226, v227
	v_med3_f32 v228, v228, s6, v1
	v_med3_f32 v229, v229, s6, v1
	v_cvt_pk_fp8_f32 v196, v228, v229 op_sel:[0,0,1]
	s_waitcnt vmcnt(40)
	v_mul_f32_e32 v226, 0x43800000, v178
	v_mul_f32_e32 v227, 0x43800000, v182
	v_med3_f32 v226, v226, s6, v1
	v_med3_f32 v227, v227, s6, v1
	v_mul_f32_e32 v228, 0x43800000, v186
	v_mul_f32_e32 v229, 0x43800000, v190
	v_cvt_pk_fp8_f32 v197, v226, v227
	v_med3_f32 v228, v228, s6, v1
	v_med3_f32 v229, v229, s6, v1
	v_cvt_pk_fp8_f32 v197, v228, v229 op_sel:[0,0,1]
	s_nop 1
	ds_write_b128 v232, v[194:197] offset:0
	v_mul_f32_e32 v226, 0x43800000, v131
	v_mul_f32_e32 v227, 0x43800000, v135
	v_med3_f32 v226, v226, s6, v1
	v_med3_f32 v227, v227, s6, v1
	v_mul_f32_e32 v228, 0x43800000, v139
	v_mul_f32_e32 v229, 0x43800000, v143
	v_cvt_pk_fp8_f32 v198, v226, v227
	v_med3_f32 v228, v228, s6, v1
	v_med3_f32 v229, v229, s6, v1
	v_cvt_pk_fp8_f32 v198, v228, v229 op_sel:[0,0,1]
	v_mul_f32_e32 v226, 0x43800000, v147
	v_mul_f32_e32 v227, 0x43800000, v151
	v_med3_f32 v226, v226, s6, v1
	v_med3_f32 v227, v227, s6, v1
	v_mul_f32_e32 v228, 0x43800000, v155
	v_mul_f32_e32 v229, 0x43800000, v159
	v_cvt_pk_fp8_f32 v199, v226, v227
	v_med3_f32 v228, v228, s6, v1
	v_med3_f32 v229, v229, s6, v1
	v_cvt_pk_fp8_f32 v199, v228, v229 op_sel:[0,0,1]
	v_mul_f32_e32 v226, 0x43800000, v163
	v_mul_f32_e32 v227, 0x43800000, v167
	v_med3_f32 v226, v226, s6, v1
	v_med3_f32 v227, v227, s6, v1
	v_mul_f32_e32 v228, 0x43800000, v171
	v_mul_f32_e32 v229, 0x43800000, v175
	v_cvt_pk_fp8_f32 v200, v226, v227
	v_med3_f32 v228, v228, s6, v1
	v_med3_f32 v229, v229, s6, v1
	v_cvt_pk_fp8_f32 v200, v228, v229 op_sel:[0,0,1]
	v_mul_f32_e32 v226, 0x43800000, v179
	v_mul_f32_e32 v227, 0x43800000, v183
	v_med3_f32 v226, v226, s6, v1
	v_med3_f32 v227, v227, s6, v1
	v_mul_f32_e32 v228, 0x43800000, v187
	v_mul_f32_e32 v229, 0x43800000, v191
	v_cvt_pk_fp8_f32 v201, v226, v227
	v_med3_f32 v228, v228, s6, v1
	v_med3_f32 v229, v229, s6, v1
	v_cvt_pk_fp8_f32 v201, v228, v229 op_sel:[0,0,1]
	s_nop 1
	ds_write_b128 v232, v[198:201] offset:272
	v_mul_f32_e32 v226, 0x43800000, v132
	v_mul_f32_e32 v227, 0x43800000, v136
	v_med3_f32 v226, v226, s6, v1
	v_med3_f32 v227, v227, s6, v1
	v_mul_f32_e32 v228, 0x43800000, v140
	v_mul_f32_e32 v229, 0x43800000, v144
	v_cvt_pk_fp8_f32 v202, v226, v227
	v_med3_f32 v228, v228, s6, v1
	v_med3_f32 v229, v229, s6, v1
	v_cvt_pk_fp8_f32 v202, v228, v229 op_sel:[0,0,1]
	v_mul_f32_e32 v226, 0x43800000, v148
	v_mul_f32_e32 v227, 0x43800000, v152
	v_med3_f32 v226, v226, s6, v1
	v_med3_f32 v227, v227, s6, v1
	v_mul_f32_e32 v228, 0x43800000, v156
	v_mul_f32_e32 v229, 0x43800000, v160
	v_cvt_pk_fp8_f32 v203, v226, v227
	v_med3_f32 v228, v228, s6, v1
	v_med3_f32 v229, v229, s6, v1
	v_cvt_pk_fp8_f32 v203, v228, v229 op_sel:[0,0,1]
	v_mul_f32_e32 v226, 0x43800000, v164
	v_mul_f32_e32 v227, 0x43800000, v168
	v_med3_f32 v226, v226, s6, v1
	v_med3_f32 v227, v227, s6, v1
	v_mul_f32_e32 v228, 0x43800000, v172
	v_mul_f32_e32 v229, 0x43800000, v176
	v_cvt_pk_fp8_f32 v204, v226, v227
	v_med3_f32 v228, v228, s6, v1
	v_med3_f32 v229, v229, s6, v1
	v_cvt_pk_fp8_f32 v204, v228, v229 op_sel:[0,0,1]
	v_mul_f32_e32 v226, 0x43800000, v180
	v_mul_f32_e32 v227, 0x43800000, v184
	v_med3_f32 v226, v226, s6, v1
	v_med3_f32 v227, v227, s6, v1
	v_mul_f32_e32 v228, 0x43800000, v188
	v_mul_f32_e32 v229, 0x43800000, v192
	v_cvt_pk_fp8_f32 v205, v226, v227
	v_med3_f32 v228, v228, s6, v1
	v_med3_f32 v229, v229, s6, v1
	v_cvt_pk_fp8_f32 v205, v228, v229 op_sel:[0,0,1]
	s_nop 1
	ds_write_b128 v232, v[202:205] offset:544
	v_mul_f32_e32 v226, 0x43800000, v133
	v_mul_f32_e32 v227, 0x43800000, v137
	v_med3_f32 v226, v226, s6, v1
	v_med3_f32 v227, v227, s6, v1
	v_mul_f32_e32 v228, 0x43800000, v141
	v_mul_f32_e32 v229, 0x43800000, v145
	v_cvt_pk_fp8_f32 v206, v226, v227
	v_med3_f32 v228, v228, s6, v1
	v_med3_f32 v229, v229, s6, v1
	v_cvt_pk_fp8_f32 v206, v228, v229 op_sel:[0,0,1]
	v_mul_f32_e32 v226, 0x43800000, v149
	v_mul_f32_e32 v227, 0x43800000, v153
	v_med3_f32 v226, v226, s6, v1
	v_med3_f32 v227, v227, s6, v1
	v_mul_f32_e32 v228, 0x43800000, v157
	v_mul_f32_e32 v229, 0x43800000, v161
	v_cvt_pk_fp8_f32 v207, v226, v227
	v_med3_f32 v228, v228, s6, v1
	v_med3_f32 v229, v229, s6, v1
	v_cvt_pk_fp8_f32 v207, v228, v229 op_sel:[0,0,1]
	v_mul_f32_e32 v226, 0x43800000, v165
	v_mul_f32_e32 v227, 0x43800000, v169
	v_med3_f32 v226, v226, s6, v1
	v_med3_f32 v227, v227, s6, v1
	v_mul_f32_e32 v228, 0x43800000, v173
	v_mul_f32_e32 v229, 0x43800000, v177
	v_cvt_pk_fp8_f32 v208, v226, v227
	v_med3_f32 v228, v228, s6, v1
	v_med3_f32 v229, v229, s6, v1
	v_cvt_pk_fp8_f32 v208, v228, v229 op_sel:[0,0,1]
	v_mul_f32_e32 v226, 0x43800000, v181
	v_mul_f32_e32 v227, 0x43800000, v185
	v_med3_f32 v226, v226, s6, v1
	v_med3_f32 v227, v227, s6, v1
	v_mul_f32_e32 v228, 0x43800000, v189
	v_mul_f32_e32 v229, 0x43800000, v193
	v_cvt_pk_fp8_f32 v209, v226, v227
	v_med3_f32 v228, v228, s6, v1
	v_med3_f32 v229, v229, s6, v1
	v_cvt_pk_fp8_f32 v209, v228, v229 op_sel:[0,0,1]
	s_nop 1
	ds_write_b128 v232, v[206:209] offset:816
	s_waitcnt lgkmcnt(0)
	s_barrier
	global_load_dwordx4 v[130:133], v250, s[0:1] nt
	global_load_dwordx4 v[134:137], v251, s[0:1] nt
	global_load_dwordx4 v[138:141], v246, s[0:1] nt
	global_load_dwordx4 v[142:145], v247, s[0:1] nt
	global_load_dwordx4 v[146:149], v248, s[0:1] nt
	global_load_dwordx4 v[150:153], v249, s[0:1] nt
	global_load_dwordx4 v[154:157], v242, s[0:1] nt
	global_load_dwordx4 v[158:161], v243, s[0:1] nt
	global_load_dwordx4 v[162:165], v244, s[0:1] nt
	global_load_dwordx4 v[166:169], v245, s[0:1] nt
	global_load_dwordx4 v[170:173], v238, s[0:1] nt
	global_load_dwordx4 v[174:177], v239, s[0:1] nt
	global_load_dwordx4 v[178:181], v240, s[0:1] nt
	global_load_dwordx4 v[182:185], v241, s[0:1] nt
	global_load_dwordx4 v[186:189], v234, s[0:1] nt
	global_load_dwordx4 v[190:193], v235, s[0:1] nt
	s_add_u32 s0, s0, 0x400000
	s_addc_u32 s1, s1, 0
	ds_read_b128 v[194:197], v233 offset:0
	ds_read_b128 v[198:201], v233 offset:8704
	ds_read_b128 v[202:205], v233 offset:17408
	ds_read_b128 v[206:209], v233 offset:26112
	s_waitcnt lgkmcnt(3)
	global_store_dwordx4 v236, v[194:197], s[2:3] nt
	s_waitcnt lgkmcnt(2)
	global_store_dwordx4 v237, v[198:201], s[2:3] nt
	s_waitcnt lgkmcnt(1)
	global_store_dwordx4 v230, v[202:205], s[2:3] nt
	s_waitcnt lgkmcnt(0)
	global_store_dwordx4 v231, v[206:209], s[2:3] nt
	s_add_u32 s2, s2, 0x100
	s_addc_u32 s3, s3, 0
	s_waitcnt vmcnt(56)
	v_mul_f32_e32 v226, 0x43800000, v2
	v_mul_f32_e32 v227, 0x43800000, v6
	v_med3_f32 v226, v226, s6, v1
	v_med3_f32 v227, v227, s6, v1
	v_mul_f32_e32 v228, 0x43800000, v10
	v_mul_f32_e32 v229, 0x43800000, v14
	v_cvt_pk_fp8_f32 v194, v226, v227
	v_med3_f32 v228, v228, s6, v1
	v_med3_f32 v229, v229, s6, v1
	v_cvt_pk_fp8_f32 v194, v228, v229 op_sel:[0,0,1]
	s_waitcnt vmcnt(52)
	v_mul_f32_e32 v226, 0x43800000, v18
	v_mul_f32_e32 v227, 0x43800000, v22
	v_med3_f32 v226, v226, s6, v1
	v_med3_f32 v227, v227, s6, v1
	v_mul_f32_e32 v228, 0x43800000, v26
	v_mul_f32_e32 v229, 0x43800000, v30
	v_cvt_pk_fp8_f32 v195, v226, v227
	v_med3_f32 v228, v228, s6, v1
	v_med3_f32 v229, v229, s6, v1
	v_cvt_pk_fp8_f32 v195, v228, v229 op_sel:[0,0,1]
	s_waitcnt vmcnt(48)
	v_mul_f32_e32 v226, 0x43800000, v34
	v_mul_f32_e32 v227, 0x43800000, v38
	v_med3_f32 v226, v226, s6, v1
	v_med3_f32 v227, v227, s6, v1
	v_mul_f32_e32 v228, 0x43800000, v42
	v_mul_f32_e32 v229, 0x43800000, v46
	v_cvt_pk_fp8_f32 v196, v226, v227
	v_med3_f32 v228, v228, s6, v1
	v_med3_f32 v229, v229, s6, v1
	v_cvt_pk_fp8_f32 v196, v228, v229 op_sel:[0,0,1]
	s_waitcnt vmcnt(44)
	v_mul_f32_e32 v226, 0x43800000, v50
	v_mul_f32_e32 v227, 0x43800000, v54
	v_med3_f32 v226, v226, s6, v1
	v_med3_f32 v227, v227, s6, v1
	v_mul_f32_e32 v228, 0x43800000, v58
	v_mul_f32_e32 v229, 0x43800000, v62
	v_cvt_pk_fp8_f32 v197, v226, v227
	v_med3_f32 v228, v228, s6, v1
	v_med3_f32 v229, v229, s6, v1
	v_cvt_pk_fp8_f32 v197, v228, v229 op_sel:[0,0,1]
	s_nop 1
	ds_write_b128 v232, v[194:197] offset:34816
	v_mul_f32_e32 v226, 0x43800000, v3
	v_mul_f32_e32 v227, 0x43800000, v7
	v_med3_f32 v226, v226, s6, v1
	v_med3_f32 v227, v227, s6, v1
	v_mul_f32_e32 v228, 0x43800000, v11
	v_mul_f32_e32 v229, 0x43800000, v15
	v_cvt_pk_fp8_f32 v198, v226, v227
	v_med3_f32 v228, v228, s6, v1
	v_med3_f32 v229, v229, s6, v1
	v_cvt_pk_fp8_f32 v198, v228, v229 op_sel:[0,0,1]
	v_mul_f32_e32 v226, 0x43800000, v19
	v_mul_f32_e32 v227, 0x43800000, v23
	v_med3_f32 v226, v226, s6, v1
	v_med3_f32 v227, v227, s6, v1
	v_mul_f32_e32 v228, 0x43800000, v27
	v_mul_f32_e32 v229, 0x43800000, v31
	v_cvt_pk_fp8_f32 v199, v226, v227
	v_med3_f32 v228, v228, s6, v1
	v_med3_f32 v229, v229, s6, v1
	v_cvt_pk_fp8_f32 v199, v228, v229 op_sel:[0,0,1]
	v_mul_f32_e32 v226, 0x43800000, v35
	v_mul_f32_e32 v227, 0x43800000, v39
	v_med3_f32 v226, v226, s6, v1
	v_med3_f32 v227, v227, s6, v1
	v_mul_f32_e32 v228, 0x43800000, v43
	v_mul_f32_e32 v229, 0x43800000, v47
	v_cvt_pk_fp8_f32 v200, v226, v227
	v_med3_f32 v228, v228, s6, v1
	v_med3_f32 v229, v229, s6, v1
	v_cvt_pk_fp8_f32 v200, v228, v229 op_sel:[0,0,1]
	v_mul_f32_e32 v226, 0x43800000, v51
	v_mul_f32_e32 v227, 0x43800000, v55
	v_med3_f32 v226, v226, s6, v1
	v_med3_f32 v227, v227, s6, v1
	v_mul_f32_e32 v228, 0x43800000, v59
	v_mul_f32_e32 v229, 0x43800000, v63
	v_cvt_pk_fp8_f32 v201, v226, v227
	v_med3_f32 v228, v228, s6, v1
	v_med3_f32 v229, v229, s6, v1
	v_cvt_pk_fp8_f32 v201, v228, v229 op_sel:[0,0,1]
	s_nop 1
	ds_write_b128 v232, v[198:201] offset:35088
	v_mul_f32_e32 v226, 0x43800000, v4
	v_mul_f32_e32 v227, 0x43800000, v8
	v_med3_f32 v226, v226, s6, v1
	v_med3_f32 v227, v227, s6, v1
	v_mul_f32_e32 v228, 0x43800000, v12
	v_mul_f32_e32 v229, 0x43800000, v16
	v_cvt_pk_fp8_f32 v202, v226, v227
	v_med3_f32 v228, v228, s6, v1
	v_med3_f32 v229, v229, s6, v1
	v_cvt_pk_fp8_f32 v202, v228, v229 op_sel:[0,0,1]
	v_mul_f32_e32 v226, 0x43800000, v20
	v_mul_f32_e32 v227, 0x43800000, v24
	v_med3_f32 v226, v226, s6, v1
	v_med3_f32 v227, v227, s6, v1
	v_mul_f32_e32 v228, 0x43800000, v28
	v_mul_f32_e32 v229, 0x43800000, v32
	v_cvt_pk_fp8_f32 v203, v226, v227
	v_med3_f32 v228, v228, s6, v1
	v_med3_f32 v229, v229, s6, v1
	v_cvt_pk_fp8_f32 v203, v228, v229 op_sel:[0,0,1]
	v_mul_f32_e32 v226, 0x43800000, v36
	v_mul_f32_e32 v227, 0x43800000, v40
	v_med3_f32 v226, v226, s6, v1
	v_med3_f32 v227, v227, s6, v1
	v_mul_f32_e32 v228, 0x43800000, v44
	v_mul_f32_e32 v229, 0x43800000, v48
	v_cvt_pk_fp8_f32 v204, v226, v227
	v_med3_f32 v228, v228, s6, v1
	v_med3_f32 v229, v229, s6, v1
	v_cvt_pk_fp8_f32 v204, v228, v229 op_sel:[0,0,1]
	v_mul_f32_e32 v226, 0x43800000, v52
	v_mul_f32_e32 v227, 0x43800000, v56
	v_med3_f32 v226, v226, s6, v1
	v_med3_f32 v227, v227, s6, v1
	v_mul_f32_e32 v228, 0x43800000, v60
	v_mul_f32_e32 v229, 0x43800000, v64
	v_cvt_pk_fp8_f32 v205, v226, v227
	v_med3_f32 v228, v228, s6, v1
	v_med3_f32 v229, v229, s6, v1
	v_cvt_pk_fp8_f32 v205, v228, v229 op_sel:[0,0,1]
	s_nop 1
	ds_write_b128 v232, v[202:205] offset:35360
	v_mul_f32_e32 v226, 0x43800000, v5
	v_mul_f32_e32 v227, 0x43800000, v9
	v_med3_f32 v226, v226, s6, v1
	v_med3_f32 v227, v227, s6, v1
	v_mul_f32_e32 v228, 0x43800000, v13
	v_mul_f32_e32 v229, 0x43800000, v17
	v_cvt_pk_fp8_f32 v206, v226, v227
	v_med3_f32 v228, v228, s6, v1
	v_med3_f32 v229, v229, s6, v1
	v_cvt_pk_fp8_f32 v206, v228, v229 op_sel:[0,0,1]
	v_mul_f32_e32 v226, 0x43800000, v21
	v_mul_f32_e32 v227, 0x43800000, v25
	v_med3_f32 v226, v226, s6, v1
	v_med3_f32 v227, v227, s6, v1
	v_mul_f32_e32 v228, 0x43800000, v29
	v_mul_f32_e32 v229, 0x43800000, v33
	v_cvt_pk_fp8_f32 v207, v226, v227
	v_med3_f32 v228, v228, s6, v1
	v_med3_f32 v229, v229, s6, v1
	v_cvt_pk_fp8_f32 v207, v228, v229 op_sel:[0,0,1]
	v_mul_f32_e32 v226, 0x43800000, v37
	v_mul_f32_e32 v227, 0x43800000, v41
	v_med3_f32 v226, v226, s6, v1
	v_med3_f32 v227, v227, s6, v1
	v_mul_f32_e32 v228, 0x43800000, v45
	v_mul_f32_e32 v229, 0x43800000, v49
	v_cvt_pk_fp8_f32 v208, v226, v227
	v_med3_f32 v228, v228, s6, v1
	v_med3_f32 v229, v229, s6, v1
	v_cvt_pk_fp8_f32 v208, v228, v229 op_sel:[0,0,1]
	v_mul_f32_e32 v226, 0x43800000, v53
	v_mul_f32_e32 v227, 0x43800000, v57
	v_med3_f32 v226, v226, s6, v1
	v_med3_f32 v227, v227, s6, v1
	v_mul_f32_e32 v228, 0x43800000, v61
	v_mul_f32_e32 v229, 0x43800000, v65
	v_cvt_pk_fp8_f32 v209, v226, v227
	v_med3_f32 v228, v228, s6, v1
	v_med3_f32 v229, v229, s6, v1
	v_cvt_pk_fp8_f32 v209, v228, v229 op_sel:[0,0,1]
	s_nop 1
	ds_write_b128 v232, v[206:209] offset:35632
	s_waitcnt lgkmcnt(0)
	s_barrier
	global_load_dwordx4 v[2:5], v250, s[0:1] nt
	global_load_dwordx4 v[6:9], v251, s[0:1] nt
	global_load_dwordx4 v[10:13], v246, s[0:1] nt
	global_load_dwordx4 v[14:17], v247, s[0:1] nt
	global_load_dwordx4 v[18:21], v248, s[0:1] nt
	global_load_dwordx4 v[22:25], v249, s[0:1] nt
	global_load_dwordx4 v[26:29], v242, s[0:1] nt
	global_load_dwordx4 v[30:33], v243, s[0:1] nt
	global_load_dwordx4 v[34:37], v244, s[0:1] nt
	global_load_dwordx4 v[38:41], v245, s[0:1] nt
	global_load_dwordx4 v[42:45], v238, s[0:1] nt
	global_load_dwordx4 v[46:49], v239, s[0:1] nt
	global_load_dwordx4 v[50:53], v240, s[0:1] nt
	global_load_dwordx4 v[54:57], v241, s[0:1] nt
	global_load_dwordx4 v[58:61], v234, s[0:1] nt
	global_load_dwordx4 v[62:65], v235, s[0:1] nt
	s_add_u32 s0, s0, 0x400000
	s_addc_u32 s1, s1, 0
	ds_read_b128 v[194:197], v233 offset:34816
	ds_read_b128 v[198:201], v233 offset:43520
	ds_read_b128 v[202:205], v233 offset:52224
	ds_read_b128 v[206:209], v233 offset:60928
	s_waitcnt lgkmcnt(3)
	global_store_dwordx4 v236, v[194:197], s[2:3] nt
	s_waitcnt lgkmcnt(2)
	global_store_dwordx4 v237, v[198:201], s[2:3] nt
	s_waitcnt lgkmcnt(1)
	global_store_dwordx4 v230, v[202:205], s[2:3] nt
	s_waitcnt lgkmcnt(0)
	global_store_dwordx4 v231, v[206:209], s[2:3] nt
	s_add_u32 s2, s2, 0x100
	s_addc_u32 s3, s3, 0
	s_waitcnt vmcnt(56)
	v_mul_f32_e32 v226, 0x43800000, v66
	v_mul_f32_e32 v227, 0x43800000, v70
	v_med3_f32 v226, v226, s6, v1
	v_med3_f32 v227, v227, s6, v1
	v_mul_f32_e32 v228, 0x43800000, v74
	v_mul_f32_e32 v229, 0x43800000, v78
	v_cvt_pk_fp8_f32 v194, v226, v227
	v_med3_f32 v228, v228, s6, v1
	v_med3_f32 v229, v229, s6, v1
	v_cvt_pk_fp8_f32 v194, v228, v229 op_sel:[0,0,1]
	s_waitcnt vmcnt(52)
	v_mul_f32_e32 v226, 0x43800000, v82
	v_mul_f32_e32 v227, 0x43800000, v86
	v_med3_f32 v226, v226, s6, v1
	v_med3_f32 v227, v227, s6, v1
	v_mul_f32_e32 v228, 0x43800000, v90
	v_mul_f32_e32 v229, 0x43800000, v94
	v_cvt_pk_fp8_f32 v195, v226, v227
	v_med3_f32 v228, v228, s6, v1
	v_med3_f32 v229, v229, s6, v1
	v_cvt_pk_fp8_f32 v195, v228, v229 op_sel:[0,0,1]
	s_waitcnt vmcnt(48)
	v_mul_f32_e32 v226, 0x43800000, v98
	v_mul_f32_e32 v227, 0x43800000, v102
	v_med3_f32 v226, v226, s6, v1
	v_med3_f32 v227, v227, s6, v1
	v_mul_f32_e32 v228, 0x43800000, v106
	v_mul_f32_e32 v229, 0x43800000, v110
	v_cvt_pk_fp8_f32 v196, v226, v227
	v_med3_f32 v228, v228, s6, v1
	v_med3_f32 v229, v229, s6, v1
	v_cvt_pk_fp8_f32 v196, v228, v229 op_sel:[0,0,1]
	s_waitcnt vmcnt(44)
	v_mul_f32_e32 v226, 0x43800000, v114
	v_mul_f32_e32 v227, 0x43800000, v118
	v_med3_f32 v226, v226, s6, v1
	v_med3_f32 v227, v227, s6, v1
	v_mul_f32_e32 v228, 0x43800000, v122
	v_mul_f32_e32 v229, 0x43800000, v126
	v_cvt_pk_fp8_f32 v197, v226, v227
	v_med3_f32 v228, v228, s6, v1
	v_med3_f32 v229, v229, s6, v1
	v_cvt_pk_fp8_f32 v197, v228, v229 op_sel:[0,0,1]
	s_nop 1
	ds_write_b128 v232, v[194:197] offset:0
	v_mul_f32_e32 v226, 0x43800000, v67
	v_mul_f32_e32 v227, 0x43800000, v71
	v_med3_f32 v226, v226, s6, v1
	v_med3_f32 v227, v227, s6, v1
	v_mul_f32_e32 v228, 0x43800000, v75
	v_mul_f32_e32 v229, 0x43800000, v79
	v_cvt_pk_fp8_f32 v198, v226, v227
	v_med3_f32 v228, v228, s6, v1
	v_med3_f32 v229, v229, s6, v1
	v_cvt_pk_fp8_f32 v198, v228, v229 op_sel:[0,0,1]
	v_mul_f32_e32 v226, 0x43800000, v83
	v_mul_f32_e32 v227, 0x43800000, v87
	v_med3_f32 v226, v226, s6, v1
	v_med3_f32 v227, v227, s6, v1
	v_mul_f32_e32 v228, 0x43800000, v91
	v_mul_f32_e32 v229, 0x43800000, v95
	v_cvt_pk_fp8_f32 v199, v226, v227
	v_med3_f32 v228, v228, s6, v1
	v_med3_f32 v229, v229, s6, v1
	v_cvt_pk_fp8_f32 v199, v228, v229 op_sel:[0,0,1]
	v_mul_f32_e32 v226, 0x43800000, v99
	v_mul_f32_e32 v227, 0x43800000, v103
	v_med3_f32 v226, v226, s6, v1
	v_med3_f32 v227, v227, s6, v1
	v_mul_f32_e32 v228, 0x43800000, v107
	v_mul_f32_e32 v229, 0x43800000, v111
	v_cvt_pk_fp8_f32 v200, v226, v227
	v_med3_f32 v228, v228, s6, v1
	v_med3_f32 v229, v229, s6, v1
	v_cvt_pk_fp8_f32 v200, v228, v229 op_sel:[0,0,1]
	v_mul_f32_e32 v226, 0x43800000, v115
	v_mul_f32_e32 v227, 0x43800000, v119
	v_med3_f32 v226, v226, s6, v1
	v_med3_f32 v227, v227, s6, v1
	v_mul_f32_e32 v228, 0x43800000, v123
	v_mul_f32_e32 v229, 0x43800000, v127
	v_cvt_pk_fp8_f32 v201, v226, v227
	v_med3_f32 v228, v228, s6, v1
	v_med3_f32 v229, v229, s6, v1
	v_cvt_pk_fp8_f32 v201, v228, v229 op_sel:[0,0,1]
	s_nop 1
	ds_write_b128 v232, v[198:201] offset:272
	v_mul_f32_e32 v226, 0x43800000, v68
	v_mul_f32_e32 v227, 0x43800000, v72
	v_med3_f32 v226, v226, s6, v1
	v_med3_f32 v227, v227, s6, v1
	v_mul_f32_e32 v228, 0x43800000, v76
	v_mul_f32_e32 v229, 0x43800000, v80
	v_cvt_pk_fp8_f32 v202, v226, v227
	v_med3_f32 v228, v228, s6, v1
	v_med3_f32 v229, v229, s6, v1
	v_cvt_pk_fp8_f32 v202, v228, v229 op_sel:[0,0,1]
	v_mul_f32_e32 v226, 0x43800000, v84
	v_mul_f32_e32 v227, 0x43800000, v88
	v_med3_f32 v226, v226, s6, v1
	v_med3_f32 v227, v227, s6, v1
	v_mul_f32_e32 v228, 0x43800000, v92
	v_mul_f32_e32 v229, 0x43800000, v96
	v_cvt_pk_fp8_f32 v203, v226, v227
	v_med3_f32 v228, v228, s6, v1
	v_med3_f32 v229, v229, s6, v1
	v_cvt_pk_fp8_f32 v203, v228, v229 op_sel:[0,0,1]
	v_mul_f32_e32 v226, 0x43800000, v100
	v_mul_f32_e32 v227, 0x43800000, v104
	v_med3_f32 v226, v226, s6, v1
	v_med3_f32 v227, v227, s6, v1
	v_mul_f32_e32 v228, 0x43800000, v108
	v_mul_f32_e32 v229, 0x43800000, v112
	v_cvt_pk_fp8_f32 v204, v226, v227
	v_med3_f32 v228, v228, s6, v1
	v_med3_f32 v229, v229, s6, v1
	v_cvt_pk_fp8_f32 v204, v228, v229 op_sel:[0,0,1]
	v_mul_f32_e32 v226, 0x43800000, v116
	v_mul_f32_e32 v227, 0x43800000, v120
	v_med3_f32 v226, v226, s6, v1
	v_med3_f32 v227, v227, s6, v1
	v_mul_f32_e32 v228, 0x43800000, v124
	v_mul_f32_e32 v229, 0x43800000, v128
	v_cvt_pk_fp8_f32 v205, v226, v227
	v_med3_f32 v228, v228, s6, v1
	v_med3_f32 v229, v229, s6, v1
	v_cvt_pk_fp8_f32 v205, v228, v229 op_sel:[0,0,1]
	s_nop 1
	ds_write_b128 v232, v[202:205] offset:544
	v_mul_f32_e32 v226, 0x43800000, v69
	v_mul_f32_e32 v227, 0x43800000, v73
	v_med3_f32 v226, v226, s6, v1
	v_med3_f32 v227, v227, s6, v1
	v_mul_f32_e32 v228, 0x43800000, v77
	v_mul_f32_e32 v229, 0x43800000, v81
	v_cvt_pk_fp8_f32 v206, v226, v227
	v_med3_f32 v228, v228, s6, v1
	v_med3_f32 v229, v229, s6, v1
	v_cvt_pk_fp8_f32 v206, v228, v229 op_sel:[0,0,1]
	v_mul_f32_e32 v226, 0x43800000, v85
	v_mul_f32_e32 v227, 0x43800000, v89
	v_med3_f32 v226, v226, s6, v1
	v_med3_f32 v227, v227, s6, v1
	v_mul_f32_e32 v228, 0x43800000, v93
	v_mul_f32_e32 v229, 0x43800000, v97
	v_cvt_pk_fp8_f32 v207, v226, v227
	v_med3_f32 v228, v228, s6, v1
	v_med3_f32 v229, v229, s6, v1
	v_cvt_pk_fp8_f32 v207, v228, v229 op_sel:[0,0,1]
	v_mul_f32_e32 v226, 0x43800000, v101
	v_mul_f32_e32 v227, 0x43800000, v105
	v_med3_f32 v226, v226, s6, v1
	v_med3_f32 v227, v227, s6, v1
	v_mul_f32_e32 v228, 0x43800000, v109
	v_mul_f32_e32 v229, 0x43800000, v113
	v_cvt_pk_fp8_f32 v208, v226, v227
	v_med3_f32 v228, v228, s6, v1
	v_med3_f32 v229, v229, s6, v1
	v_cvt_pk_fp8_f32 v208, v228, v229 op_sel:[0,0,1]
	v_mul_f32_e32 v226, 0x43800000, v117
	v_mul_f32_e32 v227, 0x43800000, v121
	v_med3_f32 v226, v226, s6, v1
	v_med3_f32 v227, v227, s6, v1
	v_mul_f32_e32 v228, 0x43800000, v125
	v_mul_f32_e32 v229, 0x43800000, v129
	v_cvt_pk_fp8_f32 v209, v226, v227
	v_med3_f32 v228, v228, s6, v1
	v_med3_f32 v229, v229, s6, v1
	v_cvt_pk_fp8_f32 v209, v228, v229 op_sel:[0,0,1]
	s_nop 1
	ds_write_b128 v232, v[206:209] offset:816
	s_waitcnt lgkmcnt(0)
	s_barrier
	global_load_dwordx4 v[66:69], v250, s[0:1] nt
	global_load_dwordx4 v[70:73], v251, s[0:1] nt
	global_load_dwordx4 v[74:77], v246, s[0:1] nt
	global_load_dwordx4 v[78:81], v247, s[0:1] nt
	global_load_dwordx4 v[82:85], v248, s[0:1] nt
	global_load_dwordx4 v[86:89], v249, s[0:1] nt
	global_load_dwordx4 v[90:93], v242, s[0:1] nt
	global_load_dwordx4 v[94:97], v243, s[0:1] nt
	global_load_dwordx4 v[98:101], v244, s[0:1] nt
	global_load_dwordx4 v[102:105], v245, s[0:1] nt
	global_load_dwordx4 v[106:109], v238, s[0:1] nt
	global_load_dwordx4 v[110:113], v239, s[0:1] nt
	global_load_dwordx4 v[114:117], v240, s[0:1] nt
	global_load_dwordx4 v[118:121], v241, s[0:1] nt
	global_load_dwordx4 v[122:125], v234, s[0:1] nt
	global_load_dwordx4 v[126:129], v235, s[0:1] nt
	s_add_u32 s0, s0, 0x400000
	s_addc_u32 s1, s1, 0
	ds_read_b128 v[194:197], v233 offset:0
	ds_read_b128 v[198:201], v233 offset:8704
	ds_read_b128 v[202:205], v233 offset:17408
	ds_read_b128 v[206:209], v233 offset:26112
	s_waitcnt lgkmcnt(3)
	global_store_dwordx4 v236, v[194:197], s[2:3] nt
	s_waitcnt lgkmcnt(2)
	global_store_dwordx4 v237, v[198:201], s[2:3] nt
	s_waitcnt lgkmcnt(1)
	global_store_dwordx4 v230, v[202:205], s[2:3] nt
	s_waitcnt lgkmcnt(0)
	global_store_dwordx4 v231, v[206:209], s[2:3] nt
	s_add_u32 s2, s2, 0x100
	s_addc_u32 s3, s3, 0
	s_waitcnt vmcnt(56)
	v_mul_f32_e32 v226, 0x43800000, v130
	v_mul_f32_e32 v227, 0x43800000, v134
	v_med3_f32 v226, v226, s6, v1
	v_med3_f32 v227, v227, s6, v1
	v_mul_f32_e32 v228, 0x43800000, v138
	v_mul_f32_e32 v229, 0x43800000, v142
	v_cvt_pk_fp8_f32 v194, v226, v227
	v_med3_f32 v228, v228, s6, v1
	v_med3_f32 v229, v229, s6, v1
	v_cvt_pk_fp8_f32 v194, v228, v229 op_sel:[0,0,1]
	s_waitcnt vmcnt(52)
	v_mul_f32_e32 v226, 0x43800000, v146
	v_mul_f32_e32 v227, 0x43800000, v150
	v_med3_f32 v226, v226, s6, v1
	v_med3_f32 v227, v227, s6, v1
	v_mul_f32_e32 v228, 0x43800000, v154
	v_mul_f32_e32 v229, 0x43800000, v158
	v_cvt_pk_fp8_f32 v195, v226, v227
	v_med3_f32 v228, v228, s6, v1
	v_med3_f32 v229, v229, s6, v1
	v_cvt_pk_fp8_f32 v195, v228, v229 op_sel:[0,0,1]
	s_waitcnt vmcnt(48)
	v_mul_f32_e32 v226, 0x43800000, v162
	v_mul_f32_e32 v227, 0x43800000, v166
	v_med3_f32 v226, v226, s6, v1
	v_med3_f32 v227, v227, s6, v1
	v_mul_f32_e32 v228, 0x43800000, v170
	v_mul_f32_e32 v229, 0x43800000, v174
	v_cvt_pk_fp8_f32 v196, v226, v227
	v_med3_f32 v228, v228, s6, v1
	v_med3_f32 v229, v229, s6, v1
	v_cvt_pk_fp8_f32 v196, v228, v229 op_sel:[0,0,1]
	s_waitcnt vmcnt(44)
	v_mul_f32_e32 v226, 0x43800000, v178
	v_mul_f32_e32 v227, 0x43800000, v182
	v_med3_f32 v226, v226, s6, v1
	v_med3_f32 v227, v227, s6, v1
	v_mul_f32_e32 v228, 0x43800000, v186
	v_mul_f32_e32 v229, 0x43800000, v190
	v_cvt_pk_fp8_f32 v197, v226, v227
	v_med3_f32 v228, v228, s6, v1
	v_med3_f32 v229, v229, s6, v1
	v_cvt_pk_fp8_f32 v197, v228, v229 op_sel:[0,0,1]
	s_nop 1
	ds_write_b128 v232, v[194:197] offset:34816
	v_mul_f32_e32 v226, 0x43800000, v131
	v_mul_f32_e32 v227, 0x43800000, v135
	v_med3_f32 v226, v226, s6, v1
	v_med3_f32 v227, v227, s6, v1
	v_mul_f32_e32 v228, 0x43800000, v139
	v_mul_f32_e32 v229, 0x43800000, v143
	v_cvt_pk_fp8_f32 v198, v226, v227
	v_med3_f32 v228, v228, s6, v1
	v_med3_f32 v229, v229, s6, v1
	v_cvt_pk_fp8_f32 v198, v228, v229 op_sel:[0,0,1]
	v_mul_f32_e32 v226, 0x43800000, v147
	v_mul_f32_e32 v227, 0x43800000, v151
	v_med3_f32 v226, v226, s6, v1
	v_med3_f32 v227, v227, s6, v1
	v_mul_f32_e32 v228, 0x43800000, v155
	v_mul_f32_e32 v229, 0x43800000, v159
	v_cvt_pk_fp8_f32 v199, v226, v227
	v_med3_f32 v228, v228, s6, v1
	v_med3_f32 v229, v229, s6, v1
	v_cvt_pk_fp8_f32 v199, v228, v229 op_sel:[0,0,1]
	v_mul_f32_e32 v226, 0x43800000, v163
	v_mul_f32_e32 v227, 0x43800000, v167
	v_med3_f32 v226, v226, s6, v1
	v_med3_f32 v227, v227, s6, v1
	v_mul_f32_e32 v228, 0x43800000, v171
	v_mul_f32_e32 v229, 0x43800000, v175
	v_cvt_pk_fp8_f32 v200, v226, v227
	v_med3_f32 v228, v228, s6, v1
	v_med3_f32 v229, v229, s6, v1
	v_cvt_pk_fp8_f32 v200, v228, v229 op_sel:[0,0,1]
	v_mul_f32_e32 v226, 0x43800000, v179
	v_mul_f32_e32 v227, 0x43800000, v183
	v_med3_f32 v226, v226, s6, v1
	v_med3_f32 v227, v227, s6, v1
	v_mul_f32_e32 v228, 0x43800000, v187
	v_mul_f32_e32 v229, 0x43800000, v191
	v_cvt_pk_fp8_f32 v201, v226, v227
	v_med3_f32 v228, v228, s6, v1
	v_med3_f32 v229, v229, s6, v1
	v_cvt_pk_fp8_f32 v201, v228, v229 op_sel:[0,0,1]
	s_nop 1
	ds_write_b128 v232, v[198:201] offset:35088
	v_mul_f32_e32 v226, 0x43800000, v132
	v_mul_f32_e32 v227, 0x43800000, v136
	v_med3_f32 v226, v226, s6, v1
	v_med3_f32 v227, v227, s6, v1
	v_mul_f32_e32 v228, 0x43800000, v140
	v_mul_f32_e32 v229, 0x43800000, v144
	v_cvt_pk_fp8_f32 v202, v226, v227
	v_med3_f32 v228, v228, s6, v1
	v_med3_f32 v229, v229, s6, v1
	v_cvt_pk_fp8_f32 v202, v228, v229 op_sel:[0,0,1]
	v_mul_f32_e32 v226, 0x43800000, v148
	v_mul_f32_e32 v227, 0x43800000, v152
	v_med3_f32 v226, v226, s6, v1
	v_med3_f32 v227, v227, s6, v1
	v_mul_f32_e32 v228, 0x43800000, v156
	v_mul_f32_e32 v229, 0x43800000, v160
	v_cvt_pk_fp8_f32 v203, v226, v227
	v_med3_f32 v228, v228, s6, v1
	v_med3_f32 v229, v229, s6, v1
	v_cvt_pk_fp8_f32 v203, v228, v229 op_sel:[0,0,1]
	v_mul_f32_e32 v226, 0x43800000, v164
	v_mul_f32_e32 v227, 0x43800000, v168
	v_med3_f32 v226, v226, s6, v1
	v_med3_f32 v227, v227, s6, v1
	v_mul_f32_e32 v228, 0x43800000, v172
	v_mul_f32_e32 v229, 0x43800000, v176
	v_cvt_pk_fp8_f32 v204, v226, v227
	v_med3_f32 v228, v228, s6, v1
	v_med3_f32 v229, v229, s6, v1
	v_cvt_pk_fp8_f32 v204, v228, v229 op_sel:[0,0,1]
	v_mul_f32_e32 v226, 0x43800000, v180
	v_mul_f32_e32 v227, 0x43800000, v184
	v_med3_f32 v226, v226, s6, v1
	v_med3_f32 v227, v227, s6, v1
	v_mul_f32_e32 v228, 0x43800000, v188
	v_mul_f32_e32 v229, 0x43800000, v192
	v_cvt_pk_fp8_f32 v205, v226, v227
	v_med3_f32 v228, v228, s6, v1
	v_med3_f32 v229, v229, s6, v1
	v_cvt_pk_fp8_f32 v205, v228, v229 op_sel:[0,0,1]
	s_nop 1
	ds_write_b128 v232, v[202:205] offset:35360
	v_mul_f32_e32 v226, 0x43800000, v133
	v_mul_f32_e32 v227, 0x43800000, v137
	v_med3_f32 v226, v226, s6, v1
	v_med3_f32 v227, v227, s6, v1
	v_mul_f32_e32 v228, 0x43800000, v141
	v_mul_f32_e32 v229, 0x43800000, v145
	v_cvt_pk_fp8_f32 v206, v226, v227
	v_med3_f32 v228, v228, s6, v1
	v_med3_f32 v229, v229, s6, v1
	v_cvt_pk_fp8_f32 v206, v228, v229 op_sel:[0,0,1]
	v_mul_f32_e32 v226, 0x43800000, v149
	v_mul_f32_e32 v227, 0x43800000, v153
	v_med3_f32 v226, v226, s6, v1
	v_med3_f32 v227, v227, s6, v1
	v_mul_f32_e32 v228, 0x43800000, v157
	v_mul_f32_e32 v229, 0x43800000, v161
	v_cvt_pk_fp8_f32 v207, v226, v227
	v_med3_f32 v228, v228, s6, v1
	v_med3_f32 v229, v229, s6, v1
	v_cvt_pk_fp8_f32 v207, v228, v229 op_sel:[0,0,1]
	v_mul_f32_e32 v226, 0x43800000, v165
	v_mul_f32_e32 v227, 0x43800000, v169
	v_med3_f32 v226, v226, s6, v1
	v_med3_f32 v227, v227, s6, v1
	v_mul_f32_e32 v228, 0x43800000, v173
	v_mul_f32_e32 v229, 0x43800000, v177
	v_cvt_pk_fp8_f32 v208, v226, v227
	v_med3_f32 v228, v228, s6, v1
	v_med3_f32 v229, v229, s6, v1
	v_cvt_pk_fp8_f32 v208, v228, v229 op_sel:[0,0,1]
	v_mul_f32_e32 v226, 0x43800000, v181
	v_mul_f32_e32 v227, 0x43800000, v185
	v_med3_f32 v226, v226, s6, v1
	v_med3_f32 v227, v227, s6, v1
	v_mul_f32_e32 v228, 0x43800000, v189
	v_mul_f32_e32 v229, 0x43800000, v193
	v_cvt_pk_fp8_f32 v209, v226, v227
	v_med3_f32 v228, v228, s6, v1
	v_med3_f32 v229, v229, s6, v1
	v_cvt_pk_fp8_f32 v209, v228, v229 op_sel:[0,0,1]
	s_nop 1
	ds_write_b128 v232, v[206:209] offset:35632
	s_waitcnt lgkmcnt(0)
	s_barrier
	ds_read_b128 v[194:197], v233 offset:34816
	ds_read_b128 v[198:201], v233 offset:43520
	ds_read_b128 v[202:205], v233 offset:52224
	ds_read_b128 v[206:209], v233 offset:60928
	s_waitcnt lgkmcnt(3)
	global_store_dwordx4 v236, v[194:197], s[2:3] nt
	s_waitcnt lgkmcnt(2)
	global_store_dwordx4 v237, v[198:201], s[2:3] nt
	s_waitcnt lgkmcnt(1)
	global_store_dwordx4 v230, v[202:205], s[2:3] nt
	s_waitcnt lgkmcnt(0)
	global_store_dwordx4 v231, v[206:209], s[2:3] nt
	s_add_u32 s2, s2, 0x100
	s_addc_u32 s3, s3, 0
	s_waitcnt vmcnt(40)
	v_mul_f32_e32 v226, 0x43800000, v2
	v_mul_f32_e32 v227, 0x43800000, v6
	v_med3_f32 v226, v226, s6, v1
	v_med3_f32 v227, v227, s6, v1
	v_mul_f32_e32 v228, 0x43800000, v10
	v_mul_f32_e32 v229, 0x43800000, v14
	v_cvt_pk_fp8_f32 v194, v226, v227
	v_med3_f32 v228, v228, s6, v1
	v_med3_f32 v229, v229, s6, v1
	v_cvt_pk_fp8_f32 v194, v228, v229 op_sel:[0,0,1]
	s_waitcnt vmcnt(36)
	v_mul_f32_e32 v226, 0x43800000, v18
	v_mul_f32_e32 v227, 0x43800000, v22
	v_med3_f32 v226, v226, s6, v1
	v_med3_f32 v227, v227, s6, v1
	v_mul_f32_e32 v228, 0x43800000, v26
	v_mul_f32_e32 v229, 0x43800000, v30
	v_cvt_pk_fp8_f32 v195, v226, v227
	v_med3_f32 v228, v228, s6, v1
	v_med3_f32 v229, v229, s6, v1
	v_cvt_pk_fp8_f32 v195, v228, v229 op_sel:[0,0,1]
	s_waitcnt vmcnt(32)
	v_mul_f32_e32 v226, 0x43800000, v34
	v_mul_f32_e32 v227, 0x43800000, v38
	v_med3_f32 v226, v226, s6, v1
	v_med3_f32 v227, v227, s6, v1
	v_mul_f32_e32 v228, 0x43800000, v42
	v_mul_f32_e32 v229, 0x43800000, v46
	v_cvt_pk_fp8_f32 v196, v226, v227
	v_med3_f32 v228, v228, s6, v1
	v_med3_f32 v229, v229, s6, v1
	v_cvt_pk_fp8_f32 v196, v228, v229 op_sel:[0,0,1]
	s_waitcnt vmcnt(28)
	v_mul_f32_e32 v226, 0x43800000, v50
	v_mul_f32_e32 v227, 0x43800000, v54
	v_med3_f32 v226, v226, s6, v1
	v_med3_f32 v227, v227, s6, v1
	v_mul_f32_e32 v228, 0x43800000, v58
	v_mul_f32_e32 v229, 0x43800000, v62
	v_cvt_pk_fp8_f32 v197, v226, v227
	v_med3_f32 v228, v228, s6, v1
	v_med3_f32 v229, v229, s6, v1
	v_cvt_pk_fp8_f32 v197, v228, v229 op_sel:[0,0,1]
	s_nop 1
	ds_write_b128 v232, v[194:197] offset:0
	v_mul_f32_e32 v226, 0x43800000, v3
	v_mul_f32_e32 v227, 0x43800000, v7
	v_med3_f32 v226, v226, s6, v1
	v_med3_f32 v227, v227, s6, v1
	v_mul_f32_e32 v228, 0x43800000, v11
	v_mul_f32_e32 v229, 0x43800000, v15
	v_cvt_pk_fp8_f32 v198, v226, v227
	v_med3_f32 v228, v228, s6, v1
	v_med3_f32 v229, v229, s6, v1
	v_cvt_pk_fp8_f32 v198, v228, v229 op_sel:[0,0,1]
	v_mul_f32_e32 v226, 0x43800000, v19
	v_mul_f32_e32 v227, 0x43800000, v23
	v_med3_f32 v226, v226, s6, v1
	v_med3_f32 v227, v227, s6, v1
	v_mul_f32_e32 v228, 0x43800000, v27
	v_mul_f32_e32 v229, 0x43800000, v31
	v_cvt_pk_fp8_f32 v199, v226, v227
	v_med3_f32 v228, v228, s6, v1
	v_med3_f32 v229, v229, s6, v1
	v_cvt_pk_fp8_f32 v199, v228, v229 op_sel:[0,0,1]
	v_mul_f32_e32 v226, 0x43800000, v35
	v_mul_f32_e32 v227, 0x43800000, v39
	v_med3_f32 v226, v226, s6, v1
	v_med3_f32 v227, v227, s6, v1
	v_mul_f32_e32 v228, 0x43800000, v43
	v_mul_f32_e32 v229, 0x43800000, v47
	v_cvt_pk_fp8_f32 v200, v226, v227
	v_med3_f32 v228, v228, s6, v1
	v_med3_f32 v229, v229, s6, v1
	v_cvt_pk_fp8_f32 v200, v228, v229 op_sel:[0,0,1]
	v_mul_f32_e32 v226, 0x43800000, v51
	v_mul_f32_e32 v227, 0x43800000, v55
	v_med3_f32 v226, v226, s6, v1
	v_med3_f32 v227, v227, s6, v1
	v_mul_f32_e32 v228, 0x43800000, v59
	v_mul_f32_e32 v229, 0x43800000, v63
	v_cvt_pk_fp8_f32 v201, v226, v227
	v_med3_f32 v228, v228, s6, v1
	v_med3_f32 v229, v229, s6, v1
	v_cvt_pk_fp8_f32 v201, v228, v229 op_sel:[0,0,1]
	s_nop 1
	ds_write_b128 v232, v[198:201] offset:272
	v_mul_f32_e32 v226, 0x43800000, v4
	v_mul_f32_e32 v227, 0x43800000, v8
	v_med3_f32 v226, v226, s6, v1
	v_med3_f32 v227, v227, s6, v1
	v_mul_f32_e32 v228, 0x43800000, v12
	v_mul_f32_e32 v229, 0x43800000, v16
	v_cvt_pk_fp8_f32 v202, v226, v227
	v_med3_f32 v228, v228, s6, v1
	v_med3_f32 v229, v229, s6, v1
	v_cvt_pk_fp8_f32 v202, v228, v229 op_sel:[0,0,1]
	v_mul_f32_e32 v226, 0x43800000, v20
	v_mul_f32_e32 v227, 0x43800000, v24
	v_med3_f32 v226, v226, s6, v1
	v_med3_f32 v227, v227, s6, v1
	v_mul_f32_e32 v228, 0x43800000, v28
	v_mul_f32_e32 v229, 0x43800000, v32
	v_cvt_pk_fp8_f32 v203, v226, v227
	v_med3_f32 v228, v228, s6, v1
	v_med3_f32 v229, v229, s6, v1
	v_cvt_pk_fp8_f32 v203, v228, v229 op_sel:[0,0,1]
	v_mul_f32_e32 v226, 0x43800000, v36
	v_mul_f32_e32 v227, 0x43800000, v40
	v_med3_f32 v226, v226, s6, v1
	v_med3_f32 v227, v227, s6, v1
	v_mul_f32_e32 v228, 0x43800000, v44
	v_mul_f32_e32 v229, 0x43800000, v48
	v_cvt_pk_fp8_f32 v204, v226, v227
	v_med3_f32 v228, v228, s6, v1
	v_med3_f32 v229, v229, s6, v1
	v_cvt_pk_fp8_f32 v204, v228, v229 op_sel:[0,0,1]
	v_mul_f32_e32 v226, 0x43800000, v52
	v_mul_f32_e32 v227, 0x43800000, v56
	v_med3_f32 v226, v226, s6, v1
	v_med3_f32 v227, v227, s6, v1
	v_mul_f32_e32 v228, 0x43800000, v60
	v_mul_f32_e32 v229, 0x43800000, v64
	v_cvt_pk_fp8_f32 v205, v226, v227
	v_med3_f32 v228, v228, s6, v1
	v_med3_f32 v229, v229, s6, v1
	v_cvt_pk_fp8_f32 v205, v228, v229 op_sel:[0,0,1]
	s_nop 1
	ds_write_b128 v232, v[202:205] offset:544
	v_mul_f32_e32 v226, 0x43800000, v5
	v_mul_f32_e32 v227, 0x43800000, v9
	v_med3_f32 v226, v226, s6, v1
	v_med3_f32 v227, v227, s6, v1
	v_mul_f32_e32 v228, 0x43800000, v13
	v_mul_f32_e32 v229, 0x43800000, v17
	v_cvt_pk_fp8_f32 v206, v226, v227
	v_med3_f32 v228, v228, s6, v1
	v_med3_f32 v229, v229, s6, v1
	v_cvt_pk_fp8_f32 v206, v228, v229 op_sel:[0,0,1]
	v_mul_f32_e32 v226, 0x43800000, v21
	v_mul_f32_e32 v227, 0x43800000, v25
	v_med3_f32 v226, v226, s6, v1
	v_med3_f32 v227, v227, s6, v1
	v_mul_f32_e32 v228, 0x43800000, v29
	v_mul_f32_e32 v229, 0x43800000, v33
	v_cvt_pk_fp8_f32 v207, v226, v227
	v_med3_f32 v228, v228, s6, v1
	v_med3_f32 v229, v229, s6, v1
	v_cvt_pk_fp8_f32 v207, v228, v229 op_sel:[0,0,1]
	v_mul_f32_e32 v226, 0x43800000, v37
	v_mul_f32_e32 v227, 0x43800000, v41
	v_med3_f32 v226, v226, s6, v1
	v_med3_f32 v227, v227, s6, v1
	v_mul_f32_e32 v228, 0x43800000, v45
	v_mul_f32_e32 v229, 0x43800000, v49
	v_cvt_pk_fp8_f32 v208, v226, v227
	v_med3_f32 v228, v228, s6, v1
	v_med3_f32 v229, v229, s6, v1
	v_cvt_pk_fp8_f32 v208, v228, v229 op_sel:[0,0,1]
	v_mul_f32_e32 v226, 0x43800000, v53
	v_mul_f32_e32 v227, 0x43800000, v57
	v_med3_f32 v226, v226, s6, v1
	v_med3_f32 v227, v227, s6, v1
	v_mul_f32_e32 v228, 0x43800000, v61
	v_mul_f32_e32 v229, 0x43800000, v65
	v_cvt_pk_fp8_f32 v209, v226, v227
	v_med3_f32 v228, v228, s6, v1
	v_med3_f32 v229, v229, s6, v1
	v_cvt_pk_fp8_f32 v209, v228, v229 op_sel:[0,0,1]
	s_nop 1
	ds_write_b128 v232, v[206:209] offset:816
	s_waitcnt lgkmcnt(0)
	s_barrier
	ds_read_b128 v[194:197], v233 offset:0
	ds_read_b128 v[198:201], v233 offset:8704
	ds_read_b128 v[202:205], v233 offset:17408
	ds_read_b128 v[206:209], v233 offset:26112
	s_waitcnt lgkmcnt(3)
	global_store_dwordx4 v236, v[194:197], s[2:3] nt
	s_waitcnt lgkmcnt(2)
	global_store_dwordx4 v237, v[198:201], s[2:3] nt
	s_waitcnt lgkmcnt(1)
	global_store_dwordx4 v230, v[202:205], s[2:3] nt
	s_waitcnt lgkmcnt(0)
	global_store_dwordx4 v231, v[206:209], s[2:3] nt
	s_add_u32 s2, s2, 0x100
	s_addc_u32 s3, s3, 0
	s_waitcnt vmcnt(24)
	v_mul_f32_e32 v226, 0x43800000, v66
	v_mul_f32_e32 v227, 0x43800000, v70
	v_med3_f32 v226, v226, s6, v1
	v_med3_f32 v227, v227, s6, v1
	v_mul_f32_e32 v228, 0x43800000, v74
	v_mul_f32_e32 v229, 0x43800000, v78
	v_cvt_pk_fp8_f32 v194, v226, v227
	v_med3_f32 v228, v228, s6, v1
	v_med3_f32 v229, v229, s6, v1
	v_cvt_pk_fp8_f32 v194, v228, v229 op_sel:[0,0,1]
	s_waitcnt vmcnt(20)
	v_mul_f32_e32 v226, 0x43800000, v82
	v_mul_f32_e32 v227, 0x43800000, v86
	v_med3_f32 v226, v226, s6, v1
	v_med3_f32 v227, v227, s6, v1
	v_mul_f32_e32 v228, 0x43800000, v90
	v_mul_f32_e32 v229, 0x43800000, v94
	v_cvt_pk_fp8_f32 v195, v226, v227
	v_med3_f32 v228, v228, s6, v1
	v_med3_f32 v229, v229, s6, v1
	v_cvt_pk_fp8_f32 v195, v228, v229 op_sel:[0,0,1]
	s_waitcnt vmcnt(16)
	v_mul_f32_e32 v226, 0x43800000, v98
	v_mul_f32_e32 v227, 0x43800000, v102
	v_med3_f32 v226, v226, s6, v1
	v_med3_f32 v227, v227, s6, v1
	v_mul_f32_e32 v228, 0x43800000, v106
	v_mul_f32_e32 v229, 0x43800000, v110
	v_cvt_pk_fp8_f32 v196, v226, v227
	v_med3_f32 v228, v228, s6, v1
	v_med3_f32 v229, v229, s6, v1
	v_cvt_pk_fp8_f32 v196, v228, v229 op_sel:[0,0,1]
	s_waitcnt vmcnt(12)
	v_mul_f32_e32 v226, 0x43800000, v114
	v_mul_f32_e32 v227, 0x43800000, v118
	v_med3_f32 v226, v226, s6, v1
	v_med3_f32 v227, v227, s6, v1
	v_mul_f32_e32 v228, 0x43800000, v122
	v_mul_f32_e32 v229, 0x43800000, v126
	v_cvt_pk_fp8_f32 v197, v226, v227
	v_med3_f32 v228, v228, s6, v1
	v_med3_f32 v229, v229, s6, v1
	v_cvt_pk_fp8_f32 v197, v228, v229 op_sel:[0,0,1]
	s_nop 1
	ds_write_b128 v232, v[194:197] offset:34816
	v_mul_f32_e32 v226, 0x43800000, v67
	v_mul_f32_e32 v227, 0x43800000, v71
	v_med3_f32 v226, v226, s6, v1
	v_med3_f32 v227, v227, s6, v1
	v_mul_f32_e32 v228, 0x43800000, v75
	v_mul_f32_e32 v229, 0x43800000, v79
	v_cvt_pk_fp8_f32 v198, v226, v227
	v_med3_f32 v228, v228, s6, v1
	v_med3_f32 v229, v229, s6, v1
	v_cvt_pk_fp8_f32 v198, v228, v229 op_sel:[0,0,1]
	v_mul_f32_e32 v226, 0x43800000, v83
	v_mul_f32_e32 v227, 0x43800000, v87
	v_med3_f32 v226, v226, s6, v1
	v_med3_f32 v227, v227, s6, v1
	v_mul_f32_e32 v228, 0x43800000, v91
	v_mul_f32_e32 v229, 0x43800000, v95
	v_cvt_pk_fp8_f32 v199, v226, v227
	v_med3_f32 v228, v228, s6, v1
	v_med3_f32 v229, v229, s6, v1
	v_cvt_pk_fp8_f32 v199, v228, v229 op_sel:[0,0,1]
	v_mul_f32_e32 v226, 0x43800000, v99
	v_mul_f32_e32 v227, 0x43800000, v103
	v_med3_f32 v226, v226, s6, v1
	v_med3_f32 v227, v227, s6, v1
	v_mul_f32_e32 v228, 0x43800000, v107
	v_mul_f32_e32 v229, 0x43800000, v111
	v_cvt_pk_fp8_f32 v200, v226, v227
	v_med3_f32 v228, v228, s6, v1
	v_med3_f32 v229, v229, s6, v1
	v_cvt_pk_fp8_f32 v200, v228, v229 op_sel:[0,0,1]
	v_mul_f32_e32 v226, 0x43800000, v115
	v_mul_f32_e32 v227, 0x43800000, v119
	v_med3_f32 v226, v226, s6, v1
	v_med3_f32 v227, v227, s6, v1
	v_mul_f32_e32 v228, 0x43800000, v123
	v_mul_f32_e32 v229, 0x43800000, v127
	v_cvt_pk_fp8_f32 v201, v226, v227
	v_med3_f32 v228, v228, s6, v1
	v_med3_f32 v229, v229, s6, v1
	v_cvt_pk_fp8_f32 v201, v228, v229 op_sel:[0,0,1]
	s_nop 1
	ds_write_b128 v232, v[198:201] offset:35088
	v_mul_f32_e32 v226, 0x43800000, v68
	v_mul_f32_e32 v227, 0x43800000, v72
	v_med3_f32 v226, v226, s6, v1
	v_med3_f32 v227, v227, s6, v1
	v_mul_f32_e32 v228, 0x43800000, v76
	v_mul_f32_e32 v229, 0x43800000, v80
	v_cvt_pk_fp8_f32 v202, v226, v227
	v_med3_f32 v228, v228, s6, v1
	v_med3_f32 v229, v229, s6, v1
	v_cvt_pk_fp8_f32 v202, v228, v229 op_sel:[0,0,1]
	v_mul_f32_e32 v226, 0x43800000, v84
	v_mul_f32_e32 v227, 0x43800000, v88
	v_med3_f32 v226, v226, s6, v1
	v_med3_f32 v227, v227, s6, v1
	v_mul_f32_e32 v228, 0x43800000, v92
	v_mul_f32_e32 v229, 0x43800000, v96
	v_cvt_pk_fp8_f32 v203, v226, v227
	v_med3_f32 v228, v228, s6, v1
	v_med3_f32 v229, v229, s6, v1
	v_cvt_pk_fp8_f32 v203, v228, v229 op_sel:[0,0,1]
	v_mul_f32_e32 v226, 0x43800000, v100
	v_mul_f32_e32 v227, 0x43800000, v104
	v_med3_f32 v226, v226, s6, v1
	v_med3_f32 v227, v227, s6, v1
	v_mul_f32_e32 v228, 0x43800000, v108
	v_mul_f32_e32 v229, 0x43800000, v112
	v_cvt_pk_fp8_f32 v204, v226, v227
	v_med3_f32 v228, v228, s6, v1
	v_med3_f32 v229, v229, s6, v1
	v_cvt_pk_fp8_f32 v204, v228, v229 op_sel:[0,0,1]
	v_mul_f32_e32 v226, 0x43800000, v116
	v_mul_f32_e32 v227, 0x43800000, v120
	v_med3_f32 v226, v226, s6, v1
	v_med3_f32 v227, v227, s6, v1
	v_mul_f32_e32 v228, 0x43800000, v124
	v_mul_f32_e32 v229, 0x43800000, v128
	v_cvt_pk_fp8_f32 v205, v226, v227
	v_med3_f32 v228, v228, s6, v1
	v_med3_f32 v229, v229, s6, v1
	v_cvt_pk_fp8_f32 v205, v228, v229 op_sel:[0,0,1]
	s_nop 1
	ds_write_b128 v232, v[202:205] offset:35360
	v_mul_f32_e32 v226, 0x43800000, v69
	v_mul_f32_e32 v227, 0x43800000, v73
	v_med3_f32 v226, v226, s6, v1
	v_med3_f32 v227, v227, s6, v1
	v_mul_f32_e32 v228, 0x43800000, v77
	v_mul_f32_e32 v229, 0x43800000, v81
	v_cvt_pk_fp8_f32 v206, v226, v227
	v_med3_f32 v228, v228, s6, v1
	v_med3_f32 v229, v229, s6, v1
	v_cvt_pk_fp8_f32 v206, v228, v229 op_sel:[0,0,1]
	v_mul_f32_e32 v226, 0x43800000, v85
	v_mul_f32_e32 v227, 0x43800000, v89
	v_med3_f32 v226, v226, s6, v1
	v_med3_f32 v227, v227, s6, v1
	v_mul_f32_e32 v228, 0x43800000, v93
	v_mul_f32_e32 v229, 0x43800000, v97
	v_cvt_pk_fp8_f32 v207, v226, v227
	v_med3_f32 v228, v228, s6, v1
	v_med3_f32 v229, v229, s6, v1
	v_cvt_pk_fp8_f32 v207, v228, v229 op_sel:[0,0,1]
	v_mul_f32_e32 v226, 0x43800000, v101
	v_mul_f32_e32 v227, 0x43800000, v105
	v_med3_f32 v226, v226, s6, v1
	v_med3_f32 v227, v227, s6, v1
	v_mul_f32_e32 v228, 0x43800000, v109
	v_mul_f32_e32 v229, 0x43800000, v113
	v_cvt_pk_fp8_f32 v208, v226, v227
	v_med3_f32 v228, v228, s6, v1
	v_med3_f32 v229, v229, s6, v1
	v_cvt_pk_fp8_f32 v208, v228, v229 op_sel:[0,0,1]
	v_mul_f32_e32 v226, 0x43800000, v117
	v_mul_f32_e32 v227, 0x43800000, v121
	v_med3_f32 v226, v226, s6, v1
	v_med3_f32 v227, v227, s6, v1
	v_mul_f32_e32 v228, 0x43800000, v125
	v_mul_f32_e32 v229, 0x43800000, v129
	v_cvt_pk_fp8_f32 v209, v226, v227
	v_med3_f32 v228, v228, s6, v1
	v_med3_f32 v229, v229, s6, v1
	v_cvt_pk_fp8_f32 v209, v228, v229 op_sel:[0,0,1]
	s_nop 1
	ds_write_b128 v232, v[206:209] offset:35632
	s_waitcnt lgkmcnt(0)
	s_barrier
	ds_read_b128 v[194:197], v233 offset:34816
	ds_read_b128 v[198:201], v233 offset:43520
	ds_read_b128 v[202:205], v233 offset:52224
	ds_read_b128 v[206:209], v233 offset:60928
	s_waitcnt lgkmcnt(3)
	global_store_dwordx4 v236, v[194:197], s[2:3] nt
	s_waitcnt lgkmcnt(2)
	global_store_dwordx4 v237, v[198:201], s[2:3] nt
	s_waitcnt lgkmcnt(1)
	global_store_dwordx4 v230, v[202:205], s[2:3] nt
	s_waitcnt lgkmcnt(0)
	global_store_dwordx4 v231, v[206:209], s[2:3] nt
	s_add_u32 s2, s2, 0x100
	s_addc_u32 s3, s3, 0
	s_barrier

.LBB0_689:
	s_barrier
	s_add_u32 s7, s1, 0x200
	s_lshr_b32 s12, s7, 5
	s_and_b32 s7, s7, 31
	v_readlane_b32 s8, v254, 6
	v_readlane_b32 s9, v254, 7
	s_lshl_b32 s2, s12, 25
	s_and_b32 s1, s7, 1
	s_lshl_b32 s1, s1, 13
	s_add_u32 s2, s2, s1
	s_lshr_b32 s1, s7, 1
	s_lshl_b32 s1, s1, 9
	s_add_u32 s2, s2, s1
	s_add_u32 s8, s8, s2
	s_addc_u32 s9, s9, 0
	s_lshl_b32 s2, s12, 23
	s_lshl_b32 s1, s7, 18
	s_add_u32 s2, s2, s1
	s_add_u32 s2, s2, 0x40000000
	v_readlane_b32 s10, v254, 57
	v_readlane_b32 s11, v254, 58
	s_add_u32 s10, s10, s2
	s_addc_u32 s11, s11, 0
	s_mov_b32 s2, 0xc3e00000
	v_mov_b32_e32 v1, 0x43e00000
	v_lshrrev_b32_e32 v231, 5, v0
	v_and_b32_e32 v232, 31, v0
	v_lshlrev_b32_e32 v233, 4, v232
	v_lshlrev_b32_e32 v226, 18, v231
	v_add_u32_e32 v162, v226, v233
	v_add_u32_e32 v188, 0x4000, v162
	v_add_u32_e32 v194, 0x8000, v162
	v_add_u32_e32 v250, 0xc000, v162
	v_add_u32_e32 v251, 0x10000, v162
	v_add_u32_e32 v246, 0x14000, v162
	v_add_u32_e32 v247, 0x18000, v162
	v_add_u32_e32 v248, 0x1c000, v162
	v_add_u32_e32 v249, 0x20000, v162
	v_add_u32_e32 v242, 0x24000, v162
	v_add_u32_e32 v243, 0x28000, v162
	v_add_u32_e32 v244, 0x2c000, v162
	v_add_u32_e32 v245, 0x30000, v162
	v_add_u32_e32 v238, 0x34000, v162
	v_add_u32_e32 v239, 0x38000, v162
	v_add_u32_e32 v240, 0x3c000, v162
	v_lshrrev_b32_e32 v210, 4, v0
	v_and_b32_e32 v211, 15, v0
	v_lshlrev_b32_e32 v241, 11, v210
	v_lshl_add_u32 v241, v211, 4, v241
	v_add_u32_e32 v234, 0x10000, v241
	v_add_u32_e32 v235, 0x20000, v241
	v_add_u32_e32 v236, 0x30000, v241
	v_mul_u32_u24_e32 v237, 0x440, v232
	v_lshl_add_u32 v237, v231, 4, v237
	v_mul_u32_u24_e32 v230, 0x110, v210
	v_lshl_add_u32 v230, v211, 4, v230
	global_load_dwordx4 v[2:5], v162, s[8:9] nt
	global_load_dwordx4 v[6:9], v188, s[8:9] nt
	global_load_dwordx4 v[10:13], v194, s[8:9] nt
	global_load_dwordx4 v[14:17], v250, s[8:9] nt
	global_load_dwordx4 v[18:21], v251, s[8:9] nt
	global_load_dwordx4 v[22:25], v246, s[8:9] nt
	global_load_dwordx4 v[26:29], v247, s[8:9] nt
	global_load_dwordx4 v[30:33], v248, s[8:9] nt
	global_load_dwordx4 v[34:37], v249, s[8:9] nt
	global_load_dwordx4 v[38:41], v242, s[8:9] nt
	global_load_dwordx4 v[42:45], v243, s[8:9] nt
	global_load_dwordx4 v[46:49], v244, s[8:9] nt
	global_load_dwordx4 v[50:53], v245, s[8:9] nt
	global_load_dwordx4 v[54:57], v238, s[8:9] nt
	global_load_dwordx4 v[58:61], v239, s[8:9] nt
	global_load_dwordx4 v[62:65], v240, s[8:9] nt
	s_add_u32 s8, s8, 0x400000
	s_addc_u32 s9, s9, 0
	global_load_dwordx4 v[66:69], v162, s[8:9] nt
	global_load_dwordx4 v[70:73], v188, s[8:9] nt
	global_load_dwordx4 v[74:77], v194, s[8:9] nt
	global_load_dwordx4 v[78:81], v250, s[8:9] nt
	global_load_dwordx4 v[82:85], v251, s[8:9] nt
	global_load_dwordx4 v[86:89], v246, s[8:9] nt
	global_load_dwordx4 v[90:93], v247, s[8:9] nt
	global_load_dwordx4 v[94:97], v248, s[8:9] nt
	global_load_dwordx4 v[98:101], v249, s[8:9] nt
	global_load_dwordx4 v[102:105], v242, s[8:9] nt
	global_load_dwordx4 v[106:109], v243, s[8:9] nt
	global_load_dwordx4 v[110:113], v244, s[8:9] nt
	global_load_dwordx4 v[114:117], v245, s[8:9] nt
	global_load_dwordx4 v[118:121], v238, s[8:9] nt
	global_load_dwordx4 v[122:125], v239, s[8:9] nt
	global_load_dwordx4 v[126:129], v240, s[8:9] nt
	s_add_u32 s8, s8, 0x400000
	s_addc_u32 s9, s9, 0
	global_load_dwordx4 v[130:133], v162, s[8:9] nt
	global_load_dwordx4 v[134:137], v188, s[8:9] nt
	global_load_dwordx4 v[138:141], v194, s[8:9] nt
	global_load_dwordx4 v[142:145], v250, s[8:9] nt
	global_load_dwordx4 v[146:149], v251, s[8:9] nt
	global_load_dwordx4 v[150:153], v246, s[8:9] nt
	global_load_dwordx4 v[154:157], v247, s[8:9] nt
	global_load_dwordx4 v[158:161], v248, s[8:9] nt
	global_load_dwordx4 v[164:167], v249, s[8:9] nt
	global_load_dwordx4 v[168:171], v242, s[8:9] nt
	global_load_dwordx4 v[172:175], v243, s[8:9] nt
	global_load_dwordx4 v[176:179], v244, s[8:9] nt
	global_load_dwordx4 v[180:183], v245, s[8:9] nt
	global_load_dwordx4 v[184:187], v238, s[8:9] nt
	global_load_dwordx4 v[202:205], v239, s[8:9] nt
	global_load_dwordx4 v[206:209], v240, s[8:9] nt
	s_add_u32 s8, s8, 0x400000
	s_addc_u32 s9, s9, 0
	s_waitcnt vmcnt(44)
	v_mul_f32_e32 v231, 0x43800000, v2
	v_mul_f32_e32 v232, 0x43800000, v6
	v_med3_f32 v231, v231, s2, v1
	v_med3_f32 v232, v232, s2, v1
	v_mul_f32_e32 v233, 0x43800000, v10
	v_mul_f32_e32 v226, 0x43800000, v14
	v_cvt_pk_fp8_f32 v210, v231, v232
	v_med3_f32 v233, v233, s2, v1
	v_med3_f32 v226, v226, s2, v1
	v_cvt_pk_fp8_f32 v210, v233, v226 op_sel:[0,0,1]
	s_waitcnt vmcnt(40)
	v_mul_f32_e32 v231, 0x43800000, v18
	v_mul_f32_e32 v232, 0x43800000, v22
	v_med3_f32 v231, v231, s2, v1
	v_med3_f32 v232, v232, s2, v1
	v_mul_f32_e32 v233, 0x43800000, v26
	v_mul_f32_e32 v226, 0x43800000, v30
	v_cvt_pk_fp8_f32 v211, v231, v232
	v_med3_f32 v233, v233, s2, v1
	v_med3_f32 v226, v226, s2, v1
	v_cvt_pk_fp8_f32 v211, v233, v226 op_sel:[0,0,1]
	s_waitcnt vmcnt(36)
	v_mul_f32_e32 v231, 0x43800000, v34
	v_mul_f32_e32 v232, 0x43800000, v38
	v_med3_f32 v231, v231, s2, v1
	v_med3_f32 v232, v232, s2, v1
	v_mul_f32_e32 v233, 0x43800000, v42
	v_mul_f32_e32 v226, 0x43800000, v46
	v_cvt_pk_fp8_f32 v212, v231, v232
	v_med3_f32 v233, v233, s2, v1
	v_med3_f32 v226, v226, s2, v1
	v_cvt_pk_fp8_f32 v212, v233, v226 op_sel:[0,0,1]
	s_waitcnt vmcnt(32)
	v_mul_f32_e32 v231, 0x43800000, v50
	v_mul_f32_e32 v232, 0x43800000, v54
	v_med3_f32 v231, v231, s2, v1
	v_med3_f32 v232, v232, s2, v1
	v_mul_f32_e32 v233, 0x43800000, v58
	v_mul_f32_e32 v226, 0x43800000, v62
	v_cvt_pk_fp8_f32 v213, v231, v232
	v_med3_f32 v233, v233, s2, v1
	v_med3_f32 v226, v226, s2, v1
	v_cvt_pk_fp8_f32 v213, v233, v226 op_sel:[0,0,1]
	s_nop 1
	ds_write_b128 v237, v[210:213] offset:0
	v_mul_f32_e32 v231, 0x43800000, v3
	v_mul_f32_e32 v232, 0x43800000, v7
	v_med3_f32 v231, v231, s2, v1
	v_med3_f32 v232, v232, s2, v1
	v_mul_f32_e32 v233, 0x43800000, v11
	v_mul_f32_e32 v226, 0x43800000, v15
	v_cvt_pk_fp8_f32 v214, v231, v232
	v_med3_f32 v233, v233, s2, v1
	v_med3_f32 v226, v226, s2, v1
	v_cvt_pk_fp8_f32 v214, v233, v226 op_sel:[0,0,1]
	v_mul_f32_e32 v231, 0x43800000, v19
	v_mul_f32_e32 v232, 0x43800000, v23
	v_med3_f32 v231, v231, s2, v1
	v_med3_f32 v232, v232, s2, v1
	v_mul_f32_e32 v233, 0x43800000, v27
	v_mul_f32_e32 v226, 0x43800000, v31
	v_cvt_pk_fp8_f32 v215, v231, v232
	v_med3_f32 v233, v233, s2, v1
	v_med3_f32 v226, v226, s2, v1
	v_cvt_pk_fp8_f32 v215, v233, v226 op_sel:[0,0,1]
	v_mul_f32_e32 v231, 0x43800000, v35
	v_mul_f32_e32 v232, 0x43800000, v39
	v_med3_f32 v231, v231, s2, v1
	v_med3_f32 v232, v232, s2, v1
	v_mul_f32_e32 v233, 0x43800000, v43
	v_mul_f32_e32 v226, 0x43800000, v47
	v_cvt_pk_fp8_f32 v216, v231, v232
	v_med3_f32 v233, v233, s2, v1
	v_med3_f32 v226, v226, s2, v1
	v_cvt_pk_fp8_f32 v216, v233, v226 op_sel:[0,0,1]
	v_mul_f32_e32 v231, 0x43800000, v51
	v_mul_f32_e32 v232, 0x43800000, v55
	v_med3_f32 v231, v231, s2, v1
	v_med3_f32 v232, v232, s2, v1
	v_mul_f32_e32 v233, 0x43800000, v59
	v_mul_f32_e32 v226, 0x43800000, v63
	v_cvt_pk_fp8_f32 v217, v231, v232
	v_med3_f32 v233, v233, s2, v1
	v_med3_f32 v226, v226, s2, v1
	v_cvt_pk_fp8_f32 v217, v233, v226 op_sel:[0,0,1]
	s_nop 1
	ds_write_b128 v237, v[214:217] offset:272
	v_mul_f32_e32 v231, 0x43800000, v4
	v_mul_f32_e32 v232, 0x43800000, v8
	v_med3_f32 v231, v231, s2, v1
	v_med3_f32 v232, v232, s2, v1
	v_mul_f32_e32 v233, 0x43800000, v12
	v_mul_f32_e32 v226, 0x43800000, v16
	v_cvt_pk_fp8_f32 v218, v231, v232
	v_med3_f32 v233, v233, s2, v1
	v_med3_f32 v226, v226, s2, v1
	v_cvt_pk_fp8_f32 v218, v233, v226 op_sel:[0,0,1]
	v_mul_f32_e32 v231, 0x43800000, v20
	v_mul_f32_e32 v232, 0x43800000, v24
	v_med3_f32 v231, v231, s2, v1
	v_med3_f32 v232, v232, s2, v1
	v_mul_f32_e32 v233, 0x43800000, v28
	v_mul_f32_e32 v226, 0x43800000, v32
	v_cvt_pk_fp8_f32 v219, v231, v232
	v_med3_f32 v233, v233, s2, v1
	v_med3_f32 v226, v226, s2, v1
	v_cvt_pk_fp8_f32 v219, v233, v226 op_sel:[0,0,1]
	v_mul_f32_e32 v231, 0x43800000, v36
	v_mul_f32_e32 v232, 0x43800000, v40
	v_med3_f32 v231, v231, s2, v1
	v_med3_f32 v232, v232, s2, v1
	v_mul_f32_e32 v233, 0x43800000, v44
	v_mul_f32_e32 v226, 0x43800000, v48
	v_cvt_pk_fp8_f32 v220, v231, v232
	v_med3_f32 v233, v233, s2, v1
	v_med3_f32 v226, v226, s2, v1
	v_cvt_pk_fp8_f32 v220, v233, v226 op_sel:[0,0,1]
	v_mul_f32_e32 v231, 0x43800000, v52
	v_mul_f32_e32 v232, 0x43800000, v56
	v_med3_f32 v231, v231, s2, v1
	v_med3_f32 v232, v232, s2, v1
	v_mul_f32_e32 v233, 0x43800000, v60
	v_mul_f32_e32 v226, 0x43800000, v64
	v_cvt_pk_fp8_f32 v221, v231, v232
	v_med3_f32 v233, v233, s2, v1
	v_med3_f32 v226, v226, s2, v1
	v_cvt_pk_fp8_f32 v221, v233, v226 op_sel:[0,0,1]
	s_nop 1
	ds_write_b128 v237, v[218:221] offset:544
	v_mul_f32_e32 v231, 0x43800000, v5
	v_mul_f32_e32 v232, 0x43800000, v9
	v_med3_f32 v231, v231, s2, v1
	v_med3_f32 v232, v232, s2, v1
	v_mul_f32_e32 v233, 0x43800000, v13
	v_mul_f32_e32 v226, 0x43800000, v17
	v_cvt_pk_fp8_f32 v222, v231, v232
	v_med3_f32 v233, v233, s2, v1
	v_med3_f32 v226, v226, s2, v1
	v_cvt_pk_fp8_f32 v222, v233, v226 op_sel:[0,0,1]
	v_mul_f32_e32 v231, 0x43800000, v21
	v_mul_f32_e32 v232, 0x43800000, v25
	v_med3_f32 v231, v231, s2, v1
	v_med3_f32 v232, v232, s2, v1
	v_mul_f32_e32 v233, 0x43800000, v29
	v_mul_f32_e32 v226, 0x43800000, v33
	v_cvt_pk_fp8_f32 v223, v231, v232
	v_med3_f32 v233, v233, s2, v1
	v_med3_f32 v226, v226, s2, v1
	v_cvt_pk_fp8_f32 v223, v233, v226 op_sel:[0,0,1]
	v_mul_f32_e32 v231, 0x43800000, v37
	v_mul_f32_e32 v232, 0x43800000, v41
	v_med3_f32 v231, v231, s2, v1
	v_med3_f32 v232, v232, s2, v1
	v_mul_f32_e32 v233, 0x43800000, v45
	v_mul_f32_e32 v226, 0x43800000, v49
	v_cvt_pk_fp8_f32 v224, v231, v232
	v_med3_f32 v233, v233, s2, v1
	v_med3_f32 v226, v226, s2, v1
	v_cvt_pk_fp8_f32 v224, v233, v226 op_sel:[0,0,1]
	v_mul_f32_e32 v231, 0x43800000, v53
	v_mul_f32_e32 v232, 0x43800000, v57
	v_med3_f32 v231, v231, s2, v1
	v_med3_f32 v232, v232, s2, v1
	v_mul_f32_e32 v233, 0x43800000, v61
	v_mul_f32_e32 v226, 0x43800000, v65
	v_cvt_pk_fp8_f32 v225, v231, v232
	v_med3_f32 v233, v233, s2, v1
	v_med3_f32 v226, v226, s2, v1
	v_cvt_pk_fp8_f32 v225, v233, v226 op_sel:[0,0,1]
	s_nop 1
	ds_write_b128 v237, v[222:225] offset:816
	s_waitcnt lgkmcnt(0)
	s_barrier
	global_load_dwordx4 v[2:5], v162, s[8:9] nt
	global_load_dwordx4 v[6:9], v188, s[8:9] nt
	global_load_dwordx4 v[10:13], v194, s[8:9] nt
	global_load_dwordx4 v[14:17], v250, s[8:9] nt
	global_load_dwordx4 v[18:21], v251, s[8:9] nt
	global_load_dwordx4 v[22:25], v246, s[8:9] nt
	global_load_dwordx4 v[26:29], v247, s[8:9] nt
	global_load_dwordx4 v[30:33], v248, s[8:9] nt
	global_load_dwordx4 v[34:37], v249, s[8:9] nt
	global_load_dwordx4 v[38:41], v242, s[8:9] nt
	global_load_dwordx4 v[42:45], v243, s[8:9] nt
	global_load_dwordx4 v[46:49], v244, s[8:9] nt
	global_load_dwordx4 v[50:53], v245, s[8:9] nt
	global_load_dwordx4 v[54:57], v238, s[8:9] nt
	global_load_dwordx4 v[58:61], v239, s[8:9] nt
	global_load_dwordx4 v[62:65], v240, s[8:9] nt
	s_add_u32 s8, s8, 0x400000
	s_addc_u32 s9, s9, 0
	ds_read_b128 v[210:213], v230 offset:0
	ds_read_b128 v[214:217], v230 offset:8704
	ds_read_b128 v[218:221], v230 offset:17408
	ds_read_b128 v[222:225], v230 offset:26112
	s_waitcnt lgkmcnt(3)
	global_store_dwordx4 v241, v[210:213], s[10:11] nt
	s_waitcnt lgkmcnt(2)
	global_store_dwordx4 v234, v[214:217], s[10:11] nt
	s_waitcnt lgkmcnt(1)
	global_store_dwordx4 v235, v[218:221], s[10:11] nt
	s_waitcnt lgkmcnt(0)
	global_store_dwordx4 v236, v[222:225], s[10:11] nt
	s_add_u32 s10, s10, 0x100
	s_addc_u32 s11, s11, 0
	s_waitcnt vmcnt(48)
	v_mul_f32_e32 v231, 0x43800000, v66
	v_mul_f32_e32 v232, 0x43800000, v70
	v_med3_f32 v231, v231, s2, v1
	v_med3_f32 v232, v232, s2, v1
	v_mul_f32_e32 v233, 0x43800000, v74
	v_mul_f32_e32 v226, 0x43800000, v78
	v_cvt_pk_fp8_f32 v210, v231, v232
	v_med3_f32 v233, v233, s2, v1
	v_med3_f32 v226, v226, s2, v1
	v_cvt_pk_fp8_f32 v210, v233, v226 op_sel:[0,0,1]
	s_waitcnt vmcnt(44)
	v_mul_f32_e32 v231, 0x43800000, v82
	v_mul_f32_e32 v232, 0x43800000, v86
	v_med3_f32 v231, v231, s2, v1
	v_med3_f32 v232, v232, s2, v1
	v_mul_f32_e32 v233, 0x43800000, v90
	v_mul_f32_e32 v226, 0x43800000, v94
	v_cvt_pk_fp8_f32 v211, v231, v232
	v_med3_f32 v233, v233, s2, v1
	v_med3_f32 v226, v226, s2, v1
	v_cvt_pk_fp8_f32 v211, v233, v226 op_sel:[0,0,1]
	s_waitcnt vmcnt(40)
	v_mul_f32_e32 v231, 0x43800000, v98
	v_mul_f32_e32 v232, 0x43800000, v102
	v_med3_f32 v231, v231, s2, v1
	v_med3_f32 v232, v232, s2, v1
	v_mul_f32_e32 v233, 0x43800000, v106
	v_mul_f32_e32 v226, 0x43800000, v110
	v_cvt_pk_fp8_f32 v212, v231, v232
	v_med3_f32 v233, v233, s2, v1
	v_med3_f32 v226, v226, s2, v1
	v_cvt_pk_fp8_f32 v212, v233, v226 op_sel:[0,0,1]
	s_waitcnt vmcnt(36)
	v_mul_f32_e32 v231, 0x43800000, v114
	v_mul_f32_e32 v232, 0x43800000, v118
	v_med3_f32 v231, v231, s2, v1
	v_med3_f32 v232, v232, s2, v1
	v_mul_f32_e32 v233, 0x43800000, v122
	v_mul_f32_e32 v226, 0x43800000, v126
	v_cvt_pk_fp8_f32 v213, v231, v232
	v_med3_f32 v233, v233, s2, v1
	v_med3_f32 v226, v226, s2, v1
	v_cvt_pk_fp8_f32 v213, v233, v226 op_sel:[0,0,1]
	s_nop 1
	ds_write_b128 v237, v[210:213] offset:34816
	v_mul_f32_e32 v231, 0x43800000, v67
	v_mul_f32_e32 v232, 0x43800000, v71
	v_med3_f32 v231, v231, s2, v1
	v_med3_f32 v232, v232, s2, v1
	v_mul_f32_e32 v233, 0x43800000, v75
	v_mul_f32_e32 v226, 0x43800000, v79
	v_cvt_pk_fp8_f32 v214, v231, v232
	v_med3_f32 v233, v233, s2, v1
	v_med3_f32 v226, v226, s2, v1
	v_cvt_pk_fp8_f32 v214, v233, v226 op_sel:[0,0,1]
	v_mul_f32_e32 v231, 0x43800000, v83
	v_mul_f32_e32 v232, 0x43800000, v87
	v_med3_f32 v231, v231, s2, v1
	v_med3_f32 v232, v232, s2, v1
	v_mul_f32_e32 v233, 0x43800000, v91
	v_mul_f32_e32 v226, 0x43800000, v95
	v_cvt_pk_fp8_f32 v215, v231, v232
	v_med3_f32 v233, v233, s2, v1
	v_med3_f32 v226, v226, s2, v1
	v_cvt_pk_fp8_f32 v215, v233, v226 op_sel:[0,0,1]
	v_mul_f32_e32 v231, 0x43800000, v99
	v_mul_f32_e32 v232, 0x43800000, v103
	v_med3_f32 v231, v231, s2, v1
	v_med3_f32 v232, v232, s2, v1
	v_mul_f32_e32 v233, 0x43800000, v107
	v_mul_f32_e32 v226, 0x43800000, v111
	v_cvt_pk_fp8_f32 v216, v231, v232
	v_med3_f32 v233, v233, s2, v1
	v_med3_f32 v226, v226, s2, v1
	v_cvt_pk_fp8_f32 v216, v233, v226 op_sel:[0,0,1]
	v_mul_f32_e32 v231, 0x43800000, v115
	v_mul_f32_e32 v232, 0x43800000, v119
	v_med3_f32 v231, v231, s2, v1
	v_med3_f32 v232, v232, s2, v1
	v_mul_f32_e32 v233, 0x43800000, v123
	v_mul_f32_e32 v226, 0x43800000, v127
	v_cvt_pk_fp8_f32 v217, v231, v232
	v_med3_f32 v233, v233, s2, v1
	v_med3_f32 v226, v226, s2, v1
	v_cvt_pk_fp8_f32 v217, v233, v226 op_sel:[0,0,1]
	s_nop 1
	ds_write_b128 v237, v[214:217] offset:35088
	v_mul_f32_e32 v231, 0x43800000, v68
	v_mul_f32_e32 v232, 0x43800000, v72
	v_med3_f32 v231, v231, s2, v1
	v_med3_f32 v232, v232, s2, v1
	v_mul_f32_e32 v233, 0x43800000, v76
	v_mul_f32_e32 v226, 0x43800000, v80
	v_cvt_pk_fp8_f32 v218, v231, v232
	v_med3_f32 v233, v233, s2, v1
	v_med3_f32 v226, v226, s2, v1
	v_cvt_pk_fp8_f32 v218, v233, v226 op_sel:[0,0,1]
	v_mul_f32_e32 v231, 0x43800000, v84
	v_mul_f32_e32 v232, 0x43800000, v88
	v_med3_f32 v231, v231, s2, v1
	v_med3_f32 v232, v232, s2, v1
	v_mul_f32_e32 v233, 0x43800000, v92
	v_mul_f32_e32 v226, 0x43800000, v96
	v_cvt_pk_fp8_f32 v219, v231, v232
	v_med3_f32 v233, v233, s2, v1
	v_med3_f32 v226, v226, s2, v1
	v_cvt_pk_fp8_f32 v219, v233, v226 op_sel:[0,0,1]
	v_mul_f32_e32 v231, 0x43800000, v100
	v_mul_f32_e32 v232, 0x43800000, v104
	v_med3_f32 v231, v231, s2, v1
	v_med3_f32 v232, v232, s2, v1
	v_mul_f32_e32 v233, 0x43800000, v108
	v_mul_f32_e32 v226, 0x43800000, v112
	v_cvt_pk_fp8_f32 v220, v231, v232
	v_med3_f32 v233, v233, s2, v1
	v_med3_f32 v226, v226, s2, v1
	v_cvt_pk_fp8_f32 v220, v233, v226 op_sel:[0,0,1]
	v_mul_f32_e32 v231, 0x43800000, v116
	v_mul_f32_e32 v232, 0x43800000, v120
	v_med3_f32 v231, v231, s2, v1
	v_med3_f32 v232, v232, s2, v1
	v_mul_f32_e32 v233, 0x43800000, v124
	v_mul_f32_e32 v226, 0x43800000, v128
	v_cvt_pk_fp8_f32 v221, v231, v232
	v_med3_f32 v233, v233, s2, v1
	v_med3_f32 v226, v226, s2, v1
	v_cvt_pk_fp8_f32 v221, v233, v226 op_sel:[0,0,1]
	s_nop 1
	ds_write_b128 v237, v[218:221] offset:35360
	v_mul_f32_e32 v231, 0x43800000, v69
	v_mul_f32_e32 v232, 0x43800000, v73
	v_med3_f32 v231, v231, s2, v1
	v_med3_f32 v232, v232, s2, v1
	v_mul_f32_e32 v233, 0x43800000, v77
	v_mul_f32_e32 v226, 0x43800000, v81
	v_cvt_pk_fp8_f32 v222, v231, v232
	v_med3_f32 v233, v233, s2, v1
	v_med3_f32 v226, v226, s2, v1
	v_cvt_pk_fp8_f32 v222, v233, v226 op_sel:[0,0,1]
	v_mul_f32_e32 v231, 0x43800000, v85
	v_mul_f32_e32 v232, 0x43800000, v89
	v_med3_f32 v231, v231, s2, v1
	v_med3_f32 v232, v232, s2, v1
	v_mul_f32_e32 v233, 0x43800000, v93
	v_mul_f32_e32 v226, 0x43800000, v97
	v_cvt_pk_fp8_f32 v223, v231, v232
	v_med3_f32 v233, v233, s2, v1
	v_med3_f32 v226, v226, s2, v1
	v_cvt_pk_fp8_f32 v223, v233, v226 op_sel:[0,0,1]
	v_mul_f32_e32 v231, 0x43800000, v101
	v_mul_f32_e32 v232, 0x43800000, v105
	v_med3_f32 v231, v231, s2, v1
	v_med3_f32 v232, v232, s2, v1
	v_mul_f32_e32 v233, 0x43800000, v109
	v_mul_f32_e32 v226, 0x43800000, v113
	v_cvt_pk_fp8_f32 v224, v231, v232
	v_med3_f32 v233, v233, s2, v1
	v_med3_f32 v226, v226, s2, v1
	v_cvt_pk_fp8_f32 v224, v233, v226 op_sel:[0,0,1]
	v_mul_f32_e32 v231, 0x43800000, v117
	v_mul_f32_e32 v232, 0x43800000, v121
	v_med3_f32 v231, v231, s2, v1
	v_med3_f32 v232, v232, s2, v1
	v_mul_f32_e32 v233, 0x43800000, v125
	v_mul_f32_e32 v226, 0x43800000, v129
	v_cvt_pk_fp8_f32 v225, v231, v232
	v_med3_f32 v233, v233, s2, v1
	v_med3_f32 v226, v226, s2, v1
	v_cvt_pk_fp8_f32 v225, v233, v226 op_sel:[0,0,1]
	s_nop 1
	ds_write_b128 v237, v[222:225] offset:35632
	s_waitcnt lgkmcnt(0)
	s_barrier
	global_load_dwordx4 v[66:69], v162, s[8:9] nt
	global_load_dwordx4 v[70:73], v188, s[8:9] nt
	global_load_dwordx4 v[74:77], v194, s[8:9] nt
	global_load_dwordx4 v[78:81], v250, s[8:9] nt
	global_load_dwordx4 v[82:85], v251, s[8:9] nt
	global_load_dwordx4 v[86:89], v246, s[8:9] nt
	global_load_dwordx4 v[90:93], v247, s[8:9] nt
	global_load_dwordx4 v[94:97], v248, s[8:9] nt
	global_load_dwordx4 v[98:101], v249, s[8:9] nt
	global_load_dwordx4 v[102:105], v242, s[8:9] nt
	global_load_dwordx4 v[106:109], v243, s[8:9] nt
	global_load_dwordx4 v[110:113], v244, s[8:9] nt
	global_load_dwordx4 v[114:117], v245, s[8:9] nt
	global_load_dwordx4 v[118:121], v238, s[8:9] nt
	global_load_dwordx4 v[122:125], v239, s[8:9] nt
	global_load_dwordx4 v[126:129], v240, s[8:9] nt
	s_add_u32 s8, s8, 0x400000
	s_addc_u32 s9, s9, 0
	ds_read_b128 v[210:213], v230 offset:34816
	ds_read_b128 v[214:217], v230 offset:43520
	ds_read_b128 v[218:221], v230 offset:52224
	ds_read_b128 v[222:225], v230 offset:60928
	s_waitcnt lgkmcnt(3)
	global_store_dwordx4 v241, v[210:213], s[10:11] nt
	s_waitcnt lgkmcnt(2)
	global_store_dwordx4 v234, v[214:217], s[10:11] nt
	s_waitcnt lgkmcnt(1)
	global_store_dwordx4 v235, v[218:221], s[10:11] nt
	s_waitcnt lgkmcnt(0)
	global_store_dwordx4 v236, v[222:225], s[10:11] nt
	s_add_u32 s10, s10, 0x100
	s_addc_u32 s11, s11, 0
	s_waitcnt vmcnt(52)
	v_mul_f32_e32 v231, 0x43800000, v130
	v_mul_f32_e32 v232, 0x43800000, v134
	v_med3_f32 v231, v231, s2, v1
	v_med3_f32 v232, v232, s2, v1
	v_mul_f32_e32 v233, 0x43800000, v138
	v_mul_f32_e32 v226, 0x43800000, v142
	v_cvt_pk_fp8_f32 v210, v231, v232
	v_med3_f32 v233, v233, s2, v1
	v_med3_f32 v226, v226, s2, v1
	v_cvt_pk_fp8_f32 v210, v233, v226 op_sel:[0,0,1]
	s_waitcnt vmcnt(48)
	v_mul_f32_e32 v231, 0x43800000, v146
	v_mul_f32_e32 v232, 0x43800000, v150
	v_med3_f32 v231, v231, s2, v1
	v_med3_f32 v232, v232, s2, v1
	v_mul_f32_e32 v233, 0x43800000, v154
	v_mul_f32_e32 v226, 0x43800000, v158
	v_cvt_pk_fp8_f32 v211, v231, v232
	v_med3_f32 v233, v233, s2, v1
	v_med3_f32 v226, v226, s2, v1
	v_cvt_pk_fp8_f32 v211, v233, v226 op_sel:[0,0,1]
	s_waitcnt vmcnt(44)
	v_mul_f32_e32 v231, 0x43800000, v164
	v_mul_f32_e32 v232, 0x43800000, v168
	v_med3_f32 v231, v231, s2, v1
	v_med3_f32 v232, v232, s2, v1
	v_mul_f32_e32 v233, 0x43800000, v172
	v_mul_f32_e32 v226, 0x43800000, v176
	v_cvt_pk_fp8_f32 v212, v231, v232
	v_med3_f32 v233, v233, s2, v1
	v_med3_f32 v226, v226, s2, v1
	v_cvt_pk_fp8_f32 v212, v233, v226 op_sel:[0,0,1]
	s_waitcnt vmcnt(40)
	v_mul_f32_e32 v231, 0x43800000, v180
	v_mul_f32_e32 v232, 0x43800000, v184
	v_med3_f32 v231, v231, s2, v1
	v_med3_f32 v232, v232, s2, v1
	v_mul_f32_e32 v233, 0x43800000, v202
	v_mul_f32_e32 v226, 0x43800000, v206
	v_cvt_pk_fp8_f32 v213, v231, v232
	v_med3_f32 v233, v233, s2, v1
	v_med3_f32 v226, v226, s2, v1
	v_cvt_pk_fp8_f32 v213, v233, v226 op_sel:[0,0,1]
	s_nop 1
	ds_write_b128 v237, v[210:213] offset:0
	v_mul_f32_e32 v231, 0x43800000, v131
	v_mul_f32_e32 v232, 0x43800000, v135
	v_med3_f32 v231, v231, s2, v1
	v_med3_f32 v232, v232, s2, v1
	v_mul_f32_e32 v233, 0x43800000, v139
	v_mul_f32_e32 v226, 0x43800000, v143
	v_cvt_pk_fp8_f32 v214, v231, v232
	v_med3_f32 v233, v233, s2, v1
	v_med3_f32 v226, v226, s2, v1
	v_cvt_pk_fp8_f32 v214, v233, v226 op_sel:[0,0,1]
	v_mul_f32_e32 v231, 0x43800000, v147
	v_mul_f32_e32 v232, 0x43800000, v151
	v_med3_f32 v231, v231, s2, v1
	v_med3_f32 v232, v232, s2, v1
	v_mul_f32_e32 v233, 0x43800000, v155
	v_mul_f32_e32 v226, 0x43800000, v159
	v_cvt_pk_fp8_f32 v215, v231, v232
	v_med3_f32 v233, v233, s2, v1
	v_med3_f32 v226, v226, s2, v1
	v_cvt_pk_fp8_f32 v215, v233, v226 op_sel:[0,0,1]
	v_mul_f32_e32 v231, 0x43800000, v165
	v_mul_f32_e32 v232, 0x43800000, v169
	v_med3_f32 v231, v231, s2, v1
	v_med3_f32 v232, v232, s2, v1
	v_mul_f32_e32 v233, 0x43800000, v173
	v_mul_f32_e32 v226, 0x43800000, v177
	v_cvt_pk_fp8_f32 v216, v231, v232
	v_med3_f32 v233, v233, s2, v1
	v_med3_f32 v226, v226, s2, v1
	v_cvt_pk_fp8_f32 v216, v233, v226 op_sel:[0,0,1]
	v_mul_f32_e32 v231, 0x43800000, v181
	v_mul_f32_e32 v232, 0x43800000, v185
	v_med3_f32 v231, v231, s2, v1
	v_med3_f32 v232, v232, s2, v1
	v_mul_f32_e32 v233, 0x43800000, v203
	v_mul_f32_e32 v226, 0x43800000, v207
	v_cvt_pk_fp8_f32 v217, v231, v232
	v_med3_f32 v233, v233, s2, v1
	v_med3_f32 v226, v226, s2, v1
	v_cvt_pk_fp8_f32 v217, v233, v226 op_sel:[0,0,1]
	s_nop 1
	ds_write_b128 v237, v[214:217] offset:272
	v_mul_f32_e32 v231, 0x43800000, v132
	v_mul_f32_e32 v232, 0x43800000, v136
	v_med3_f32 v231, v231, s2, v1
	v_med3_f32 v232, v232, s2, v1
	v_mul_f32_e32 v233, 0x43800000, v140
	v_mul_f32_e32 v226, 0x43800000, v144
	v_cvt_pk_fp8_f32 v218, v231, v232
	v_med3_f32 v233, v233, s2, v1
	v_med3_f32 v226, v226, s2, v1
	v_cvt_pk_fp8_f32 v218, v233, v226 op_sel:[0,0,1]
	v_mul_f32_e32 v231, 0x43800000, v148
	v_mul_f32_e32 v232, 0x43800000, v152
	v_med3_f32 v231, v231, s2, v1
	v_med3_f32 v232, v232, s2, v1
	v_mul_f32_e32 v233, 0x43800000, v156
	v_mul_f32_e32 v226, 0x43800000, v160
	v_cvt_pk_fp8_f32 v219, v231, v232
	v_med3_f32 v233, v233, s2, v1
	v_med3_f32 v226, v226, s2, v1
	v_cvt_pk_fp8_f32 v219, v233, v226 op_sel:[0,0,1]
	v_mul_f32_e32 v231, 0x43800000, v166
	v_mul_f32_e32 v232, 0x43800000, v170
	v_med3_f32 v231, v231, s2, v1
	v_med3_f32 v232, v232, s2, v1
	v_mul_f32_e32 v233, 0x43800000, v174
	v_mul_f32_e32 v226, 0x43800000, v178
	v_cvt_pk_fp8_f32 v220, v231, v232
	v_med3_f32 v233, v233, s2, v1
	v_med3_f32 v226, v226, s2, v1
	v_cvt_pk_fp8_f32 v220, v233, v226 op_sel:[0,0,1]
	v_mul_f32_e32 v231, 0x43800000, v182
	v_mul_f32_e32 v232, 0x43800000, v186
	v_med3_f32 v231, v231, s2, v1
	v_med3_f32 v232, v232, s2, v1
	v_mul_f32_e32 v233, 0x43800000, v204
	v_mul_f32_e32 v226, 0x43800000, v208
	v_cvt_pk_fp8_f32 v221, v231, v232
	v_med3_f32 v233, v233, s2, v1
	v_med3_f32 v226, v226, s2, v1
	v_cvt_pk_fp8_f32 v221, v233, v226 op_sel:[0,0,1]
	s_nop 1
	ds_write_b128 v237, v[218:221] offset:544
	v_mul_f32_e32 v231, 0x43800000, v133
	v_mul_f32_e32 v232, 0x43800000, v137
	v_med3_f32 v231, v231, s2, v1
	v_med3_f32 v232, v232, s2, v1
	v_mul_f32_e32 v233, 0x43800000, v141
	v_mul_f32_e32 v226, 0x43800000, v145
	v_cvt_pk_fp8_f32 v222, v231, v232
	v_med3_f32 v233, v233, s2, v1
	v_med3_f32 v226, v226, s2, v1
	v_cvt_pk_fp8_f32 v222, v233, v226 op_sel:[0,0,1]
	v_mul_f32_e32 v231, 0x43800000, v149
	v_mul_f32_e32 v232, 0x43800000, v153
	v_med3_f32 v231, v231, s2, v1
	v_med3_f32 v232, v232, s2, v1
	v_mul_f32_e32 v233, 0x43800000, v157
	v_mul_f32_e32 v226, 0x43800000, v161
	v_cvt_pk_fp8_f32 v223, v231, v232
	v_med3_f32 v233, v233, s2, v1
	v_med3_f32 v226, v226, s2, v1
	v_cvt_pk_fp8_f32 v223, v233, v226 op_sel:[0,0,1]
	v_mul_f32_e32 v231, 0x43800000, v167
	v_mul_f32_e32 v232, 0x43800000, v171
	v_med3_f32 v231, v231, s2, v1
	v_med3_f32 v232, v232, s2, v1
	v_mul_f32_e32 v233, 0x43800000, v175
	v_mul_f32_e32 v226, 0x43800000, v179
	v_cvt_pk_fp8_f32 v224, v231, v232
	v_med3_f32 v233, v233, s2, v1
	v_med3_f32 v226, v226, s2, v1
	v_cvt_pk_fp8_f32 v224, v233, v226 op_sel:[0,0,1]
	v_mul_f32_e32 v231, 0x43800000, v183
	v_mul_f32_e32 v232, 0x43800000, v187
	v_med3_f32 v231, v231, s2, v1
	v_med3_f32 v232, v232, s2, v1
	v_mul_f32_e32 v233, 0x43800000, v205
	v_mul_f32_e32 v226, 0x43800000, v209
	v_cvt_pk_fp8_f32 v225, v231, v232
	v_med3_f32 v233, v233, s2, v1
	v_med3_f32 v226, v226, s2, v1
	v_cvt_pk_fp8_f32 v225, v233, v226 op_sel:[0,0,1]
	s_nop 1
	ds_write_b128 v237, v[222:225] offset:816
	s_waitcnt lgkmcnt(0)
	s_barrier
	global_load_dwordx4 v[130:133], v162, s[8:9] nt
	global_load_dwordx4 v[134:137], v188, s[8:9] nt
	global_load_dwordx4 v[138:141], v194, s[8:9] nt
	global_load_dwordx4 v[142:145], v250, s[8:9] nt
	global_load_dwordx4 v[146:149], v251, s[8:9] nt
	global_load_dwordx4 v[150:153], v246, s[8:9] nt
	global_load_dwordx4 v[154:157], v247, s[8:9] nt
	global_load_dwordx4 v[158:161], v248, s[8:9] nt
	global_load_dwordx4 v[164:167], v249, s[8:9] nt
	global_load_dwordx4 v[168:171], v242, s[8:9] nt
	global_load_dwordx4 v[172:175], v243, s[8:9] nt
	global_load_dwordx4 v[176:179], v244, s[8:9] nt
	global_load_dwordx4 v[180:183], v245, s[8:9] nt
	global_load_dwordx4 v[184:187], v238, s[8:9] nt
	global_load_dwordx4 v[202:205], v239, s[8:9] nt
	global_load_dwordx4 v[206:209], v240, s[8:9] nt
	s_add_u32 s8, s8, 0x400000
	s_addc_u32 s9, s9, 0
	ds_read_b128 v[210:213], v230 offset:0
	ds_read_b128 v[214:217], v230 offset:8704
	ds_read_b128 v[218:221], v230 offset:17408
	ds_read_b128 v[222:225], v230 offset:26112
	s_waitcnt lgkmcnt(3)
	global_store_dwordx4 v241, v[210:213], s[10:11] nt
	s_waitcnt lgkmcnt(2)
	global_store_dwordx4 v234, v[214:217], s[10:11] nt
	s_waitcnt lgkmcnt(1)
	global_store_dwordx4 v235, v[218:221], s[10:11] nt
	s_waitcnt lgkmcnt(0)
	global_store_dwordx4 v236, v[222:225], s[10:11] nt
	s_add_u32 s10, s10, 0x100
	s_addc_u32 s11, s11, 0
	s_waitcnt vmcnt(56)
	v_mul_f32_e32 v231, 0x43800000, v2
	v_mul_f32_e32 v232, 0x43800000, v6
	v_med3_f32 v231, v231, s2, v1
	v_med3_f32 v232, v232, s2, v1
	v_mul_f32_e32 v233, 0x43800000, v10
	v_mul_f32_e32 v226, 0x43800000, v14
	v_cvt_pk_fp8_f32 v210, v231, v232
	v_med3_f32 v233, v233, s2, v1
	v_med3_f32 v226, v226, s2, v1
	v_cvt_pk_fp8_f32 v210, v233, v226 op_sel:[0,0,1]
	s_waitcnt vmcnt(52)
	v_mul_f32_e32 v231, 0x43800000, v18
	v_mul_f32_e32 v232, 0x43800000, v22
	v_med3_f32 v231, v231, s2, v1
	v_med3_f32 v232, v232, s2, v1
	v_mul_f32_e32 v233, 0x43800000, v26
	v_mul_f32_e32 v226, 0x43800000, v30
	v_cvt_pk_fp8_f32 v211, v231, v232
	v_med3_f32 v233, v233, s2, v1
	v_med3_f32 v226, v226, s2, v1
	v_cvt_pk_fp8_f32 v211, v233, v226 op_sel:[0,0,1]
	s_waitcnt vmcnt(48)
	v_mul_f32_e32 v231, 0x43800000, v34
	v_mul_f32_e32 v232, 0x43800000, v38
	v_med3_f32 v231, v231, s2, v1
	v_med3_f32 v232, v232, s2, v1
	v_mul_f32_e32 v233, 0x43800000, v42
	v_mul_f32_e32 v226, 0x43800000, v46
	v_cvt_pk_fp8_f32 v212, v231, v232
	v_med3_f32 v233, v233, s2, v1
	v_med3_f32 v226, v226, s2, v1
	v_cvt_pk_fp8_f32 v212, v233, v226 op_sel:[0,0,1]
	s_waitcnt vmcnt(44)
	v_mul_f32_e32 v231, 0x43800000, v50
	v_mul_f32_e32 v232, 0x43800000, v54
	v_med3_f32 v231, v231, s2, v1
	v_med3_f32 v232, v232, s2, v1
	v_mul_f32_e32 v233, 0x43800000, v58
	v_mul_f32_e32 v226, 0x43800000, v62
	v_cvt_pk_fp8_f32 v213, v231, v232
	v_med3_f32 v233, v233, s2, v1
	v_med3_f32 v226, v226, s2, v1
	v_cvt_pk_fp8_f32 v213, v233, v226 op_sel:[0,0,1]
	s_nop 1
	ds_write_b128 v237, v[210:213] offset:34816
	v_mul_f32_e32 v231, 0x43800000, v3
	v_mul_f32_e32 v232, 0x43800000, v7
	v_med3_f32 v231, v231, s2, v1
	v_med3_f32 v232, v232, s2, v1
	v_mul_f32_e32 v233, 0x43800000, v11
	v_mul_f32_e32 v226, 0x43800000, v15
	v_cvt_pk_fp8_f32 v214, v231, v232
	v_med3_f32 v233, v233, s2, v1
	v_med3_f32 v226, v226, s2, v1
	v_cvt_pk_fp8_f32 v214, v233, v226 op_sel:[0,0,1]
	v_mul_f32_e32 v231, 0x43800000, v19
	v_mul_f32_e32 v232, 0x43800000, v23
	v_med3_f32 v231, v231, s2, v1
	v_med3_f32 v232, v232, s2, v1
	v_mul_f32_e32 v233, 0x43800000, v27
	v_mul_f32_e32 v226, 0x43800000, v31
	v_cvt_pk_fp8_f32 v215, v231, v232
	v_med3_f32 v233, v233, s2, v1
	v_med3_f32 v226, v226, s2, v1
	v_cvt_pk_fp8_f32 v215, v233, v226 op_sel:[0,0,1]
	v_mul_f32_e32 v231, 0x43800000, v35
	v_mul_f32_e32 v232, 0x43800000, v39
	v_med3_f32 v231, v231, s2, v1
	v_med3_f32 v232, v232, s2, v1
	v_mul_f32_e32 v233, 0x43800000, v43
	v_mul_f32_e32 v226, 0x43800000, v47
	v_cvt_pk_fp8_f32 v216, v231, v232
	v_med3_f32 v233, v233, s2, v1
	v_med3_f32 v226, v226, s2, v1
	v_cvt_pk_fp8_f32 v216, v233, v226 op_sel:[0,0,1]
	v_mul_f32_e32 v231, 0x43800000, v51
	v_mul_f32_e32 v232, 0x43800000, v55
	v_med3_f32 v231, v231, s2, v1
	v_med3_f32 v232, v232, s2, v1
	v_mul_f32_e32 v233, 0x43800000, v59
	v_mul_f32_e32 v226, 0x43800000, v63
	v_cvt_pk_fp8_f32 v217, v231, v232
	v_med3_f32 v233, v233, s2, v1
	v_med3_f32 v226, v226, s2, v1
	v_cvt_pk_fp8_f32 v217, v233, v226 op_sel:[0,0,1]
	s_nop 1
	ds_write_b128 v237, v[214:217] offset:35088
	v_mul_f32_e32 v231, 0x43800000, v4
	v_mul_f32_e32 v232, 0x43800000, v8
	v_med3_f32 v231, v231, s2, v1
	v_med3_f32 v232, v232, s2, v1
	v_mul_f32_e32 v233, 0x43800000, v12
	v_mul_f32_e32 v226, 0x43800000, v16
	v_cvt_pk_fp8_f32 v218, v231, v232
	v_med3_f32 v233, v233, s2, v1
	v_med3_f32 v226, v226, s2, v1
	v_cvt_pk_fp8_f32 v218, v233, v226 op_sel:[0,0,1]
	v_mul_f32_e32 v231, 0x43800000, v20
	v_mul_f32_e32 v232, 0x43800000, v24
	v_med3_f32 v231, v231, s2, v1
	v_med3_f32 v232, v232, s2, v1
	v_mul_f32_e32 v233, 0x43800000, v28
	v_mul_f32_e32 v226, 0x43800000, v32
	v_cvt_pk_fp8_f32 v219, v231, v232
	v_med3_f32 v233, v233, s2, v1
	v_med3_f32 v226, v226, s2, v1
	v_cvt_pk_fp8_f32 v219, v233, v226 op_sel:[0,0,1]
	v_mul_f32_e32 v231, 0x43800000, v36
	v_mul_f32_e32 v232, 0x43800000, v40
	v_med3_f32 v231, v231, s2, v1
	v_med3_f32 v232, v232, s2, v1
	v_mul_f32_e32 v233, 0x43800000, v44
	v_mul_f32_e32 v226, 0x43800000, v48
	v_cvt_pk_fp8_f32 v220, v231, v232
	v_med3_f32 v233, v233, s2, v1
	v_med3_f32 v226, v226, s2, v1
	v_cvt_pk_fp8_f32 v220, v233, v226 op_sel:[0,0,1]
	v_mul_f32_e32 v231, 0x43800000, v52
	v_mul_f32_e32 v232, 0x43800000, v56
	v_med3_f32 v231, v231, s2, v1
	v_med3_f32 v232, v232, s2, v1
	v_mul_f32_e32 v233, 0x43800000, v60
	v_mul_f32_e32 v226, 0x43800000, v64
	v_cvt_pk_fp8_f32 v221, v231, v232
	v_med3_f32 v233, v233, s2, v1
	v_med3_f32 v226, v226, s2, v1
	v_cvt_pk_fp8_f32 v221, v233, v226 op_sel:[0,0,1]
	s_nop 1
	ds_write_b128 v237, v[218:221] offset:35360
	v_mul_f32_e32 v231, 0x43800000, v5
	v_mul_f32_e32 v232, 0x43800000, v9
	v_med3_f32 v231, v231, s2, v1
	v_med3_f32 v232, v232, s2, v1
	v_mul_f32_e32 v233, 0x43800000, v13
	v_mul_f32_e32 v226, 0x43800000, v17
	v_cvt_pk_fp8_f32 v222, v231, v232
	v_med3_f32 v233, v233, s2, v1
	v_med3_f32 v226, v226, s2, v1
	v_cvt_pk_fp8_f32 v222, v233, v226 op_sel:[0,0,1]
	v_mul_f32_e32 v231, 0x43800000, v21
	v_mul_f32_e32 v232, 0x43800000, v25
	v_med3_f32 v231, v231, s2, v1
	v_med3_f32 v232, v232, s2, v1
	v_mul_f32_e32 v233, 0x43800000, v29
	v_mul_f32_e32 v226, 0x43800000, v33
	v_cvt_pk_fp8_f32 v223, v231, v232
	v_med3_f32 v233, v233, s2, v1
	v_med3_f32 v226, v226, s2, v1
	v_cvt_pk_fp8_f32 v223, v233, v226 op_sel:[0,0,1]
	v_mul_f32_e32 v231, 0x43800000, v37
	v_mul_f32_e32 v232, 0x43800000, v41
	v_med3_f32 v231, v231, s2, v1
	v_med3_f32 v232, v232, s2, v1
	v_mul_f32_e32 v233, 0x43800000, v45
	v_mul_f32_e32 v226, 0x43800000, v49
	v_cvt_pk_fp8_f32 v224, v231, v232
	v_med3_f32 v233, v233, s2, v1
	v_med3_f32 v226, v226, s2, v1
	v_cvt_pk_fp8_f32 v224, v233, v226 op_sel:[0,0,1]
	v_mul_f32_e32 v231, 0x43800000, v53
	v_mul_f32_e32 v232, 0x43800000, v57
	v_med3_f32 v231, v231, s2, v1
	v_med3_f32 v232, v232, s2, v1
	v_mul_f32_e32 v233, 0x43800000, v61
	v_mul_f32_e32 v226, 0x43800000, v65
	v_cvt_pk_fp8_f32 v225, v231, v232
	v_med3_f32 v233, v233, s2, v1
	v_med3_f32 v226, v226, s2, v1
	v_cvt_pk_fp8_f32 v225, v233, v226 op_sel:[0,0,1]
	s_nop 1
	ds_write_b128 v237, v[222:225] offset:35632
	s_waitcnt lgkmcnt(0)
	s_barrier
	global_load_dwordx4 v[2:5], v162, s[8:9] nt
	global_load_dwordx4 v[6:9], v188, s[8:9] nt
	global_load_dwordx4 v[10:13], v194, s[8:9] nt
	global_load_dwordx4 v[14:17], v250, s[8:9] nt
	global_load_dwordx4 v[18:21], v251, s[8:9] nt
	global_load_dwordx4 v[22:25], v246, s[8:9] nt
	global_load_dwordx4 v[26:29], v247, s[8:9] nt
	global_load_dwordx4 v[30:33], v248, s[8:9] nt
	global_load_dwordx4 v[34:37], v249, s[8:9] nt
	global_load_dwordx4 v[38:41], v242, s[8:9] nt
	global_load_dwordx4 v[42:45], v243, s[8:9] nt
	global_load_dwordx4 v[46:49], v244, s[8:9] nt
	global_load_dwordx4 v[50:53], v245, s[8:9] nt
	global_load_dwordx4 v[54:57], v238, s[8:9] nt
	global_load_dwordx4 v[58:61], v239, s[8:9] nt
	global_load_dwordx4 v[62:65], v240, s[8:9] nt
	s_add_u32 s8, s8, 0x400000
	s_addc_u32 s9, s9, 0
	ds_read_b128 v[210:213], v230 offset:34816
	ds_read_b128 v[214:217], v230 offset:43520
	ds_read_b128 v[218:221], v230 offset:52224
	ds_read_b128 v[222:225], v230 offset:60928
	s_waitcnt lgkmcnt(3)
	global_store_dwordx4 v241, v[210:213], s[10:11] nt
	s_waitcnt lgkmcnt(2)
	global_store_dwordx4 v234, v[214:217], s[10:11] nt
	s_waitcnt lgkmcnt(1)
	global_store_dwordx4 v235, v[218:221], s[10:11] nt
	s_waitcnt lgkmcnt(0)
	global_store_dwordx4 v236, v[222:225], s[10:11] nt
	s_add_u32 s10, s10, 0x100
	s_addc_u32 s11, s11, 0
	s_waitcnt vmcnt(56)
	v_mul_f32_e32 v231, 0x43800000, v66
	v_mul_f32_e32 v232, 0x43800000, v70
	v_med3_f32 v231, v231, s2, v1
	v_med3_f32 v232, v232, s2, v1
	v_mul_f32_e32 v233, 0x43800000, v74
	v_mul_f32_e32 v226, 0x43800000, v78
	v_cvt_pk_fp8_f32 v210, v231, v232
	v_med3_f32 v233, v233, s2, v1
	v_med3_f32 v226, v226, s2, v1
	v_cvt_pk_fp8_f32 v210, v233, v226 op_sel:[0,0,1]
	s_waitcnt vmcnt(52)
	v_mul_f32_e32 v231, 0x43800000, v82
	v_mul_f32_e32 v232, 0x43800000, v86
	v_med3_f32 v231, v231, s2, v1
	v_med3_f32 v232, v232, s2, v1
	v_mul_f32_e32 v233, 0x43800000, v90
	v_mul_f32_e32 v226, 0x43800000, v94
	v_cvt_pk_fp8_f32 v211, v231, v232
	v_med3_f32 v233, v233, s2, v1
	v_med3_f32 v226, v226, s2, v1
	v_cvt_pk_fp8_f32 v211, v233, v226 op_sel:[0,0,1]
	s_waitcnt vmcnt(48)
	v_mul_f32_e32 v231, 0x43800000, v98
	v_mul_f32_e32 v232, 0x43800000, v102
	v_med3_f32 v231, v231, s2, v1
	v_med3_f32 v232, v232, s2, v1
	v_mul_f32_e32 v233, 0x43800000, v106
	v_mul_f32_e32 v226, 0x43800000, v110
	v_cvt_pk_fp8_f32 v212, v231, v232
	v_med3_f32 v233, v233, s2, v1
	v_med3_f32 v226, v226, s2, v1
	v_cvt_pk_fp8_f32 v212, v233, v226 op_sel:[0,0,1]
	s_waitcnt vmcnt(44)
	v_mul_f32_e32 v231, 0x43800000, v114
	v_mul_f32_e32 v232, 0x43800000, v118
	v_med3_f32 v231, v231, s2, v1
	v_med3_f32 v232, v232, s2, v1
	v_mul_f32_e32 v233, 0x43800000, v122
	v_mul_f32_e32 v226, 0x43800000, v126
	v_cvt_pk_fp8_f32 v213, v231, v232
	v_med3_f32 v233, v233, s2, v1
	v_med3_f32 v226, v226, s2, v1
	v_cvt_pk_fp8_f32 v213, v233, v226 op_sel:[0,0,1]
	s_nop 1
	ds_write_b128 v237, v[210:213] offset:0
	v_mul_f32_e32 v231, 0x43800000, v67
	v_mul_f32_e32 v232, 0x43800000, v71
	v_med3_f32 v231, v231, s2, v1
	v_med3_f32 v232, v232, s2, v1
	v_mul_f32_e32 v233, 0x43800000, v75
	v_mul_f32_e32 v226, 0x43800000, v79
	v_cvt_pk_fp8_f32 v214, v231, v232
	v_med3_f32 v233, v233, s2, v1
	v_med3_f32 v226, v226, s2, v1
	v_cvt_pk_fp8_f32 v214, v233, v226 op_sel:[0,0,1]
	v_mul_f32_e32 v231, 0x43800000, v83
	v_mul_f32_e32 v232, 0x43800000, v87
	v_med3_f32 v231, v231, s2, v1
	v_med3_f32 v232, v232, s2, v1
	v_mul_f32_e32 v233, 0x43800000, v91
	v_mul_f32_e32 v226, 0x43800000, v95
	v_cvt_pk_fp8_f32 v215, v231, v232
	v_med3_f32 v233, v233, s2, v1
	v_med3_f32 v226, v226, s2, v1
	v_cvt_pk_fp8_f32 v215, v233, v226 op_sel:[0,0,1]
	v_mul_f32_e32 v231, 0x43800000, v99
	v_mul_f32_e32 v232, 0x43800000, v103
	v_med3_f32 v231, v231, s2, v1
	v_med3_f32 v232, v232, s2, v1
	v_mul_f32_e32 v233, 0x43800000, v107
	v_mul_f32_e32 v226, 0x43800000, v111
	v_cvt_pk_fp8_f32 v216, v231, v232
	v_med3_f32 v233, v233, s2, v1
	v_med3_f32 v226, v226, s2, v1
	v_cvt_pk_fp8_f32 v216, v233, v226 op_sel:[0,0,1]
	v_mul_f32_e32 v231, 0x43800000, v115
	v_mul_f32_e32 v232, 0x43800000, v119
	v_med3_f32 v231, v231, s2, v1
	v_med3_f32 v232, v232, s2, v1
	v_mul_f32_e32 v233, 0x43800000, v123
	v_mul_f32_e32 v226, 0x43800000, v127
	v_cvt_pk_fp8_f32 v217, v231, v232
	v_med3_f32 v233, v233, s2, v1
	v_med3_f32 v226, v226, s2, v1
	v_cvt_pk_fp8_f32 v217, v233, v226 op_sel:[0,0,1]
	s_nop 1
	ds_write_b128 v237, v[214:217] offset:272
	v_mul_f32_e32 v231, 0x43800000, v68
	v_mul_f32_e32 v232, 0x43800000, v72
	v_med3_f32 v231, v231, s2, v1
	v_med3_f32 v232, v232, s2, v1
	v_mul_f32_e32 v233, 0x43800000, v76
	v_mul_f32_e32 v226, 0x43800000, v80
	v_cvt_pk_fp8_f32 v218, v231, v232
	v_med3_f32 v233, v233, s2, v1
	v_med3_f32 v226, v226, s2, v1
	v_cvt_pk_fp8_f32 v218, v233, v226 op_sel:[0,0,1]
	v_mul_f32_e32 v231, 0x43800000, v84
	v_mul_f32_e32 v232, 0x43800000, v88
	v_med3_f32 v231, v231, s2, v1
	v_med3_f32 v232, v232, s2, v1
	v_mul_f32_e32 v233, 0x43800000, v92
	v_mul_f32_e32 v226, 0x43800000, v96
	v_cvt_pk_fp8_f32 v219, v231, v232
	v_med3_f32 v233, v233, s2, v1
	v_med3_f32 v226, v226, s2, v1
	v_cvt_pk_fp8_f32 v219, v233, v226 op_sel:[0,0,1]
	v_mul_f32_e32 v231, 0x43800000, v100
	v_mul_f32_e32 v232, 0x43800000, v104
	v_med3_f32 v231, v231, s2, v1
	v_med3_f32 v232, v232, s2, v1
	v_mul_f32_e32 v233, 0x43800000, v108
	v_mul_f32_e32 v226, 0x43800000, v112
	v_cvt_pk_fp8_f32 v220, v231, v232
	v_med3_f32 v233, v233, s2, v1
	v_med3_f32 v226, v226, s2, v1
	v_cvt_pk_fp8_f32 v220, v233, v226 op_sel:[0,0,1]
	v_mul_f32_e32 v231, 0x43800000, v116
	v_mul_f32_e32 v232, 0x43800000, v120
	v_med3_f32 v231, v231, s2, v1
	v_med3_f32 v232, v232, s2, v1
	v_mul_f32_e32 v233, 0x43800000, v124
	v_mul_f32_e32 v226, 0x43800000, v128
	v_cvt_pk_fp8_f32 v221, v231, v232
	v_med3_f32 v233, v233, s2, v1
	v_med3_f32 v226, v226, s2, v1
	v_cvt_pk_fp8_f32 v221, v233, v226 op_sel:[0,0,1]
	s_nop 1
	ds_write_b128 v237, v[218:221] offset:544
	v_mul_f32_e32 v231, 0x43800000, v69
	v_mul_f32_e32 v232, 0x43800000, v73
	v_med3_f32 v231, v231, s2, v1
	v_med3_f32 v232, v232, s2, v1
	v_mul_f32_e32 v233, 0x43800000, v77
	v_mul_f32_e32 v226, 0x43800000, v81
	v_cvt_pk_fp8_f32 v222, v231, v232
	v_med3_f32 v233, v233, s2, v1
	v_med3_f32 v226, v226, s2, v1
	v_cvt_pk_fp8_f32 v222, v233, v226 op_sel:[0,0,1]
	v_mul_f32_e32 v231, 0x43800000, v85
	v_mul_f32_e32 v232, 0x43800000, v89
	v_med3_f32 v231, v231, s2, v1
	v_med3_f32 v232, v232, s2, v1
	v_mul_f32_e32 v233, 0x43800000, v93
	v_mul_f32_e32 v226, 0x43800000, v97
	v_cvt_pk_fp8_f32 v223, v231, v232
	v_med3_f32 v233, v233, s2, v1
	v_med3_f32 v226, v226, s2, v1
	v_cvt_pk_fp8_f32 v223, v233, v226 op_sel:[0,0,1]
	v_mul_f32_e32 v231, 0x43800000, v101
	v_mul_f32_e32 v232, 0x43800000, v105
	v_med3_f32 v231, v231, s2, v1
	v_med3_f32 v232, v232, s2, v1
	v_mul_f32_e32 v233, 0x43800000, v109
	v_mul_f32_e32 v226, 0x43800000, v113
	v_cvt_pk_fp8_f32 v224, v231, v232
	v_med3_f32 v233, v233, s2, v1
	v_med3_f32 v226, v226, s2, v1
	v_cvt_pk_fp8_f32 v224, v233, v226 op_sel:[0,0,1]
	v_mul_f32_e32 v231, 0x43800000, v117
	v_mul_f32_e32 v232, 0x43800000, v121
	v_med3_f32 v231, v231, s2, v1
	v_med3_f32 v232, v232, s2, v1
	v_mul_f32_e32 v233, 0x43800000, v125
	v_mul_f32_e32 v226, 0x43800000, v129
	v_cvt_pk_fp8_f32 v225, v231, v232
	v_med3_f32 v233, v233, s2, v1
	v_med3_f32 v226, v226, s2, v1
	v_cvt_pk_fp8_f32 v225, v233, v226 op_sel:[0,0,1]
	s_nop 1
	ds_write_b128 v237, v[222:225] offset:816
	s_waitcnt lgkmcnt(0)
	s_barrier
	global_load_dwordx4 v[66:69], v162, s[8:9] nt
	global_load_dwordx4 v[70:73], v188, s[8:9] nt
	global_load_dwordx4 v[74:77], v194, s[8:9] nt
	global_load_dwordx4 v[78:81], v250, s[8:9] nt
	global_load_dwordx4 v[82:85], v251, s[8:9] nt
	global_load_dwordx4 v[86:89], v246, s[8:9] nt
	global_load_dwordx4 v[90:93], v247, s[8:9] nt
	global_load_dwordx4 v[94:97], v248, s[8:9] nt
	global_load_dwordx4 v[98:101], v249, s[8:9] nt
	global_load_dwordx4 v[102:105], v242, s[8:9] nt
	global_load_dwordx4 v[106:109], v243, s[8:9] nt
	global_load_dwordx4 v[110:113], v244, s[8:9] nt
	global_load_dwordx4 v[114:117], v245, s[8:9] nt
	global_load_dwordx4 v[118:121], v238, s[8:9] nt
	global_load_dwordx4 v[122:125], v239, s[8:9] nt
	global_load_dwordx4 v[126:129], v240, s[8:9] nt
	s_add_u32 s8, s8, 0x400000
	s_addc_u32 s9, s9, 0
	ds_read_b128 v[210:213], v230 offset:0
	ds_read_b128 v[214:217], v230 offset:8704
	ds_read_b128 v[218:221], v230 offset:17408
	ds_read_b128 v[222:225], v230 offset:26112
	s_waitcnt lgkmcnt(3)
	global_store_dwordx4 v241, v[210:213], s[10:11] nt
	s_waitcnt lgkmcnt(2)
	global_store_dwordx4 v234, v[214:217], s[10:11] nt
	s_waitcnt lgkmcnt(1)
	global_store_dwordx4 v235, v[218:221], s[10:11] nt
	s_waitcnt lgkmcnt(0)
	global_store_dwordx4 v236, v[222:225], s[10:11] nt
	s_add_u32 s10, s10, 0x100
	s_addc_u32 s11, s11, 0
	s_waitcnt vmcnt(56)
	v_mul_f32_e32 v231, 0x43800000, v130
	v_mul_f32_e32 v232, 0x43800000, v134
	v_med3_f32 v231, v231, s2, v1
	v_med3_f32 v232, v232, s2, v1
	v_mul_f32_e32 v233, 0x43800000, v138
	v_mul_f32_e32 v226, 0x43800000, v142
	v_cvt_pk_fp8_f32 v210, v231, v232
	v_med3_f32 v233, v233, s2, v1
	v_med3_f32 v226, v226, s2, v1
	v_cvt_pk_fp8_f32 v210, v233, v226 op_sel:[0,0,1]
	s_waitcnt vmcnt(52)
	v_mul_f32_e32 v231, 0x43800000, v146
	v_mul_f32_e32 v232, 0x43800000, v150
	v_med3_f32 v231, v231, s2, v1
	v_med3_f32 v232, v232, s2, v1
	v_mul_f32_e32 v233, 0x43800000, v154
	v_mul_f32_e32 v226, 0x43800000, v158
	v_cvt_pk_fp8_f32 v211, v231, v232
	v_med3_f32 v233, v233, s2, v1
	v_med3_f32 v226, v226, s2, v1
	v_cvt_pk_fp8_f32 v211, v233, v226 op_sel:[0,0,1]
	s_waitcnt vmcnt(48)
	v_mul_f32_e32 v231, 0x43800000, v164
	v_mul_f32_e32 v232, 0x43800000, v168
	v_med3_f32 v231, v231, s2, v1
	v_med3_f32 v232, v232, s2, v1
	v_mul_f32_e32 v233, 0x43800000, v172
	v_mul_f32_e32 v226, 0x43800000, v176
	v_cvt_pk_fp8_f32 v212, v231, v232
	v_med3_f32 v233, v233, s2, v1
	v_med3_f32 v226, v226, s2, v1
	v_cvt_pk_fp8_f32 v212, v233, v226 op_sel:[0,0,1]
	s_waitcnt vmcnt(44)
	v_mul_f32_e32 v231, 0x43800000, v180
	v_mul_f32_e32 v232, 0x43800000, v184
	v_med3_f32 v231, v231, s2, v1
	v_med3_f32 v232, v232, s2, v1
	v_mul_f32_e32 v233, 0x43800000, v202
	v_mul_f32_e32 v226, 0x43800000, v206
	v_cvt_pk_fp8_f32 v213, v231, v232
	v_med3_f32 v233, v233, s2, v1
	v_med3_f32 v226, v226, s2, v1
	v_cvt_pk_fp8_f32 v213, v233, v226 op_sel:[0,0,1]
	s_nop 1
	ds_write_b128 v237, v[210:213] offset:34816
	v_mul_f32_e32 v231, 0x43800000, v131
	v_mul_f32_e32 v232, 0x43800000, v135
	v_med3_f32 v231, v231, s2, v1
	v_med3_f32 v232, v232, s2, v1
	v_mul_f32_e32 v233, 0x43800000, v139
	v_mul_f32_e32 v226, 0x43800000, v143
	v_cvt_pk_fp8_f32 v214, v231, v232
	v_med3_f32 v233, v233, s2, v1
	v_med3_f32 v226, v226, s2, v1
	v_cvt_pk_fp8_f32 v214, v233, v226 op_sel:[0,0,1]
	v_mul_f32_e32 v231, 0x43800000, v147
	v_mul_f32_e32 v232, 0x43800000, v151
	v_med3_f32 v231, v231, s2, v1
	v_med3_f32 v232, v232, s2, v1
	v_mul_f32_e32 v233, 0x43800000, v155
	v_mul_f32_e32 v226, 0x43800000, v159
	v_cvt_pk_fp8_f32 v215, v231, v232
	v_med3_f32 v233, v233, s2, v1
	v_med3_f32 v226, v226, s2, v1
	v_cvt_pk_fp8_f32 v215, v233, v226 op_sel:[0,0,1]
	v_mul_f32_e32 v231, 0x43800000, v165
	v_mul_f32_e32 v232, 0x43800000, v169
	v_med3_f32 v231, v231, s2, v1
	v_med3_f32 v232, v232, s2, v1
	v_mul_f32_e32 v233, 0x43800000, v173
	v_mul_f32_e32 v226, 0x43800000, v177
	v_cvt_pk_fp8_f32 v216, v231, v232
	v_med3_f32 v233, v233, s2, v1
	v_med3_f32 v226, v226, s2, v1
	v_cvt_pk_fp8_f32 v216, v233, v226 op_sel:[0,0,1]
	v_mul_f32_e32 v231, 0x43800000, v181
	v_mul_f32_e32 v232, 0x43800000, v185
	v_med3_f32 v231, v231, s2, v1
	v_med3_f32 v232, v232, s2, v1
	v_mul_f32_e32 v233, 0x43800000, v203
	v_mul_f32_e32 v226, 0x43800000, v207
	v_cvt_pk_fp8_f32 v217, v231, v232
	v_med3_f32 v233, v233, s2, v1
	v_med3_f32 v226, v226, s2, v1
	v_cvt_pk_fp8_f32 v217, v233, v226 op_sel:[0,0,1]
	s_nop 1
	ds_write_b128 v237, v[214:217] offset:35088
	v_mul_f32_e32 v231, 0x43800000, v132
	v_mul_f32_e32 v232, 0x43800000, v136
	v_med3_f32 v231, v231, s2, v1
	v_med3_f32 v232, v232, s2, v1
	v_mul_f32_e32 v233, 0x43800000, v140
	v_mul_f32_e32 v226, 0x43800000, v144
	v_cvt_pk_fp8_f32 v218, v231, v232
	v_med3_f32 v233, v233, s2, v1
	v_med3_f32 v226, v226, s2, v1
	v_cvt_pk_fp8_f32 v218, v233, v226 op_sel:[0,0,1]
	v_mul_f32_e32 v231, 0x43800000, v148
	v_mul_f32_e32 v232, 0x43800000, v152
	v_med3_f32 v231, v231, s2, v1
	v_med3_f32 v232, v232, s2, v1
	v_mul_f32_e32 v233, 0x43800000, v156
	v_mul_f32_e32 v226, 0x43800000, v160
	v_cvt_pk_fp8_f32 v219, v231, v232
	v_med3_f32 v233, v233, s2, v1
	v_med3_f32 v226, v226, s2, v1
	v_cvt_pk_fp8_f32 v219, v233, v226 op_sel:[0,0,1]
	v_mul_f32_e32 v231, 0x43800000, v166
	v_mul_f32_e32 v232, 0x43800000, v170
	v_med3_f32 v231, v231, s2, v1
	v_med3_f32 v232, v232, s2, v1
	v_mul_f32_e32 v233, 0x43800000, v174
	v_mul_f32_e32 v226, 0x43800000, v178
	v_cvt_pk_fp8_f32 v220, v231, v232
	v_med3_f32 v233, v233, s2, v1
	v_med3_f32 v226, v226, s2, v1
	v_cvt_pk_fp8_f32 v220, v233, v226 op_sel:[0,0,1]
	v_mul_f32_e32 v231, 0x43800000, v182
	v_mul_f32_e32 v232, 0x43800000, v186
	v_med3_f32 v231, v231, s2, v1
	v_med3_f32 v232, v232, s2, v1
	v_mul_f32_e32 v233, 0x43800000, v204
	v_mul_f32_e32 v226, 0x43800000, v208
	v_cvt_pk_fp8_f32 v221, v231, v232
	v_med3_f32 v233, v233, s2, v1
	v_med3_f32 v226, v226, s2, v1
	v_cvt_pk_fp8_f32 v221, v233, v226 op_sel:[0,0,1]
	s_nop 1
	ds_write_b128 v237, v[218:221] offset:35360
	v_mul_f32_e32 v231, 0x43800000, v133
	v_mul_f32_e32 v232, 0x43800000, v137
	v_med3_f32 v231, v231, s2, v1
	v_med3_f32 v232, v232, s2, v1
	v_mul_f32_e32 v233, 0x43800000, v141
	v_mul_f32_e32 v226, 0x43800000, v145
	v_cvt_pk_fp8_f32 v222, v231, v232
	v_med3_f32 v233, v233, s2, v1
	v_med3_f32 v226, v226, s2, v1
	v_cvt_pk_fp8_f32 v222, v233, v226 op_sel:[0,0,1]
	v_mul_f32_e32 v231, 0x43800000, v149
	v_mul_f32_e32 v232, 0x43800000, v153
	v_med3_f32 v231, v231, s2, v1
	v_med3_f32 v232, v232, s2, v1
	v_mul_f32_e32 v233, 0x43800000, v157
	v_mul_f32_e32 v226, 0x43800000, v161
	v_cvt_pk_fp8_f32 v223, v231, v232
	v_med3_f32 v233, v233, s2, v1
	v_med3_f32 v226, v226, s2, v1
	v_cvt_pk_fp8_f32 v223, v233, v226 op_sel:[0,0,1]
	v_mul_f32_e32 v231, 0x43800000, v167
	v_mul_f32_e32 v232, 0x43800000, v171
	v_med3_f32 v231, v231, s2, v1
	v_med3_f32 v232, v232, s2, v1
	v_mul_f32_e32 v233, 0x43800000, v175
	v_mul_f32_e32 v226, 0x43800000, v179
	v_cvt_pk_fp8_f32 v224, v231, v232
	v_med3_f32 v233, v233, s2, v1
	v_med3_f32 v226, v226, s2, v1
	v_cvt_pk_fp8_f32 v224, v233, v226 op_sel:[0,0,1]
	v_mul_f32_e32 v231, 0x43800000, v183
	v_mul_f32_e32 v232, 0x43800000, v187
	v_med3_f32 v231, v231, s2, v1
	v_med3_f32 v232, v232, s2, v1
	v_mul_f32_e32 v233, 0x43800000, v205
	v_mul_f32_e32 v226, 0x43800000, v209
	v_cvt_pk_fp8_f32 v225, v231, v232
	v_med3_f32 v233, v233, s2, v1
	v_med3_f32 v226, v226, s2, v1
	v_cvt_pk_fp8_f32 v225, v233, v226 op_sel:[0,0,1]
	s_nop 1
	ds_write_b128 v237, v[222:225] offset:35632
	s_waitcnt lgkmcnt(0)
	s_barrier
	ds_read_b128 v[210:213], v230 offset:34816
	ds_read_b128 v[214:217], v230 offset:43520
	ds_read_b128 v[218:221], v230 offset:52224
	ds_read_b128 v[222:225], v230 offset:60928
	s_waitcnt lgkmcnt(3)
	global_store_dwordx4 v241, v[210:213], s[10:11] nt
	s_waitcnt lgkmcnt(2)
	global_store_dwordx4 v234, v[214:217], s[10:11] nt
	s_waitcnt lgkmcnt(1)
	global_store_dwordx4 v235, v[218:221], s[10:11] nt
	s_waitcnt lgkmcnt(0)
	global_store_dwordx4 v236, v[222:225], s[10:11] nt
	s_add_u32 s10, s10, 0x100
	s_addc_u32 s11, s11, 0
	s_waitcnt vmcnt(40)
	v_mul_f32_e32 v231, 0x43800000, v2
	v_mul_f32_e32 v232, 0x43800000, v6
	v_med3_f32 v231, v231, s2, v1
	v_med3_f32 v232, v232, s2, v1
	v_mul_f32_e32 v233, 0x43800000, v10
	v_mul_f32_e32 v226, 0x43800000, v14
	v_cvt_pk_fp8_f32 v210, v231, v232
	v_med3_f32 v233, v233, s2, v1
	v_med3_f32 v226, v226, s2, v1
	v_cvt_pk_fp8_f32 v210, v233, v226 op_sel:[0,0,1]
	s_waitcnt vmcnt(36)
	v_mul_f32_e32 v231, 0x43800000, v18
	v_mul_f32_e32 v232, 0x43800000, v22
	v_med3_f32 v231, v231, s2, v1
	v_med3_f32 v232, v232, s2, v1
	v_mul_f32_e32 v233, 0x43800000, v26
	v_mul_f32_e32 v226, 0x43800000, v30
	v_cvt_pk_fp8_f32 v211, v231, v232
	v_med3_f32 v233, v233, s2, v1
	v_med3_f32 v226, v226, s2, v1
	v_cvt_pk_fp8_f32 v211, v233, v226 op_sel:[0,0,1]
	s_waitcnt vmcnt(32)
	v_mul_f32_e32 v231, 0x43800000, v34
	v_mul_f32_e32 v232, 0x43800000, v38
	v_med3_f32 v231, v231, s2, v1
	v_med3_f32 v232, v232, s2, v1
	v_mul_f32_e32 v233, 0x43800000, v42
	v_mul_f32_e32 v226, 0x43800000, v46
	v_cvt_pk_fp8_f32 v212, v231, v232
	v_med3_f32 v233, v233, s2, v1
	v_med3_f32 v226, v226, s2, v1
	v_cvt_pk_fp8_f32 v212, v233, v226 op_sel:[0,0,1]
	s_waitcnt vmcnt(28)
	v_mul_f32_e32 v231, 0x43800000, v50
	v_mul_f32_e32 v232, 0x43800000, v54
	v_med3_f32 v231, v231, s2, v1
	v_med3_f32 v232, v232, s2, v1
	v_mul_f32_e32 v233, 0x43800000, v58
	v_mul_f32_e32 v226, 0x43800000, v62
	v_cvt_pk_fp8_f32 v213, v231, v232
	v_med3_f32 v233, v233, s2, v1
	v_med3_f32 v226, v226, s2, v1
	v_cvt_pk_fp8_f32 v213, v233, v226 op_sel:[0,0,1]
	s_nop 1
	ds_write_b128 v237, v[210:213] offset:0
	v_mul_f32_e32 v231, 0x43800000, v3
	v_mul_f32_e32 v232, 0x43800000, v7
	v_med3_f32 v231, v231, s2, v1
	v_med3_f32 v232, v232, s2, v1
	v_mul_f32_e32 v233, 0x43800000, v11
	v_mul_f32_e32 v226, 0x43800000, v15
	v_cvt_pk_fp8_f32 v214, v231, v232
	v_med3_f32 v233, v233, s2, v1
	v_med3_f32 v226, v226, s2, v1
	v_cvt_pk_fp8_f32 v214, v233, v226 op_sel:[0,0,1]
	v_mul_f32_e32 v231, 0x43800000, v19
	v_mul_f32_e32 v232, 0x43800000, v23
	v_med3_f32 v231, v231, s2, v1
	v_med3_f32 v232, v232, s2, v1
	v_mul_f32_e32 v233, 0x43800000, v27
	v_mul_f32_e32 v226, 0x43800000, v31
	v_cvt_pk_fp8_f32 v215, v231, v232
	v_med3_f32 v233, v233, s2, v1
	v_med3_f32 v226, v226, s2, v1
	v_cvt_pk_fp8_f32 v215, v233, v226 op_sel:[0,0,1]
	v_mul_f32_e32 v231, 0x43800000, v35
	v_mul_f32_e32 v232, 0x43800000, v39
	v_med3_f32 v231, v231, s2, v1
	v_med3_f32 v232, v232, s2, v1
	v_mul_f32_e32 v233, 0x43800000, v43
	v_mul_f32_e32 v226, 0x43800000, v47
	v_cvt_pk_fp8_f32 v216, v231, v232
	v_med3_f32 v233, v233, s2, v1
	v_med3_f32 v226, v226, s2, v1
	v_cvt_pk_fp8_f32 v216, v233, v226 op_sel:[0,0,1]
	v_mul_f32_e32 v231, 0x43800000, v51
	v_mul_f32_e32 v232, 0x43800000, v55
	v_med3_f32 v231, v231, s2, v1
	v_med3_f32 v232, v232, s2, v1
	v_mul_f32_e32 v233, 0x43800000, v59
	v_mul_f32_e32 v226, 0x43800000, v63
	v_cvt_pk_fp8_f32 v217, v231, v232
	v_med3_f32 v233, v233, s2, v1
	v_med3_f32 v226, v226, s2, v1
	v_cvt_pk_fp8_f32 v217, v233, v226 op_sel:[0,0,1]
	s_nop 1
	ds_write_b128 v237, v[214:217] offset:272
	v_mul_f32_e32 v231, 0x43800000, v4
	v_mul_f32_e32 v232, 0x43800000, v8
	v_med3_f32 v231, v231, s2, v1
	v_med3_f32 v232, v232, s2, v1
	v_mul_f32_e32 v233, 0x43800000, v12
	v_mul_f32_e32 v226, 0x43800000, v16
	v_cvt_pk_fp8_f32 v218, v231, v232
	v_med3_f32 v233, v233, s2, v1
	v_med3_f32 v226, v226, s2, v1
	v_cvt_pk_fp8_f32 v218, v233, v226 op_sel:[0,0,1]
	v_mul_f32_e32 v231, 0x43800000, v20
	v_mul_f32_e32 v232, 0x43800000, v24
	v_med3_f32 v231, v231, s2, v1
	v_med3_f32 v232, v232, s2, v1
	v_mul_f32_e32 v233, 0x43800000, v28
	v_mul_f32_e32 v226, 0x43800000, v32
	v_cvt_pk_fp8_f32 v219, v231, v232
	v_med3_f32 v233, v233, s2, v1
	v_med3_f32 v226, v226, s2, v1
	v_cvt_pk_fp8_f32 v219, v233, v226 op_sel:[0,0,1]
	v_mul_f32_e32 v231, 0x43800000, v36
	v_mul_f32_e32 v232, 0x43800000, v40
	v_med3_f32 v231, v231, s2, v1
	v_med3_f32 v232, v232, s2, v1
	v_mul_f32_e32 v233, 0x43800000, v44
	v_mul_f32_e32 v226, 0x43800000, v48
	v_cvt_pk_fp8_f32 v220, v231, v232
	v_med3_f32 v233, v233, s2, v1
	v_med3_f32 v226, v226, s2, v1
	v_cvt_pk_fp8_f32 v220, v233, v226 op_sel:[0,0,1]
	v_mul_f32_e32 v231, 0x43800000, v52
	v_mul_f32_e32 v232, 0x43800000, v56
	v_med3_f32 v231, v231, s2, v1
	v_med3_f32 v232, v232, s2, v1
	v_mul_f32_e32 v233, 0x43800000, v60
	v_mul_f32_e32 v226, 0x43800000, v64
	v_cvt_pk_fp8_f32 v221, v231, v232
	v_med3_f32 v233, v233, s2, v1
	v_med3_f32 v226, v226, s2, v1
	v_cvt_pk_fp8_f32 v221, v233, v226 op_sel:[0,0,1]
	s_nop 1
	ds_write_b128 v237, v[218:221] offset:544
	v_mul_f32_e32 v231, 0x43800000, v5
	v_mul_f32_e32 v232, 0x43800000, v9
	v_med3_f32 v231, v231, s2, v1
	v_med3_f32 v232, v232, s2, v1
	v_mul_f32_e32 v233, 0x43800000, v13
	v_mul_f32_e32 v226, 0x43800000, v17
	v_cvt_pk_fp8_f32 v222, v231, v232
	v_med3_f32 v233, v233, s2, v1
	v_med3_f32 v226, v226, s2, v1
	v_cvt_pk_fp8_f32 v222, v233, v226 op_sel:[0,0,1]
	v_mul_f32_e32 v231, 0x43800000, v21
	v_mul_f32_e32 v232, 0x43800000, v25
	v_med3_f32 v231, v231, s2, v1
	v_med3_f32 v232, v232, s2, v1
	v_mul_f32_e32 v233, 0x43800000, v29
	v_mul_f32_e32 v226, 0x43800000, v33
	v_cvt_pk_fp8_f32 v223, v231, v232
	v_med3_f32 v233, v233, s2, v1
	v_med3_f32 v226, v226, s2, v1
	v_cvt_pk_fp8_f32 v223, v233, v226 op_sel:[0,0,1]
	v_mul_f32_e32 v231, 0x43800000, v37
	v_mul_f32_e32 v232, 0x43800000, v41
	v_med3_f32 v231, v231, s2, v1
	v_med3_f32 v232, v232, s2, v1
	v_mul_f32_e32 v233, 0x43800000, v45
	v_mul_f32_e32 v226, 0x43800000, v49
	v_cvt_pk_fp8_f32 v224, v231, v232
	v_med3_f32 v233, v233, s2, v1
	v_med3_f32 v226, v226, s2, v1
	v_cvt_pk_fp8_f32 v224, v233, v226 op_sel:[0,0,1]
	v_mul_f32_e32 v231, 0x43800000, v53
	v_mul_f32_e32 v232, 0x43800000, v57
	v_med3_f32 v231, v231, s2, v1
	v_med3_f32 v232, v232, s2, v1
	v_mul_f32_e32 v233, 0x43800000, v61
	v_mul_f32_e32 v226, 0x43800000, v65
	v_cvt_pk_fp8_f32 v225, v231, v232
	v_med3_f32 v233, v233, s2, v1
	v_med3_f32 v226, v226, s2, v1
	v_cvt_pk_fp8_f32 v225, v233, v226 op_sel:[0,0,1]
	s_nop 1
	ds_write_b128 v237, v[222:225] offset:816
	s_waitcnt lgkmcnt(0)
	s_barrier
	ds_read_b128 v[210:213], v230 offset:0
	ds_read_b128 v[214:217], v230 offset:8704
	ds_read_b128 v[218:221], v230 offset:17408
	ds_read_b128 v[222:225], v230 offset:26112
	s_waitcnt lgkmcnt(3)
	global_store_dwordx4 v241, v[210:213], s[10:11] nt
	s_waitcnt lgkmcnt(2)
	global_store_dwordx4 v234, v[214:217], s[10:11] nt
	s_waitcnt lgkmcnt(1)
	global_store_dwordx4 v235, v[218:221], s[10:11] nt
	s_waitcnt lgkmcnt(0)
	global_store_dwordx4 v236, v[222:225], s[10:11] nt
	s_add_u32 s10, s10, 0x100
	s_addc_u32 s11, s11, 0
	s_waitcnt vmcnt(24)
	v_mul_f32_e32 v231, 0x43800000, v66
	v_mul_f32_e32 v232, 0x43800000, v70
	v_med3_f32 v231, v231, s2, v1
	v_med3_f32 v232, v232, s2, v1
	v_mul_f32_e32 v233, 0x43800000, v74
	v_mul_f32_e32 v226, 0x43800000, v78
	v_cvt_pk_fp8_f32 v210, v231, v232
	v_med3_f32 v233, v233, s2, v1
	v_med3_f32 v226, v226, s2, v1
	v_cvt_pk_fp8_f32 v210, v233, v226 op_sel:[0,0,1]
	s_waitcnt vmcnt(20)
	v_mul_f32_e32 v231, 0x43800000, v82
	v_mul_f32_e32 v232, 0x43800000, v86
	v_med3_f32 v231, v231, s2, v1
	v_med3_f32 v232, v232, s2, v1
	v_mul_f32_e32 v233, 0x43800000, v90
	v_mul_f32_e32 v226, 0x43800000, v94
	v_cvt_pk_fp8_f32 v211, v231, v232
	v_med3_f32 v233, v233, s2, v1
	v_med3_f32 v226, v226, s2, v1
	v_cvt_pk_fp8_f32 v211, v233, v226 op_sel:[0,0,1]
	s_waitcnt vmcnt(16)
	v_mul_f32_e32 v231, 0x43800000, v98
	v_mul_f32_e32 v232, 0x43800000, v102
	v_med3_f32 v231, v231, s2, v1
	v_med3_f32 v232, v232, s2, v1
	v_mul_f32_e32 v233, 0x43800000, v106
	v_mul_f32_e32 v226, 0x43800000, v110
	v_cvt_pk_fp8_f32 v212, v231, v232
	v_med3_f32 v233, v233, s2, v1
	v_med3_f32 v226, v226, s2, v1
	v_cvt_pk_fp8_f32 v212, v233, v226 op_sel:[0,0,1]
	s_waitcnt vmcnt(12)
	v_mul_f32_e32 v231, 0x43800000, v114
	v_mul_f32_e32 v232, 0x43800000, v118
	v_med3_f32 v231, v231, s2, v1
	v_med3_f32 v232, v232, s2, v1
	v_mul_f32_e32 v233, 0x43800000, v122
	v_mul_f32_e32 v226, 0x43800000, v126
	v_cvt_pk_fp8_f32 v213, v231, v232
	v_med3_f32 v233, v233, s2, v1
	v_med3_f32 v226, v226, s2, v1
	v_cvt_pk_fp8_f32 v213, v233, v226 op_sel:[0,0,1]
	s_nop 1
	ds_write_b128 v237, v[210:213] offset:34816
	v_mul_f32_e32 v231, 0x43800000, v67
	v_mul_f32_e32 v232, 0x43800000, v71
	v_med3_f32 v231, v231, s2, v1
	v_med3_f32 v232, v232, s2, v1
	v_mul_f32_e32 v233, 0x43800000, v75
	v_mul_f32_e32 v226, 0x43800000, v79
	v_cvt_pk_fp8_f32 v214, v231, v232
	v_med3_f32 v233, v233, s2, v1
	v_med3_f32 v226, v226, s2, v1
	v_cvt_pk_fp8_f32 v214, v233, v226 op_sel:[0,0,1]
	v_mul_f32_e32 v231, 0x43800000, v83
	v_mul_f32_e32 v232, 0x43800000, v87
	v_med3_f32 v231, v231, s2, v1
	v_med3_f32 v232, v232, s2, v1
	v_mul_f32_e32 v233, 0x43800000, v91
	v_mul_f32_e32 v226, 0x43800000, v95
	v_cvt_pk_fp8_f32 v215, v231, v232
	v_med3_f32 v233, v233, s2, v1
	v_med3_f32 v226, v226, s2, v1
	v_cvt_pk_fp8_f32 v215, v233, v226 op_sel:[0,0,1]
	v_mul_f32_e32 v231, 0x43800000, v99
	v_mul_f32_e32 v232, 0x43800000, v103
	v_med3_f32 v231, v231, s2, v1
	v_med3_f32 v232, v232, s2, v1
	v_mul_f32_e32 v233, 0x43800000, v107
	v_mul_f32_e32 v226, 0x43800000, v111
	v_cvt_pk_fp8_f32 v216, v231, v232
	v_med3_f32 v233, v233, s2, v1
	v_med3_f32 v226, v226, s2, v1
	v_cvt_pk_fp8_f32 v216, v233, v226 op_sel:[0,0,1]
	v_mul_f32_e32 v231, 0x43800000, v115
	v_mul_f32_e32 v232, 0x43800000, v119
	v_med3_f32 v231, v231, s2, v1
	v_med3_f32 v232, v232, s2, v1
	v_mul_f32_e32 v233, 0x43800000, v123
	v_mul_f32_e32 v226, 0x43800000, v127
	v_cvt_pk_fp8_f32 v217, v231, v232
	v_med3_f32 v233, v233, s2, v1
	v_med3_f32 v226, v226, s2, v1
	v_cvt_pk_fp8_f32 v217, v233, v226 op_sel:[0,0,1]
	s_nop 1
	ds_write_b128 v237, v[214:217] offset:35088
	v_mul_f32_e32 v231, 0x43800000, v68
	v_mul_f32_e32 v232, 0x43800000, v72
	v_med3_f32 v231, v231, s2, v1
	v_med3_f32 v232, v232, s2, v1
	v_mul_f32_e32 v233, 0x43800000, v76
	v_mul_f32_e32 v226, 0x43800000, v80
	v_cvt_pk_fp8_f32 v218, v231, v232
	v_med3_f32 v233, v233, s2, v1
	v_med3_f32 v226, v226, s2, v1
	v_cvt_pk_fp8_f32 v218, v233, v226 op_sel:[0,0,1]
	v_mul_f32_e32 v231, 0x43800000, v84
	v_mul_f32_e32 v232, 0x43800000, v88
	v_med3_f32 v231, v231, s2, v1
	v_med3_f32 v232, v232, s2, v1
	v_mul_f32_e32 v233, 0x43800000, v92
	v_mul_f32_e32 v226, 0x43800000, v96
	v_cvt_pk_fp8_f32 v219, v231, v232
	v_med3_f32 v233, v233, s2, v1
	v_med3_f32 v226, v226, s2, v1
	v_cvt_pk_fp8_f32 v219, v233, v226 op_sel:[0,0,1]
	v_mul_f32_e32 v231, 0x43800000, v100
	v_mul_f32_e32 v232, 0x43800000, v104
	v_med3_f32 v231, v231, s2, v1
	v_med3_f32 v232, v232, s2, v1
	v_mul_f32_e32 v233, 0x43800000, v108
	v_mul_f32_e32 v226, 0x43800000, v112
	v_cvt_pk_fp8_f32 v220, v231, v232
	v_med3_f32 v233, v233, s2, v1
	v_med3_f32 v226, v226, s2, v1
	v_cvt_pk_fp8_f32 v220, v233, v226 op_sel:[0,0,1]
	v_mul_f32_e32 v231, 0x43800000, v116
	v_mul_f32_e32 v232, 0x43800000, v120
	v_med3_f32 v231, v231, s2, v1
	v_med3_f32 v232, v232, s2, v1
	v_mul_f32_e32 v233, 0x43800000, v124
	v_mul_f32_e32 v226, 0x43800000, v128
	v_cvt_pk_fp8_f32 v221, v231, v232
	v_med3_f32 v233, v233, s2, v1
	v_med3_f32 v226, v226, s2, v1
	v_cvt_pk_fp8_f32 v221, v233, v226 op_sel:[0,0,1]
	s_nop 1
	ds_write_b128 v237, v[218:221] offset:35360
	v_mul_f32_e32 v231, 0x43800000, v69
	v_mul_f32_e32 v232, 0x43800000, v73
	v_med3_f32 v231, v231, s2, v1
	v_med3_f32 v232, v232, s2, v1
	v_mul_f32_e32 v233, 0x43800000, v77
	v_mul_f32_e32 v226, 0x43800000, v81
	v_cvt_pk_fp8_f32 v222, v231, v232
	v_med3_f32 v233, v233, s2, v1
	v_med3_f32 v226, v226, s2, v1
	v_cvt_pk_fp8_f32 v222, v233, v226 op_sel:[0,0,1]
	v_mul_f32_e32 v231, 0x43800000, v85
	v_mul_f32_e32 v232, 0x43800000, v89
	v_med3_f32 v231, v231, s2, v1
	v_med3_f32 v232, v232, s2, v1
	v_mul_f32_e32 v233, 0x43800000, v93
	v_mul_f32_e32 v226, 0x43800000, v97
	v_cvt_pk_fp8_f32 v223, v231, v232
	v_med3_f32 v233, v233, s2, v1
	v_med3_f32 v226, v226, s2, v1
	v_cvt_pk_fp8_f32 v223, v233, v226 op_sel:[0,0,1]
	v_mul_f32_e32 v231, 0x43800000, v101
	v_mul_f32_e32 v232, 0x43800000, v105
	v_med3_f32 v231, v231, s2, v1
	v_med3_f32 v232, v232, s2, v1
	v_mul_f32_e32 v233, 0x43800000, v109
	v_mul_f32_e32 v226, 0x43800000, v113
	v_cvt_pk_fp8_f32 v224, v231, v232
	v_med3_f32 v233, v233, s2, v1
	v_med3_f32 v226, v226, s2, v1
	v_cvt_pk_fp8_f32 v224, v233, v226 op_sel:[0,0,1]
	v_mul_f32_e32 v231, 0x43800000, v117
	v_mul_f32_e32 v232, 0x43800000, v121
	v_med3_f32 v231, v231, s2, v1
	v_med3_f32 v232, v232, s2, v1
	v_mul_f32_e32 v233, 0x43800000, v125
	v_mul_f32_e32 v226, 0x43800000, v129
	v_cvt_pk_fp8_f32 v225, v231, v232
	v_med3_f32 v233, v233, s2, v1
	v_med3_f32 v226, v226, s2, v1
	v_cvt_pk_fp8_f32 v225, v233, v226 op_sel:[0,0,1]
	s_nop 1
	ds_write_b128 v237, v[222:225] offset:35632
	s_waitcnt lgkmcnt(0)
	s_barrier
	ds_read_b128 v[210:213], v230 offset:34816
	ds_read_b128 v[214:217], v230 offset:43520
	ds_read_b128 v[218:221], v230 offset:52224
	ds_read_b128 v[222:225], v230 offset:60928
	s_waitcnt lgkmcnt(3)
	global_store_dwordx4 v241, v[210:213], s[10:11] nt
	s_waitcnt lgkmcnt(2)
	global_store_dwordx4 v234, v[214:217], s[10:11] nt
	s_waitcnt lgkmcnt(1)
	global_store_dwordx4 v235, v[218:221], s[10:11] nt
	s_waitcnt lgkmcnt(0)
	global_store_dwordx4 v236, v[222:225], s[10:11] nt
	s_add_u32 s10, s10, 0x100
	s_addc_u32 s11, s11, 0
	s_mov_b64 s[10:11], 0
	s_mov_b32 s2, s0
	s_barrier
